# DPP reductions, batched loads in mixout/EpiResid/EpiDown/gla_c epilogues, conversion split 31pct in gemm_in slack
# speedup vs baseline: 1.0199x; 1.0199x over previous
.LBB0_86:
	global_load_dwordx4 v[18:21], v13, s[10:11]
	s_lshl_b64 s[12:13], s[12:13], 11
	v_lshl_add_u64 v[34:35], v[2:3], 0, s[12:13]
	s_ashr_i32 s2, s0, 31
	s_lshr_b32 s2, s2, 20
	s_add_i32 s2, s0, s2
	s_ashr_i32 s2, s2, 12
	s_and_b64 s[8:9], exec, s[8:9]
	s_cselect_b32 s2, s2, 4
	s_mul_hi_i32 s9, s2, 0x6000
	s_mulk_i32 s2, 0x6000
	s_add_u32 s8, s14, s2
	s_addc_u32 s9, s15, s9
	s_waitcnt vmcnt(0)
	v_cvt_pk_bf16_f32 v22, v18, v19
	v_cvt_pk_bf16_f32 v23, v20, v21
	global_store_dwordx2 v[34:35], v[22:23], off
	global_load_dwordx4 v[22:25], v13, s[10:11] offset:1024
	v_pk_mul_f32 v[46:47], v[20:21], v[20:21]
	v_pk_mul_f32 v[48:49], v[18:19], v[18:19]
	s_waitcnt vmcnt(0)
	v_cvt_pk_bf16_f32 v26, v22, v23
	v_cvt_pk_bf16_f32 v27, v24, v25
	global_store_dwordx2 v[34:35], v[26:27], off offset:512
	global_load_dwordx4 v[26:29], v13, s[10:11] offset:2048
	v_pk_mov_b32 v[50:51], v[48:49], v[46:47] op_sel:[1,0]
	v_mov_b32_e32 v49, v47
	v_pk_add_f32 v[46:47], v[50:51], v[48:49]
	v_pk_mul_f32 v[48:49], v[24:25], v[24:25]
	v_pk_mul_f32 v[50:51], v[22:23], v[22:23]
	v_pk_add_f32 v[46:47], v[46:47], v[46:47] op_sel:[0,1] op_sel_hi:[1,0]
	v_pk_mov_b32 v[52:53], v[50:51], v[48:49] op_sel:[1,0]
	v_mov_b32_e32 v51, v49
	v_pk_add_f32 v[48:49], v[52:53], v[50:51]
	s_waitcnt vmcnt(0)
	v_cvt_pk_bf16_f32 v30, v26, v27
	v_cvt_pk_bf16_f32 v31, v28, v29
	global_store_dwordx2 v[34:35], v[30:31], off offset:1024
	global_load_dwordx4 v[30:33], v13, s[10:11] offset:3072
	s_add_u32 s10, s8, 0x1000
	s_addc_u32 s11, s9, 0
	v_mul_f32_e32 v50, v27, v27
	v_mul_f32_e32 v52, v29, v29
	v_pk_add_f32 v[48:49], v[48:49], v[48:49] op_sel:[0,1] op_sel_hi:[1,0]
	v_pk_fma_f32 v[50:51], v[26:27], v[26:27], v[50:51] op_sel_hi:[1,1,0]
	v_pk_fma_f32 v[52:53], v[28:29], v[28:29], v[52:53] op_sel_hi:[1,1,0]
	s_add_u32 s0, s0, s28
	s_addc_u32 s1, s1, s29
	s_add_u32 s4, s4, s6
	s_addc_u32 s5, s5, s7
	s_cmpk_lt_i32 s0, 0x4400
	s_waitcnt vmcnt(0)
	v_cvt_pk_bf16_f32 v36, v30, v31
	v_cvt_pk_bf16_f32 v37, v32, v33
	global_store_dwordx2 v[34:35], v[36:37], off offset:1536
	global_load_dwordx4 v[34:37], v[4:5], off
	s_nop 0
	global_load_dwordx4 v[38:41], v13, s[10:11]
	global_load_dwordx4 v[42:45], v13, s[8:9]
	v_mul_f32_e32 v47, v30, v30
	v_mul_f32_e32 v49, v31, v31
	v_mul_f32_e32 v51, v32, v32
	v_mul_f32_e32 v53, v33, v33
	v_pk_add_f32 v[46:47], v[46:47], v[48:49]
	v_pk_add_f32 v[48:49], v[50:51], v[52:53]
	s_nop 0
	v_pk_add_f32 v[46:47], v[46:47], v[48:49]
	v_lshl_add_u64 v[48:49], v[6:7], 0, s[12:13]
	v_add_f32_e32 v46, v46, v47
	s_nop 1
	v_mov_b32_dpp v47, v46 quad_perm:[1,0,3,2] row_mask:0xf bank_mask:0xf
	s_waitcnt lgkmcnt(0)
	v_add_f32_e32 v46, v46, v47
	s_nop 1
	v_mov_b32_dpp v47, v46 quad_perm:[2,3,0,1] row_mask:0xf bank_mask:0xf
	s_waitcnt lgkmcnt(0)
	v_add_f32_e32 v46, v46, v47
	s_nop 1
	v_mov_b32_dpp v47, v46 row_half_mirror row_mask:0xf bank_mask:0xf
	s_waitcnt lgkmcnt(0)
	v_add_f32_e32 v46, v46, v47
	s_nop 1
	v_mov_b32_dpp v47, v46 row_mirror row_mask:0xf bank_mask:0xf
	s_waitcnt lgkmcnt(0)
	v_add_f32_e32 v46, v46, v47
	v_mov_b32_e32 v47, v46
	s_nop 1
	v_permlane16_swap_b32_e32 v47, v46
	s_waitcnt lgkmcnt(0)
	v_add_f32_e32 v46, v46, v47
	ds_bpermute_b32 v47, v12, v46
	s_waitcnt lgkmcnt(0)
	v_add_f32_e32 v46, v46, v47
	v_fmamk_f32 v46, v46, 0x3a800000, v14
	v_rsq_f32_e32 v46, v46
	s_nop 0
	v_pk_mul_f32 v[20:21], v[20:21], v[46:47] op_sel_hi:[1,0]
	v_pk_mul_f32 v[18:19], v[18:19], v[46:47] op_sel_hi:[1,0]
	v_pk_mul_f32 v[24:25], v[24:25], v[46:47] op_sel_hi:[1,0]
	v_pk_mul_f32 v[22:23], v[22:23], v[46:47] op_sel_hi:[1,0]
	v_pk_mul_f32 v[28:29], v[28:29], v[46:47] op_sel_hi:[1,0]
	v_pk_mul_f32 v[26:27], v[26:27], v[46:47] op_sel_hi:[1,0]
	v_pk_mul_f32 v[32:33], v[32:33], v[46:47] op_sel_hi:[1,0]
	v_pk_mul_f32 v[30:31], v[30:31], v[46:47] op_sel_hi:[1,0]
	s_waitcnt vmcnt(2)
	v_pk_mul_f32 v[18:19], v[34:35], v[18:19]
	v_pk_mul_f32 v[20:21], v[36:37], v[20:21]
	s_waitcnt vmcnt(1)
	v_pk_add_f32 v[34:35], v[40:41], 1.0 op_sel_hi:[1,0]
	v_pk_add_f32 v[36:37], v[38:39], 1.0 op_sel_hi:[1,0]
	s_waitcnt vmcnt(0)
	v_pk_fma_f32 v[20:21], v[34:35], v[20:21], v[44:45]
	v_pk_fma_f32 v[18:19], v[36:37], v[18:19], v[42:43]
	s_nop 0
	v_cvt_pk_bf16_f32 v18, v18, v19
	v_cvt_pk_bf16_f32 v19, v20, v21
	global_store_dwordx2 v[48:49], v[18:19], off
	global_load_dwordx4 v[18:21], v[4:5], off offset:1024
	s_nop 0
	global_load_dwordx4 v[34:37], v15, s[10:11]
	global_load_dwordx4 v[38:41], v13, s[8:9] offset:1024
	s_waitcnt vmcnt(2)
	v_pk_mul_f32 v[18:19], v[18:19], v[22:23]
	v_pk_mul_f32 v[20:21], v[20:21], v[24:25]
	s_waitcnt vmcnt(1)
	v_pk_add_f32 v[22:23], v[36:37], 1.0 op_sel_hi:[1,0]
	v_pk_add_f32 v[24:25], v[34:35], 1.0 op_sel_hi:[1,0]
	s_waitcnt vmcnt(0)
	v_pk_fma_f32 v[20:21], v[22:23], v[20:21], v[40:41]
	v_pk_fma_f32 v[18:19], v[24:25], v[18:19], v[38:39]
	s_nop 0
	v_cvt_pk_bf16_f32 v18, v18, v19
	v_cvt_pk_bf16_f32 v19, v20, v21
	global_store_dwordx2 v[48:49], v[18:19], off offset:512
	global_load_dwordx4 v[18:21], v[4:5], off offset:2048
	s_nop 0
	global_load_dwordx4 v[22:25], v16, s[10:11]
	global_load_dwordx4 v[34:37], v13, s[8:9] offset:2048
	s_waitcnt vmcnt(2)
	v_pk_mul_f32 v[18:19], v[18:19], v[26:27]
	v_pk_mul_f32 v[20:21], v[20:21], v[28:29]
	s_waitcnt vmcnt(1)
	v_pk_add_f32 v[24:25], v[24:25], 1.0 op_sel_hi:[1,0]
	v_pk_add_f32 v[22:23], v[22:23], 1.0 op_sel_hi:[1,0]
	s_waitcnt vmcnt(0)
	v_pk_fma_f32 v[20:21], v[20:21], v[24:25], v[36:37]
	v_pk_fma_f32 v[18:19], v[18:19], v[22:23], v[34:35]
	s_nop 0
	v_cvt_pk_bf16_f32 v18, v18, v19
	v_cvt_pk_bf16_f32 v19, v20, v21
	global_store_dwordx2 v[48:49], v[18:19], off offset:1024
	global_load_dwordx4 v[18:21], v[4:5], off offset:3072
	s_nop 0
	global_load_dwordx4 v[22:25], v17, s[10:11]
	global_load_dwordx4 v[26:29], v13, s[8:9] offset:3072
	s_waitcnt vmcnt(2)
	v_pk_mul_f32 v[18:19], v[30:31], v[18:19]
	v_pk_mul_f32 v[20:21], v[32:33], v[20:21]
	s_waitcnt vmcnt(1)
	v_pk_add_f32 v[24:25], v[24:25], 1.0 op_sel_hi:[1,0]
	v_pk_add_f32 v[22:23], v[22:23], 1.0 op_sel_hi:[1,0]
	s_waitcnt vmcnt(0)
	v_pk_fma_f32 v[20:21], v[20:21], v[24:25], v[28:29]
	v_pk_fma_f32 v[18:19], v[18:19], v[22:23], v[26:27]
	s_nop 0
	v_cvt_pk_bf16_f32 v18, v18, v19
	v_cvt_pk_bf16_f32 v19, v20, v21
	global_store_dwordx2 v[48:49], v[18:19], off offset:1536
	s_cbranch_scc0 .LBB0_89

.LBB0_163:
	v_readlane_b32 s0, v254, 30
	v_readlane_b32 s1, v254, 31
	s_and_b64 vcc, exec, s[0:1]
	s_cbranch_vccz .LBB0_183
	v_readlane_b32 s0, v254, 32
	s_add_i32 s27, s0, s26
	s_cmpk_gt_i32 s27, 0x3bff
	s_cbranch_scc1 .LBB0_183
	s_mul_hi_i32 s0, s27, 0x2aaaaaab
	s_lshr_b32 s1, s0, 31
	s_ashr_i32 s0, s0, 8
	s_add_i32 s0, s0, s1
	s_mul_i32 s1, s0, 0x600
	s_sub_i32 s3, s27, s1
	s_cmpk_gt_i32 s3, 0x3ff
	s_mov_b64 s[10:11], -1
	s_cbranch_scc0 .LBB0_167
	v_readlane_b32 s8, v255, 37
	s_ashr_i32 s1, s0, 31
	v_readlane_b32 s9, v255, 38
	v_readlane_b32 s36, v252, 48
	s_lshl_b64 s[6:7], s[8:9], 27
	s_lshl_b64 s[4:5], s[0:1], 22
	v_readlane_b32 s40, v252, 52
	v_readlane_b32 s41, v252, 53
	s_add_u32 s1, s40, s4
	s_addc_u32 s2, s41, s5
	s_add_u32 s4, s1, s6
	s_addc_u32 s5, s2, s7
	s_lshl_b32 s1, s3, 1
	s_and_b32 s1, s1, 0x7fffffc0
	s_lshl_b32 s2, s3, 5
	v_readlane_b32 s37, v252, 49
	v_readlane_b32 s38, v252, 50
	v_readlane_b32 s39, v252, 51
	v_readlane_b32 s42, v252, 54
	v_readlane_b32 s43, v252, 55
	s_addk_i32 s1, 0xf800
	s_and_b32 s2, s2, 0x3e0
	s_lshl_b64 s[8:9], s[8:9], 28
	s_mov_b64 s[10:11], 0

.LBB0_175:
	s_add_i32 s27, s27, s49
	s_cmpk_lt_i32 s27, 0x3c00
	s_cselect_b64 s[8:9], -1, 0
	s_cmpk_gt_i32 s27, 0x3bff
	s_cbranch_scc1 .LBB0_181
	s_mul_hi_i32 s0, s27, 0x2aaaaaab
	s_lshr_b32 s1, s0, 31
	s_ashr_i32 s0, s0, 8
	s_add_i32 s0, s0, s1
	s_mul_i32 s1, s0, 0xfffffa00
	s_add_i32 s19, s27, s1
	s_cmpk_gt_i32 s19, 0x3ff
	s_mov_b64 s[24:25], -1
	s_cbranch_scc0 .LBB0_178
	s_ashr_i32 s1, s0, 31
	s_lshl_b64 s[22:23], s[0:1], 22
	s_add_u32 s22, s26, s22
	s_addc_u32 s23, s28, s23
	s_mul_i32 s1, s0, 0xfffff400
	s_add_i32 s18, s36, s35
	s_add_i32 s18, s18, s1
	s_and_b32 s1, s18, 0x7fffffc0
	s_add_i32 s18, s34, s31
	s_addk_i32 s1, 0xf800
	s_and_b32 s18, s18, 0x3e0
	s_mov_b64 s[24:25], 0

.LBB0_249:
	v_add_u32_e32 v171, 0, v162
	v_add_u32_e32 v2, 0x12000, v171
	ds_read2st64_b32 v[118:119], v171 offset0:32 offset1:36
	ds_read2st64_b32 v[114:115], v171 offset0:160 offset1:164
	ds_read_b32 v34, v2
	v_add_u32_e32 v2, 0x12400, v171
	ds_read_b32 v108, v2
	ds_read2st64_b32 v[120:121], v171 offset0:40 offset1:44
	ds_read2st64_b32 v[116:117], v171 offset0:168 offset1:172
	v_add_u32_e32 v2, 0x12800, v171
	ds_read_b32 v110, v2
	v_add_u32_e32 v2, 0x12c00, v171
	v_add_u32_e32 v170, 0, v163
	ds_read_b32 v112, v2
	ds_read_b128 v[122:125], v170 offset:256
	ds_read_b128 v[126:129], v170
	ds_read_b128 v[2:5], v170 offset:16
	ds_read_b128 v[130:133], v170 offset:128
	ds_read_b128 v[172:175], v170 offset:768
	ds_read_b128 v[176:179], v170 offset:512
	ds_read_b128 v[180:183], v170 offset:640
	s_waitcnt lgkmcnt(0)
	v_mov_b32_e32 v184, v122
	v_mov_b32_e32 v134, v119
	v_mov_b32_e32 v185, v172
	v_pk_fma_f32 v[102:103], v[118:119], v[184:185], v[102:103] op_sel_hi:[0,1,1]
	v_mov_b32_e32 v172, v123
	v_pk_fma_f32 v[102:103], v[134:135], v[172:173], v[102:103] op_sel_hi:[0,1,1]
	v_mov_b32_e32 v122, v124
	v_mov_b32_e32 v123, v174
	v_pk_fma_f32 v[102:103], v[120:121], v[122:123], v[102:103] op_sel_hi:[0,1,1]
	v_mov_b32_e32 v122, v176
	v_mov_b32_e32 v123, v126
	v_pk_fma_f32 v[106:107], v[114:115], v[122:123], v[106:107] op_sel_hi:[0,1,1]
	v_mov_b32_e32 v138, v115
	v_mov_b32_e32 v126, v177
	v_pk_fma_f32 v[106:107], v[138:139], v[126:127], v[106:107] op_sel_hi:[0,1,1]
	v_mov_b32_e32 v122, v178
	v_mov_b32_e32 v123, v128
	v_pk_fma_f32 v[106:107], v[116:117], v[122:123], v[106:107] op_sel_hi:[0,1,1]
	v_mov_b32_e32 v122, v180
	v_mov_b32_e32 v123, v130
	v_pk_fma_f32 v[104:105], v[34:35], v[122:123], v[104:105] op_sel_hi:[0,1,1]
	v_mov_b32_e32 v130, v181
	v_pk_fma_f32 v[104:105], v[108:109], v[130:131], v[104:105] op_sel_hi:[0,1,1]
	v_mov_b32_e32 v122, v182
	v_mov_b32_e32 v123, v132
	v_mov_b32_e32 v136, v121
	v_mov_b32_e32 v174, v125
	v_mov_b32_e32 v140, v117
	v_mov_b32_e32 v128, v179
	v_pk_fma_f32 v[104:105], v[110:111], v[122:123], v[104:105] op_sel_hi:[0,1,1]
	v_mov_b32_e32 v132, v183
	v_pk_fma_f32 v[102:103], v[136:137], v[174:175], v[102:103] op_sel_hi:[0,1,1]
	v_pk_fma_f32 v[106:107], v[140:141], v[128:129], v[106:107] op_sel_hi:[0,1,1]
	v_pk_fma_f32 v[104:105], v[112:113], v[132:133], v[104:105] op_sel_hi:[0,1,1]
	ds_read_b128 v[122:125], v170 offset:1280
	ds_read_b128 v[126:129], v170 offset:1024
	ds_read_b128 v[130:133], v170 offset:1152
	ds_read_b128 v[172:175], v170 offset:1792
	ds_read_b128 v[176:179], v170 offset:1536
	ds_read_b128 v[180:183], v170 offset:1664
	s_waitcnt lgkmcnt(5)
	v_mov_b32_e32 v184, v122
	v_mov_b32_e32 v122, v124
	s_waitcnt lgkmcnt(2)
	v_mov_b32_e32 v185, v172
	v_pk_fma_f32 v[16:17], v[118:119], v[184:185], v[16:17] op_sel_hi:[0,1,1]
	v_mov_b32_e32 v172, v123
	v_pk_fma_f32 v[16:17], v[134:135], v[172:173], v[16:17] op_sel_hi:[0,1,1]
	v_mov_b32_e32 v123, v174
	v_pk_fma_f32 v[16:17], v[120:121], v[122:123], v[16:17] op_sel_hi:[0,1,1]
	v_mov_b32_e32 v174, v125
	v_pk_fma_f32 v[122:123], v[136:137], v[174:175], v[16:17] op_sel_hi:[0,1,1]
	s_waitcnt lgkmcnt(1)
	v_mov_b32_e32 v16, v176
	v_mov_b32_e32 v17, v126
	v_pk_fma_f32 v[12:13], v[114:115], v[16:17], v[12:13] op_sel_hi:[0,1,1]
	v_mov_b32_e32 v126, v177
	v_pk_fma_f32 v[12:13], v[138:139], v[126:127], v[12:13] op_sel_hi:[0,1,1]
	v_mov_b32_e32 v16, v178
	v_mov_b32_e32 v17, v128
	v_pk_fma_f32 v[12:13], v[116:117], v[16:17], v[12:13] op_sel_hi:[0,1,1]
	v_mov_b32_e32 v128, v179
	v_pk_fma_f32 v[124:125], v[140:141], v[128:129], v[12:13] op_sel_hi:[0,1,1]
	s_waitcnt lgkmcnt(0)
	v_mov_b32_e32 v12, v180
	v_mov_b32_e32 v13, v130
	v_pk_fma_f32 v[12:13], v[34:35], v[12:13], v[14:15] op_sel_hi:[0,1,1]
	v_mov_b32_e32 v130, v181
	v_pk_fma_f32 v[12:13], v[108:109], v[130:131], v[12:13] op_sel_hi:[0,1,1]
	v_mov_b32_e32 v14, v182
	v_mov_b32_e32 v15, v132
	v_pk_fma_f32 v[12:13], v[110:111], v[14:15], v[12:13] op_sel_hi:[0,1,1]
	v_mov_b32_e32 v132, v183
	v_pk_fma_f32 v[126:127], v[112:113], v[132:133], v[12:13] op_sel_hi:[0,1,1]
	ds_read_b128 v[12:15], v170 offset:2304
	ds_read_b128 v[130:133], v170 offset:2048
	ds_read_b128 v[172:175], v170 offset:2176
	ds_read_b128 v[176:179], v170 offset:2816
	ds_read_b128 v[180:183], v170 offset:2560
	ds_read_b128 v[184:187], v170 offset:2688
	s_waitcnt lgkmcnt(5)
	v_mov_b32_e32 v16, v12
	v_mov_b32_e32 v12, v14
	s_waitcnt lgkmcnt(2)
	v_mov_b32_e32 v17, v176
	v_pk_fma_f32 v[10:11], v[118:119], v[16:17], v[10:11] op_sel_hi:[0,1,1]
	v_mov_b32_e32 v176, v13
	v_pk_fma_f32 v[10:11], v[134:135], v[176:177], v[10:11] op_sel_hi:[0,1,1]
	v_mov_b32_e32 v13, v178
	v_pk_fma_f32 v[10:11], v[120:121], v[12:13], v[10:11] op_sel_hi:[0,1,1]
	v_mov_b32_e32 v178, v15
	v_pk_fma_f32 v[128:129], v[136:137], v[178:179], v[10:11] op_sel_hi:[0,1,1]
	v_mov_b32_e32 v10, v130
	s_waitcnt lgkmcnt(1)
	v_mov_b32_e32 v11, v180
	v_pk_fma_f32 v[8:9], v[114:115], v[10:11], v[8:9] op_sel_hi:[0,1,1]
	v_mov_b32_e32 v180, v131
	v_pk_fma_f32 v[8:9], v[138:139], v[180:181], v[8:9] op_sel_hi:[0,1,1]
	v_mov_b32_e32 v10, v132
	v_mov_b32_e32 v11, v182
	v_pk_fma_f32 v[8:9], v[116:117], v[10:11], v[8:9] op_sel_hi:[0,1,1]
	v_mov_b32_e32 v182, v133
	v_pk_fma_f32 v[130:131], v[140:141], v[182:183], v[8:9] op_sel_hi:[0,1,1]
	s_waitcnt lgkmcnt(0)
	v_mov_b32_e32 v8, v184
	v_mov_b32_e32 v9, v172
	v_pk_fma_f32 v[6:7], v[34:35], v[8:9], v[6:7] op_sel_hi:[0,1,1]
	v_mov_b32_e32 v172, v185
	v_pk_fma_f32 v[6:7], v[108:109], v[172:173], v[6:7] op_sel_hi:[0,1,1]
	v_mov_b32_e32 v8, v186
	v_mov_b32_e32 v9, v174
	v_pk_fma_f32 v[6:7], v[110:111], v[8:9], v[6:7] op_sel_hi:[0,1,1]
	v_mov_b32_e32 v174, v187
	v_pk_fma_f32 v[132:133], v[112:113], v[174:175], v[6:7] op_sel_hi:[0,1,1]
	ds_read_b128 v[14:17], v170 offset:3328
	ds_read_b128 v[10:13], v170 offset:3072
	ds_read_b128 v[6:9], v170 offset:3200
	v_add_u32_e32 v190, 0, v169
	ds_read_b128 v[172:175], v190 offset:256
	ds_read_b128 v[176:179], v190
	ds_read_b128 v[180:183], v190 offset:16
	ds_read_b128 v[184:187], v190 offset:128
	s_waitcnt lgkmcnt(6)
	v_mov_b32_e32 v188, v14
	s_waitcnt lgkmcnt(3)
	v_mov_b32_e32 v189, v172
	v_pk_fma_f32 v[96:97], v[118:119], v[188:189], v[96:97] op_sel_hi:[0,1,1]
	v_mov_b32_e32 v172, v15
	v_pk_fma_f32 v[14:15], v[134:135], v[172:173], v[96:97] op_sel_hi:[0,1,1]
	v_mov_b32_e32 v96, v16
	v_mov_b32_e32 v97, v174
	v_pk_fma_f32 v[14:15], v[120:121], v[96:97], v[14:15] op_sel_hi:[0,1,1]
	v_mov_b32_e32 v174, v17
	v_pk_fma_f32 v[172:173], v[136:137], v[174:175], v[14:15] op_sel_hi:[0,1,1]
	v_mov_b32_e32 v14, v10
	s_waitcnt lgkmcnt(2)
	v_mov_b32_e32 v15, v176
	v_pk_fma_f32 v[14:15], v[114:115], v[14:15], v[94:95] op_sel_hi:[0,1,1]
	v_mov_b32_e32 v176, v11
	v_pk_fma_f32 v[10:11], v[138:139], v[176:177], v[14:15] op_sel_hi:[0,1,1]
	v_mov_b32_e32 v14, v12
	v_mov_b32_e32 v15, v178
	v_pk_fma_f32 v[10:11], v[116:117], v[14:15], v[10:11] op_sel_hi:[0,1,1]
	v_mov_b32_e32 v178, v13
	v_pk_fma_f32 v[174:175], v[140:141], v[178:179], v[10:11] op_sel_hi:[0,1,1]
	s_waitcnt lgkmcnt(0)
	v_mov_b32_e32 v10, v184
	v_mov_b32_e32 v11, v6
	v_pk_fma_f32 v[10:11], v[34:35], v[10:11], v[90:91] op_sel_hi:[0,1,1]
	v_mov_b32_e32 v6, v185
	v_pk_fma_f32 v[6:7], v[108:109], v[6:7], v[10:11] op_sel_hi:[0,1,1]
	v_mov_b32_e32 v10, v186
	v_mov_b32_e32 v11, v8
	v_pk_fma_f32 v[6:7], v[110:111], v[10:11], v[6:7] op_sel_hi:[0,1,1]
	v_mov_b32_e32 v8, v187
	v_pk_fma_f32 v[90:91], v[112:113], v[8:9], v[6:7] op_sel_hi:[0,1,1]
	v_add_u32_e32 v6, 0x13000, v171
	ds_read2st64_b32 v[176:177], v171 offset0:48 offset1:52
	ds_read2st64_b32 v[178:179], v171 offset0:176 offset1:180
	ds_read_b32 v34, v6
	v_add_u32_e32 v6, 0x13400, v171
	ds_read_b32 v108, v6
	ds_read2st64_b32 v[184:185], v171 offset0:56 offset1:60
	ds_read2st64_b32 v[186:187], v171 offset0:184 offset1:188
	v_add_u32_e32 v6, 0x13800, v171
	ds_read_b32 v110, v6
	v_add_u32_e32 v6, 0x13c00, v171
	ds_read_b32 v112, v6
	ds_read_b128 v[6:9], v170 offset:272
	ds_read_b128 v[10:13], v170 offset:144
	ds_read_b128 v[14:17], v170 offset:784
	ds_read_b128 v[94:97], v170 offset:528
	ds_read_b128 v[114:117], v170 offset:656
	s_waitcnt lgkmcnt(4)
	v_mov_b32_e32 v118, v6
	v_mov_b32_e32 v134, v177
	s_waitcnt lgkmcnt(2)
	v_mov_b32_e32 v119, v14
	v_pk_fma_f32 v[102:103], v[176:177], v[118:119], v[102:103] op_sel_hi:[0,1,1]
	v_mov_b32_e32 v14, v7
	v_pk_fma_f32 v[6:7], v[134:135], v[14:15], v[102:103] op_sel_hi:[0,1,1]
	v_mov_b32_e32 v14, v8
	v_mov_b32_e32 v15, v16
	v_pk_fma_f32 v[6:7], v[184:185], v[14:15], v[6:7] op_sel_hi:[0,1,1]
	v_mov_b32_e32 v136, v185
	v_mov_b32_e32 v16, v9
	v_pk_fma_f32 v[102:103], v[136:137], v[16:17], v[6:7] op_sel_hi:[0,1,1]
	s_waitcnt lgkmcnt(1)
	v_mov_b32_e32 v6, v94
	v_mov_b32_e32 v7, v2
	v_pk_fma_f32 v[6:7], v[178:179], v[6:7], v[106:107] op_sel_hi:[0,1,1]
	v_mov_b32_e32 v138, v179
	v_mov_b32_e32 v2, v95
	v_pk_fma_f32 v[2:3], v[138:139], v[2:3], v[6:7] op_sel_hi:[0,1,1]
	v_mov_b32_e32 v6, v96
	v_mov_b32_e32 v7, v4
	v_pk_fma_f32 v[2:3], v[186:187], v[6:7], v[2:3] op_sel_hi:[0,1,1]
	v_mov_b32_e32 v140, v187
	v_mov_b32_e32 v4, v97
	v_pk_fma_f32 v[106:107], v[140:141], v[4:5], v[2:3] op_sel_hi:[0,1,1]
	s_waitcnt lgkmcnt(0)
	v_mov_b32_e32 v2, v114
	v_mov_b32_e32 v3, v10
	v_pk_fma_f32 v[2:3], v[34:35], v[2:3], v[104:105] op_sel_hi:[0,1,1]
	v_mov_b32_e32 v10, v115
	v_pk_fma_f32 v[2:3], v[108:109], v[10:11], v[2:3] op_sel_hi:[0,1,1]
	v_mov_b32_e32 v4, v116
	v_mov_b32_e32 v5, v12
	v_pk_fma_f32 v[2:3], v[110:111], v[4:5], v[2:3] op_sel_hi:[0,1,1]
	v_mov_b32_e32 v12, v117
	v_pk_fma_f32 v[104:105], v[112:113], v[12:13], v[2:3] op_sel_hi:[0,1,1]
	ds_read_b128 v[2:5], v170 offset:1296
	ds_read_b128 v[6:9], v170 offset:1040
	ds_read_b128 v[94:97], v170 offset:1168
	ds_read_b128 v[10:13], v170 offset:1808
	ds_read_b128 v[114:117], v170 offset:1552
	ds_read_b128 v[118:121], v170 offset:1680
	s_waitcnt lgkmcnt(5)
	v_mov_b32_e32 v14, v2
	s_add_i32 s2, s2, -2
	s_waitcnt lgkmcnt(2)
	v_mov_b32_e32 v15, v10
	v_pk_fma_f32 v[14:15], v[176:177], v[14:15], v[122:123] op_sel_hi:[0,1,1]
	v_mov_b32_e32 v10, v3
	v_pk_fma_f32 v[2:3], v[134:135], v[10:11], v[14:15] op_sel_hi:[0,1,1]
	v_mov_b32_e32 v10, v4
	v_mov_b32_e32 v11, v12
	v_pk_fma_f32 v[2:3], v[184:185], v[10:11], v[2:3] op_sel_hi:[0,1,1]
	v_mov_b32_e32 v12, v5
	v_pk_fma_f32 v[16:17], v[136:137], v[12:13], v[2:3] op_sel_hi:[0,1,1]
	s_waitcnt lgkmcnt(1)
	v_mov_b32_e32 v2, v114
	v_mov_b32_e32 v3, v6
	v_pk_fma_f32 v[2:3], v[178:179], v[2:3], v[124:125] op_sel_hi:[0,1,1]
	v_mov_b32_e32 v6, v115
	v_pk_fma_f32 v[2:3], v[138:139], v[6:7], v[2:3] op_sel_hi:[0,1,1]
	v_mov_b32_e32 v4, v116
	v_mov_b32_e32 v5, v8
	v_pk_fma_f32 v[2:3], v[186:187], v[4:5], v[2:3] op_sel_hi:[0,1,1]
	v_mov_b32_e32 v8, v117
	v_pk_fma_f32 v[12:13], v[140:141], v[8:9], v[2:3] op_sel_hi:[0,1,1]
	s_waitcnt lgkmcnt(0)
	v_mov_b32_e32 v2, v118
	v_mov_b32_e32 v3, v94
	v_pk_fma_f32 v[2:3], v[34:35], v[2:3], v[126:127] op_sel_hi:[0,1,1]
	v_mov_b32_e32 v94, v119
	v_pk_fma_f32 v[2:3], v[108:109], v[94:95], v[2:3] op_sel_hi:[0,1,1]
	v_mov_b32_e32 v4, v120
	v_mov_b32_e32 v5, v96
	v_pk_fma_f32 v[2:3], v[110:111], v[4:5], v[2:3] op_sel_hi:[0,1,1]
	v_mov_b32_e32 v96, v121
	v_pk_fma_f32 v[14:15], v[112:113], v[96:97], v[2:3] op_sel_hi:[0,1,1]
	ds_read_b128 v[2:5], v170 offset:2320
	ds_read_b128 v[6:9], v170 offset:2064
	ds_read_b128 v[94:97], v170 offset:2192
	ds_read_b128 v[114:117], v170 offset:2832
	ds_read_b128 v[118:121], v170 offset:2576
	ds_read_b128 v[122:125], v170 offset:2704
	s_waitcnt lgkmcnt(5)
	v_mov_b32_e32 v10, v2
	v_add_u32_e32 v169, 32, v169
	s_waitcnt lgkmcnt(2)
	v_mov_b32_e32 v11, v114
	v_pk_fma_f32 v[10:11], v[176:177], v[10:11], v[128:129] op_sel_hi:[0,1,1]
	v_mov_b32_e32 v114, v3
	v_pk_fma_f32 v[2:3], v[134:135], v[114:115], v[10:11] op_sel_hi:[0,1,1]
	v_mov_b32_e32 v10, v4
	v_mov_b32_e32 v11, v116
	v_pk_fma_f32 v[2:3], v[184:185], v[10:11], v[2:3] op_sel_hi:[0,1,1]
	v_mov_b32_e32 v116, v5
	v_pk_fma_f32 v[10:11], v[136:137], v[116:117], v[2:3] op_sel_hi:[0,1,1]
	v_mov_b32_e32 v2, v6
	s_waitcnt lgkmcnt(1)
	v_mov_b32_e32 v3, v118
	v_pk_fma_f32 v[2:3], v[178:179], v[2:3], v[130:131] op_sel_hi:[0,1,1]
	v_mov_b32_e32 v118, v7
	v_pk_fma_f32 v[2:3], v[138:139], v[118:119], v[2:3] op_sel_hi:[0,1,1]
	v_mov_b32_e32 v4, v8
	v_mov_b32_e32 v5, v120
	v_pk_fma_f32 v[2:3], v[186:187], v[4:5], v[2:3] op_sel_hi:[0,1,1]
	v_mov_b32_e32 v120, v9
	v_pk_fma_f32 v[8:9], v[140:141], v[120:121], v[2:3] op_sel_hi:[0,1,1]
	s_waitcnt lgkmcnt(0)
	v_mov_b32_e32 v2, v122
	v_mov_b32_e32 v3, v94
	v_pk_fma_f32 v[2:3], v[34:35], v[2:3], v[132:133] op_sel_hi:[0,1,1]
	v_mov_b32_e32 v94, v123
	v_pk_fma_f32 v[2:3], v[108:109], v[94:95], v[2:3] op_sel_hi:[0,1,1]
	v_mov_b32_e32 v4, v124
	v_mov_b32_e32 v5, v96
	v_pk_fma_f32 v[2:3], v[110:111], v[4:5], v[2:3] op_sel_hi:[0,1,1]
	v_mov_b32_e32 v96, v125
	v_pk_fma_f32 v[6:7], v[112:113], v[96:97], v[2:3] op_sel_hi:[0,1,1]
	ds_read_b128 v[2:5], v170 offset:3344
	ds_read_b128 v[114:117], v170 offset:3088
	ds_read_b128 v[118:121], v170 offset:3216
	ds_read_b128 v[94:97], v190 offset:272
	ds_read_b128 v[122:125], v190 offset:144
	s_waitcnt lgkmcnt(4)
	v_mov_b32_e32 v126, v2
	v_add_u32_e32 v163, 32, v163
	v_add_u32_e32 v162, 0x2000, v162
	s_waitcnt lgkmcnt(1)
	v_mov_b32_e32 v127, v94
	v_pk_fma_f32 v[126:127], v[176:177], v[126:127], v[172:173] op_sel_hi:[0,1,1]
	v_mov_b32_e32 v94, v3
	v_pk_fma_f32 v[2:3], v[134:135], v[94:95], v[126:127] op_sel_hi:[0,1,1]
	v_mov_b32_e32 v94, v4
	v_mov_b32_e32 v95, v96
	v_pk_fma_f32 v[2:3], v[184:185], v[94:95], v[2:3] op_sel_hi:[0,1,1]
	v_mov_b32_e32 v96, v5
	v_pk_fma_f32 v[96:97], v[136:137], v[96:97], v[2:3] op_sel_hi:[0,1,1]
	v_mov_b32_e32 v2, v114
	v_mov_b32_e32 v3, v180
	v_pk_fma_f32 v[2:3], v[178:179], v[2:3], v[174:175] op_sel_hi:[0,1,1]
	v_mov_b32_e32 v180, v115
	v_pk_fma_f32 v[2:3], v[138:139], v[180:181], v[2:3] op_sel_hi:[0,1,1]
	v_mov_b32_e32 v4, v116
	v_mov_b32_e32 v5, v182
	v_pk_fma_f32 v[2:3], v[186:187], v[4:5], v[2:3] op_sel_hi:[0,1,1]
	v_mov_b32_e32 v182, v117
	v_pk_fma_f32 v[94:95], v[140:141], v[182:183], v[2:3] op_sel_hi:[0,1,1]
	s_waitcnt lgkmcnt(0)
	v_mov_b32_e32 v2, v122
	v_mov_b32_e32 v3, v118
	v_pk_fma_f32 v[2:3], v[34:35], v[2:3], v[90:91] op_sel_hi:[0,1,1]
	v_mov_b32_e32 v118, v123
	v_pk_fma_f32 v[2:3], v[108:109], v[118:119], v[2:3] op_sel_hi:[0,1,1]
	v_mov_b32_e32 v4, v124
	v_mov_b32_e32 v5, v120
	v_pk_fma_f32 v[2:3], v[110:111], v[4:5], v[2:3] op_sel_hi:[0,1,1]
	v_mov_b32_e32 v120, v125
	v_pk_fma_f32 v[90:91], v[112:113], v[120:121], v[2:3] op_sel_hi:[0,1,1]
	s_cmp_eq_u32 s2, 0
	s_cbranch_scc0 .LBB0_249
	v_lshlrev_b32_e32 v2, 16, v157
	v_cndmask_b32_e64 v123, 0, v2, s[40:41]
	v_lshlrev_b32_e32 v2, 16, v154
	v_cndmask_b32_e32 v126, 0, v2, vcc
	v_lshlrev_b32_e32 v2, 16, v152
	v_cndmask_b32_e32 v127, 0, v2, vcc
	global_load_dword v2, v[32:33], off offset:1024
	global_load_dword v3, v[40:41], off
	global_load_dword v4, v[36:37], off
	global_load_dword v5, v[38:39], off
	global_load_dword v110, v[32:33], off offset:3712
	global_load_dword v108, v[32:33], off offset:2048
	global_load_dword v112, v[32:33], off
	v_lshlrev_b32_e32 v34, 16, v160
	v_cndmask_b32_e64 v128, 0, v34, s[42:43]
	v_lshlrev_b32_e32 v81, 16, v81
	v_lshlrev_b32_e32 v34, 16, v83
	v_cndmask_b32_e32 v129, 0, v34, vcc
	v_lshlrev_b32_e32 v34, 16, v144
	v_cndmask_b32_e32 v144, 0, v81, vcc
	global_load_dword v81, v[42:43], off
	v_lshlrev_b32_e32 v116, 16, v153
	v_cndmask_b32_e64 v130, 0, v34, s[44:45]
	v_lshlrev_b32_e32 v34, 16, v109
	v_lshlrev_b32_e32 v89, 16, v89
	v_lshlrev_b32_e32 v114, 16, v156
	v_cndmask_b32_e64 v83, 0, v34, s[46:47]
	v_lshlrev_b32_e32 v34, 16, v93
	v_lshlrev_b32_e32 v93, 16, v99
	v_cndmask_b32_e32 v133, 0, v116, vcc
	v_cndmask_b32_e64 v116, 0, v89, s[48:49]
	v_and_b32_e32 v89, 64, v203
	v_lshlrev_b32_e32 v117, 16, v155
	v_lshlrev_b32_e32 v118, 16, v151
	v_lshlrev_b32_e32 v119, 16, v161
	v_lshlrev_b32_e32 v85, 16, v85
	v_lshlrev_b32_e32 v79, 16, v79
	v_lshlrev_b32_e32 v109, 16, v111
	v_cndmask_b32_e64 v111, 0, v34, s[48:49]
	v_lshlrev_b32_e32 v99, 16, v148
	v_lshlrev_b32_e32 v34, 16, v149
	v_lshlrev_b32_e32 v122, 16, v150
	v_cndmask_b32_e64 v131, 0, v114, s[40:41]
	v_cndmask_b32_e64 v114, 0, v93, s[48:49]
	v_add_u32_e32 v89, 64, v89
	v_xor_b32_e32 v93, 1, v203
	v_cndmask_b32_e32 v34, 0, v34, vcc
	v_lshlrev_b32_e32 v124, 16, v145
	v_cndmask_b32_e32 v134, 0, v117, vcc
	v_cndmask_b32_e32 v136, 0, v118, vcc
	v_cndmask_b32_e32 v138, 0, v119, vcc
	v_cndmask_b32_e32 v85, 0, v85, vcc
	v_cndmask_b32_e64 v145, 0, v79, s[44:45]
	v_cndmask_b32_e64 v148, 0, v109, s[46:47]
	v_cndmask_b32_e32 v109, 0, v99, vcc
	v_cndmask_b32_e32 v79, 0, v122, vcc
	v_cmp_lt_i32_e32 vcc, v93, v89
	v_lshlrev_b32_e32 v121, 16, v113
	v_lshlrev_b32_e32 v113, 16, v146
	v_cndmask_b32_e32 v93, v203, v93, vcc
	v_lshlrev_b32_e32 v122, 2, v93
	v_xor_b32_e32 v93, 2, v203
	v_cmp_lt_i32_e32 vcc, v93, v89
	v_cndmask_b32_e64 v146, 0, v121, s[44:45]
	v_lshlrev_b32_e32 v120, 16, v159
	v_cndmask_b32_e32 v93, v203, v93, vcc
	v_lshlrev_b32_e32 v121, 2, v93
	v_xor_b32_e32 v93, 4, v203
	v_cmp_lt_i32_e32 vcc, v93, v89
	v_cndmask_b32_e64 v140, 0, v120, s[42:43]
	v_sub_f32_e32 v99, v127, v126
	v_cndmask_b32_e32 v93, v203, v93, vcc
	v_lshlrev_b32_e32 v120, 2, v93
	v_xor_b32_e32 v93, 8, v203
	v_cmp_lt_i32_e32 vcc, v93, v89
	v_lshlrev_b32_e32 v101, 16, v101
	v_lshlrev_b32_e32 v125, 16, v147
	v_cndmask_b32_e32 v93, v203, v93, vcc
	v_lshlrev_b32_e32 v119, 2, v93
	v_xor_b32_e32 v93, 16, v203
	v_cmp_lt_i32_e32 vcc, v93, v89
	v_cndmask_b32_e64 v147, 0, v101, s[46:47]
	v_lshlrev_b32_e32 v115, 16, v158
	v_cndmask_b32_e32 v93, v203, v93, vcc
	v_lshlrev_b32_e32 v118, 2, v93
	v_xor_b32_e32 v93, 32, v203
	v_cmp_lt_i32_e32 vcc, v93, v89
	v_cndmask_b32_e64 v132, 0, v115, s[40:41]
	v_cndmask_b32_e64 v115, 0, v125, s[50:51]
	v_cndmask_b32_e32 v89, v203, v93, vcc
	v_sub_f32_e32 v93, v123, v126
	s_waitcnt vmcnt(7)
	v_fma_f32 v93, v93, v2, v126
	s_waitcnt vmcnt(5)
	v_fmac_f32_e32 v93, v99, v4
	v_mul_f32_e32 v99, v93, v3
	v_mul_f32_e32 v101, v99, v99
	s_nop 1
	v_mov_b32_dpp v101, v101 quad_perm:[1,0,3,2] row_mask:0xf bank_mask:0xf
	v_lshlrev_b32_e32 v123, 2, v89
	v_sub_f32_e32 v89, v131, v133
	v_cndmask_b32_e64 v117, 0, v124, s[50:51]
	s_waitcnt vmcnt(1)
	v_fma_f32 v89, v89, v112, v133
	s_waitcnt lgkmcnt(0)
	v_fmac_f32_e32 v101, v99, v99
	s_nop 1
	v_mov_b32_dpp v125, v101 quad_perm:[2,3,0,1] row_mask:0xf bank_mask:0xf
	v_sub_f32_e32 v124, v136, v133
	v_fmac_f32_e32 v89, v124, v110
	v_sub_f32_e32 v124, v132, v134
	v_fma_f32 v131, v124, v108, v134
	s_waitcnt lgkmcnt(0)
	v_add_f32_e32 v101, v101, v125
	s_nop 1
	v_mov_b32_dpp v125, v101 row_half_mirror row_mask:0xf bank_mask:0xf
	v_sub_f32_e32 v124, v138, v134
	v_fmac_f32_e32 v131, v124, v5
	v_mul_f32_e32 v102, 0xbfb8aa3b, v102
	v_exp_f32_e32 v102, v102
	s_waitcnt lgkmcnt(0)
	v_add_f32_e32 v101, v101, v125
	s_nop 1
	v_mov_b32_dpp v125, v101 row_mirror row_mask:0xf bank_mask:0xf
	v_mul_f32_e32 v107, 0xbfb8aa3b, v107
	v_add_f32_e32 v102, 1.0, v102
	v_rcp_f32_e32 v102, v102
	v_exp_f32_e32 v107, v107
	s_waitcnt lgkmcnt(0)
	v_add_f32_e32 v101, v101, v125
	v_mov_b32_e32 v124, v101
	s_nop 1
	v_permlane16_swap_b32_e32 v124, v101
	v_mul_f32_e32 v105, 0xbfb8aa3b, v105
	v_exp_f32_e32 v105, v105
	v_cvt_pk_bf16_f32 v89, v89, s0
	v_add_f32_e32 v107, 1.0, v107
	s_waitcnt lgkmcnt(0)
	v_add_f32_e32 v101, v101, v124
	v_mov_b32_e32 v124, v101
	s_nop 1
	v_permlane32_swap_b32_e32 v124, v101
	v_rcp_f32_e32 v107, v107
	v_add_f32_e32 v105, 1.0, v105
	v_rcp_f32_e32 v105, v105
	v_mul_f32_e32 v103, 0xbfb8aa3b, v103
	s_waitcnt lgkmcnt(0)
	v_add_f32_e32 v101, v101, v124
	v_add_f32_e32 v101, 0x2b8cbccc, v101
	v_rsq_f32_e32 v101, v101
	v_mul_f32_e32 v107, 0xbf1b459e, v107
	v_mul_f32_e32 v107, 0x3fb8aa3b, v107
	v_mul_f32_e32 v105, 0xbf1b459e, v105
	v_mul_f32_e32 v99, v99, v101
	v_add_f32_e32 v101, -1.0, v102
	s_waitcnt vmcnt(0)
	v_fma_f32 v101, v101, v81, 1.0
	v_mul_f32_e32 v93, v93, v101
	v_ashrrev_i32_e32 v101, 31, v100
	v_lshlrev_b64 v[100:101], 9, v[100:101]
	v_or_b32_e32 v100, v100, v31
	v_lshl_add_u64 v[124:125], s[74:75], 0, v[100:101]
	global_store_short v[124:125], v89, off
	v_lshl_add_u64 v[124:125], s[76:77], 0, v[100:101]
	v_cvt_pk_bf16_f32 v89, v93, s0
	global_store_short v[124:125], v89, off
	v_lshl_add_u64 v[124:125], s[78:79], 0, v[100:101]
	v_cvt_pk_bf16_f32 v89, v131, s0
	global_store_short v[124:125], v89, off
	v_lshl_add_u64 v[124:125], s[80:81], 0, v[100:101]
	v_cvt_pk_bf16_f32 v89, v99, s0
	v_sub_f32_e32 v93, v126, v127
	global_store_short v[124:125], v89, off
	v_mul_f32_e32 v89, v102, v99
	v_fma_f32 v93, v93, v2, v127
	v_sub_f32_e32 v99, v128, v127
	v_fmac_f32_e32 v93, v99, v4
	v_mul_f32_e32 v99, v93, v3
	v_mul_f32_e32 v102, v99, v99
	v_exp_f32_e32 v107, v107
	v_mul_f32_e32 v105, 0x3fb8aa3b, v105
	s_nop 1
	v_mov_b32_dpp v102, v102 quad_perm:[1,0,3,2] row_mask:0xf bank_mask:0xf
	v_exp_f32_e32 v105, v105
	v_lshl_add_u64 v[124:125], s[82:83], 0, v[100:101]
	v_cvt_pk_bf16_f32 v89, v89, s0
	global_store_short v[124:125], v89, off
	v_lshl_add_u64 v[124:125], s[84:85], 0, v[100:101]
	v_cvt_pk_bf16_f32 v89, v107, s0
	global_store_short v[124:125], v89, off
	v_lshl_add_u64 v[100:101], s[86:87], 0, v[100:101]
	v_cvt_pk_bf16_f32 v89, v105, s0
	s_waitcnt lgkmcnt(0)
	v_fmac_f32_e32 v102, v99, v99
	global_store_short v[100:101], v89, off
	s_nop 1
	v_mov_b32_dpp v101, v102 quad_perm:[2,3,0,1] row_mask:0xf bank_mask:0xf
	v_mul_f32_e32 v106, 0xbfb8aa3b, v106
	v_sub_f32_e32 v89, v133, v136
	v_exp_f32_e32 v103, v103
	v_exp_f32_e32 v106, v106
	s_waitcnt lgkmcnt(0)
	v_add_f32_e32 v101, v102, v101
	s_nop 1
	v_mov_b32_dpp v102, v101 row_half_mirror row_mask:0xf bank_mask:0xf
	v_lshlrev_b32_e32 v87, 16, v87
	v_fma_f32 v89, v89, v112, v136
	v_sub_f32_e32 v100, v140, v136
	v_cndmask_b32_e64 v87, 0, v87, s[42:43]
	s_waitcnt lgkmcnt(0)
	v_add_f32_e32 v101, v101, v102
	s_nop 1
	v_mov_b32_dpp v102, v101 row_mirror row_mask:0xf bank_mask:0xf
	v_fmac_f32_e32 v89, v100, v110
	v_sub_f32_e32 v100, v134, v138
	v_fma_f32 v105, v100, v108, v138
	v_sub_f32_e32 v100, v87, v138
	s_waitcnt lgkmcnt(0)
	v_add_f32_e32 v101, v101, v102
	v_mov_b32_e32 v102, v101
	s_nop 1
	v_permlane16_swap_b32_e32 v102, v101
	v_fmac_f32_e32 v105, v100, v5
	v_add_f32_e32 v100, 1.0, v103
	v_add_f32_e32 v103, 1.0, v106
	v_rcp_f32_e32 v103, v103
	s_waitcnt lgkmcnt(0)
	v_add_f32_e32 v101, v101, v102
	v_mov_b32_e32 v102, v101
	s_nop 1
	v_permlane32_swap_b32_e32 v102, v101
	v_rcp_f32_e32 v106, v100
	v_mul_f32_e32 v100, 0xbf1b459e, v103
	v_mul_f32_e32 v103, 0xbfb8aa3b, v104
	v_exp_f32_e32 v103, v103
	s_waitcnt lgkmcnt(0)
	v_add_f32_e32 v101, v101, v102
	v_add_f32_e32 v101, 0x2b8cbccc, v101
	v_rsq_f32_e32 v101, v101
	v_mul_f32_e32 v100, 0x3fb8aa3b, v100
	v_exp_f32_e32 v104, v100
	v_add_f32_e32 v100, 1.0, v103
	v_rcp_f32_e32 v100, v100
	v_mul_f32_e32 v103, v99, v101
	v_add_f32_e32 v99, -1.0, v106
	v_fma_f32 v99, v99, v81, 1.0
	v_mul_f32_e32 v93, v93, v99
	v_ashrrev_i32_e32 v99, 31, v98
	v_mul_f32_e32 v100, 0xbf1b459e, v100
	v_lshlrev_b64 v[98:99], 9, v[98:99]
	v_mul_f32_e32 v100, 0x3fb8aa3b, v100
	v_or_b32_e32 v98, v98, v31
	v_exp_f32_e32 v102, v100
	v_lshl_add_u64 v[100:101], s[74:75], 0, v[98:99]
	v_cvt_pk_bf16_f32 v89, v89, s0
	global_store_short v[100:101], v89, off
	v_lshl_add_u64 v[100:101], s[76:77], 0, v[98:99]
	v_cvt_pk_bf16_f32 v89, v93, s0
	global_store_short v[100:101], v89, off
	v_lshl_add_u64 v[100:101], s[78:79], 0, v[98:99]
	v_cvt_pk_bf16_f32 v89, v105, s0
	global_store_short v[100:101], v89, off
	v_lshl_add_u64 v[100:101], s[80:81], 0, v[98:99]
	v_cvt_pk_bf16_f32 v89, v103, s0
	global_store_short v[100:101], v89, off
	v_mul_f32_e32 v89, v106, v103
	v_lshl_add_u64 v[100:101], s[82:83], 0, v[98:99]
	v_cvt_pk_bf16_f32 v89, v89, s0
	global_store_short v[100:101], v89, off
	v_lshl_add_u64 v[100:101], s[84:85], 0, v[98:99]
	v_cvt_pk_bf16_f32 v89, v104, s0
	v_sub_f32_e32 v93, v127, v128
	global_store_short v[100:101], v89, off
	v_fma_f32 v93, v93, v2, v128
	v_sub_f32_e32 v100, v129, v128
	v_fmac_f32_e32 v93, v100, v4
	v_mul_f32_e32 v100, v93, v3
	v_mul_f32_e32 v101, v100, v100
	s_nop 1
	v_mov_b32_dpp v101, v101 quad_perm:[1,0,3,2] row_mask:0xf bank_mask:0xf
	v_lshl_add_u64 v[98:99], s[86:87], 0, v[98:99]
	v_cvt_pk_bf16_f32 v89, v102, s0
	global_store_short v[98:99], v89, off
	v_sub_f32_e32 v89, v136, v140
	s_waitcnt lgkmcnt(0)
	v_fmac_f32_e32 v101, v100, v100
	s_nop 1
	v_mov_b32_dpp v99, v101 quad_perm:[2,3,0,1] row_mask:0xf bank_mask:0xf
	v_fma_f32 v89, v89, v112, v140
	v_sub_f32_e32 v98, v144, v140
	v_fmac_f32_e32 v89, v98, v110
	v_sub_f32_e32 v98, v138, v87
	s_waitcnt lgkmcnt(0)
	v_add_f32_e32 v99, v101, v99
	s_nop 1
	v_mov_b32_dpp v101, v99 row_half_mirror row_mask:0xf bank_mask:0xf
	v_fma_f32 v102, v98, v108, v87
	v_sub_f32_e32 v98, v85, v87
	v_fmac_f32_e32 v102, v98, v5
	v_mul_f32_e32 v16, 0xbfb8aa3b, v16
	s_waitcnt lgkmcnt(0)
	v_add_f32_e32 v99, v99, v101
	s_nop 1
	v_mov_b32_dpp v101, v99 row_mirror row_mask:0xf bank_mask:0xf
	v_exp_f32_e32 v16, v16
	v_mul_f32_e32 v13, 0xbfb8aa3b, v13
	v_exp_f32_e32 v13, v13
	v_mul_f32_e32 v15, 0xbfb8aa3b, v15
	s_waitcnt lgkmcnt(0)
	v_add_f32_e32 v98, v99, v101
	v_mov_b32_e32 v99, v98
	s_nop 1
	v_permlane16_swap_b32_e32 v99, v98
	v_add_f32_e32 v16, 1.0, v16
	v_rcp_f32_e32 v16, v16
	v_exp_f32_e32 v15, v15
	v_add_f32_e32 v13, 1.0, v13
	s_waitcnt lgkmcnt(0)
	v_add_f32_e32 v98, v98, v99
	v_mov_b32_e32 v99, v98
	s_nop 1
	v_permlane32_swap_b32_e32 v99, v98
	v_rcp_f32_e32 v13, v13
	v_add_f32_e32 v15, 1.0, v15
	v_rcp_f32_e32 v15, v15
	v_cvt_pk_bf16_f32 v89, v89, s0
	s_waitcnt lgkmcnt(0)
	v_add_f32_e32 v98, v98, v99
	v_add_f32_e32 v98, 0x2b8cbccc, v98
	v_rsq_f32_e32 v98, v98
	v_mul_f32_e32 v13, 0xbf1b459e, v13
	v_mul_f32_e32 v13, 0x3fb8aa3b, v13
	v_mul_f32_e32 v15, 0xbf1b459e, v15
	v_mul_f32_e32 v100, v100, v98
	v_add_f32_e32 v98, -1.0, v16
	v_fma_f32 v98, v98, v81, 1.0
	v_mul_f32_e32 v101, v93, v98
	v_ashrrev_i32_e32 v93, 31, v92
	v_lshlrev_b64 v[92:93], 9, v[92:93]
	v_or_b32_e32 v92, v92, v31
	v_lshl_add_u64 v[98:99], s[74:75], 0, v[92:93]
	v_exp_f32_e32 v13, v13
	v_mul_f32_e32 v15, 0x3fb8aa3b, v15
	global_store_short v[98:99], v89, off
	v_lshl_add_u64 v[98:99], s[76:77], 0, v[92:93]
	v_cvt_pk_bf16_f32 v89, v101, s0
	v_exp_f32_e32 v15, v15
	global_store_short v[98:99], v89, off
	v_lshl_add_u64 v[98:99], s[78:79], 0, v[92:93]
	v_cvt_pk_bf16_f32 v89, v102, s0
	global_store_short v[98:99], v89, off
	v_lshl_add_u64 v[98:99], s[80:81], 0, v[92:93]
	v_cvt_pk_bf16_f32 v89, v100, s0
	v_mul_f32_e32 v16, v16, v100
	global_store_short v[98:99], v89, off
	v_lshl_add_u64 v[98:99], s[82:83], 0, v[92:93]
	v_cvt_pk_bf16_f32 v16, v16, s0
	global_store_short v[98:99], v16, off
	v_lshl_add_u64 v[98:99], s[84:85], 0, v[92:93]
	v_cvt_pk_bf16_f32 v13, v13, s0
	global_store_short v[98:99], v13, off
	v_cvt_pk_bf16_f32 v13, v15, s0
	v_sub_f32_e32 v15, v128, v129
	v_fma_f32 v15, v15, v2, v129
	v_sub_f32_e32 v16, v130, v129
	v_fmac_f32_e32 v15, v16, v4
	v_mul_f32_e32 v16, v15, v3
	v_mul_f32_e32 v89, v16, v16
	s_nop 1
	v_mov_b32_dpp v89, v89 quad_perm:[1,0,3,2] row_mask:0xf bank_mask:0xf
	v_lshl_add_u64 v[92:93], s[86:87], 0, v[92:93]
	global_store_short v[92:93], v13, off
	v_sub_f32_e32 v13, v140, v144
	v_fma_f32 v92, v13, v112, v144
	s_waitcnt lgkmcnt(0)
	v_fmac_f32_e32 v89, v16, v16
	s_nop 1
	v_mov_b32_dpp v93, v89 quad_perm:[2,3,0,1] row_mask:0xf bank_mask:0xf
	v_sub_f32_e32 v13, v145, v144
	v_fmac_f32_e32 v92, v13, v110
	v_sub_f32_e32 v13, v87, v85
	v_mul_f32_e32 v17, 0xbfb8aa3b, v17
	s_waitcnt lgkmcnt(0)
	v_add_f32_e32 v87, v89, v93
	s_nop 1
	v_mov_b32_dpp v89, v87 row_half_mirror row_mask:0xf bank_mask:0xf
	v_exp_f32_e32 v17, v17
	v_mul_f32_e32 v12, 0xbfb8aa3b, v12
	v_exp_f32_e32 v12, v12
	v_fma_f32 v98, v13, v108, v85
	s_waitcnt lgkmcnt(0)
	v_add_f32_e32 v87, v87, v89
	s_nop 1
	v_mov_b32_dpp v89, v87 row_mirror row_mask:0xf bank_mask:0xf
	v_sub_f32_e32 v13, v146, v85
	v_fmac_f32_e32 v98, v13, v5
	v_add_f32_e32 v13, 1.0, v17
	v_add_f32_e32 v12, 1.0, v12
	s_waitcnt lgkmcnt(0)
	v_add_f32_e32 v17, v87, v89
	v_mov_b32_e32 v87, v17
	s_nop 1
	v_permlane16_swap_b32_e32 v87, v17
	v_rcp_f32_e32 v12, v12
	v_rcp_f32_e32 v89, v13
	v_mul_f32_e32 v13, 0xbfb8aa3b, v14
	v_exp_f32_e32 v13, v13
	s_waitcnt lgkmcnt(0)
	v_add_f32_e32 v14, v17, v87
	v_mul_f32_e32 v12, 0xbf1b459e, v12
	v_mov_b32_e32 v17, v14
	s_nop 1
	v_permlane32_swap_b32_e32 v17, v14
	v_mul_f32_e32 v12, 0x3fb8aa3b, v12
	v_exp_f32_e32 v93, v12
	v_add_f32_e32 v12, 1.0, v13
	v_rcp_f32_e32 v12, v12
	s_waitcnt lgkmcnt(0)
	v_add_f32_e32 v13, v14, v17
	v_add_f32_e32 v13, 0x2b8cbccc, v13
	v_rsq_f32_e32 v13, v13
	v_mul_f32_e32 v12, 0xbf1b459e, v12
	v_mul_f32_e32 v12, 0x3fb8aa3b, v12
	v_exp_f32_e32 v17, v12
	v_add_f32_e32 v12, -1.0, v89
	v_fma_f32 v12, v12, v81, 1.0
	v_ashrrev_i32_e32 v87, 31, v86
	v_mul_f32_e32 v16, v16, v13
	v_mul_f32_e32 v99, v15, v12
	v_lshlrev_b64 v[12:13], 9, v[86:87]
	v_or_b32_e32 v12, v12, v31
	v_lshl_add_u64 v[14:15], s[74:75], 0, v[12:13]
	v_cvt_pk_bf16_f32 v86, v92, s0
	global_store_short v[14:15], v86, off
	v_lshl_add_u64 v[14:15], s[76:77], 0, v[12:13]
	v_cvt_pk_bf16_f32 v86, v99, s0
	global_store_short v[14:15], v86, off
	v_lshl_add_u64 v[14:15], s[78:79], 0, v[12:13]
	v_cvt_pk_bf16_f32 v86, v98, s0
	global_store_short v[14:15], v86, off
	v_lshl_add_u64 v[14:15], s[80:81], 0, v[12:13]
	v_cvt_pk_bf16_f32 v86, v16, s0
	v_mul_f32_e32 v16, v89, v16
	global_store_short v[14:15], v86, off
	v_lshl_add_u64 v[14:15], s[82:83], 0, v[12:13]
	v_cvt_pk_bf16_f32 v16, v16, s0
	global_store_short v[14:15], v16, off
	v_lshl_add_u64 v[14:15], s[84:85], 0, v[12:13]
	v_cvt_pk_bf16_f32 v16, v93, s0
	global_store_short v[14:15], v16, off
	v_sub_f32_e32 v15, v129, v130
	v_fma_f32 v15, v15, v2, v130
	v_sub_f32_e32 v16, v83, v130
	v_fmac_f32_e32 v15, v16, v4
	v_mul_f32_e32 v16, v15, v3
	v_cvt_pk_bf16_f32 v14, v17, s0
	v_mul_f32_e32 v17, v16, v16
	s_nop 1
	v_mov_b32_dpp v17, v17 quad_perm:[1,0,3,2] row_mask:0xf bank_mask:0xf
	v_lshl_add_u64 v[12:13], s[86:87], 0, v[12:13]
	global_store_short v[12:13], v14, off
	v_sub_f32_e32 v12, v144, v145
	v_fma_f32 v86, v12, v112, v145
	s_waitcnt lgkmcnt(0)
	v_fmac_f32_e32 v17, v16, v16
	s_nop 1
	v_mov_b32_dpp v13, v17 quad_perm:[2,3,0,1] row_mask:0xf bank_mask:0xf
	v_sub_f32_e32 v12, v147, v145
	v_fmac_f32_e32 v86, v12, v110
	v_sub_f32_e32 v12, v85, v146
	v_fma_f32 v85, v12, v108, v146
	s_waitcnt lgkmcnt(0)
	v_add_f32_e32 v13, v17, v13
	s_nop 1
	v_mov_b32_dpp v14, v13 row_half_mirror row_mask:0xf bank_mask:0xf
	v_sub_f32_e32 v12, v148, v146
	v_fmac_f32_e32 v85, v12, v5
	v_mul_f32_e32 v10, 0xbfb8aa3b, v10
	v_exp_f32_e32 v10, v10
	s_waitcnt lgkmcnt(0)
	v_add_f32_e32 v13, v13, v14
	s_nop 1
	v_mov_b32_dpp v14, v13 row_mirror row_mask:0xf bank_mask:0xf
	v_mul_f32_e32 v8, 0xbfb8aa3b, v8
	v_exp_f32_e32 v8, v8
	v_add_f32_e32 v10, 1.0, v10
	v_rcp_f32_e32 v10, v10
	s_waitcnt lgkmcnt(0)
	v_add_f32_e32 v12, v13, v14
	v_mov_b32_e32 v13, v12
	s_nop 1
	v_permlane16_swap_b32_e32 v13, v12
	v_add_f32_e32 v8, 1.0, v8
	v_rcp_f32_e32 v8, v8
	v_ashrrev_i32_e32 v89, 31, v88
	v_mul_f32_e32 v7, 0xbfb8aa3b, v7
	s_waitcnt lgkmcnt(0)
	v_add_f32_e32 v12, v12, v13
	v_mov_b32_e32 v13, v12
	s_nop 1
	v_permlane32_swap_b32_e32 v13, v12
	v_mul_f32_e32 v8, 0xbf1b459e, v8
	v_mul_f32_e32 v8, 0x3fb8aa3b, v8
	v_cvt_pk_bf16_f32 v86, v86, s0
	v_exp_f32_e32 v7, v7
	s_waitcnt lgkmcnt(0)
	v_add_f32_e32 v12, v12, v13
	v_add_f32_e32 v12, 0x2b8cbccc, v12
	v_rsq_f32_e32 v12, v12
	v_exp_f32_e32 v8, v8
	v_add_f32_e32 v7, 1.0, v7
	v_rcp_f32_e32 v7, v7
	v_mul_f32_e32 v16, v16, v12
	v_add_f32_e32 v12, -1.0, v10
	v_fma_f32 v12, v12, v81, 1.0
	v_mul_f32_e32 v17, v15, v12
	v_lshlrev_b64 v[12:13], 9, v[88:89]
	v_or_b32_e32 v12, v12, v31
	v_lshl_add_u64 v[14:15], s[74:75], 0, v[12:13]
	global_store_short v[14:15], v86, off
	v_lshl_add_u64 v[14:15], s[76:77], 0, v[12:13]
	v_cvt_pk_bf16_f32 v17, v17, s0
	global_store_short v[14:15], v17, off
	v_lshl_add_u64 v[14:15], s[78:79], 0, v[12:13]
	v_cvt_pk_bf16_f32 v17, v85, s0
	global_store_short v[14:15], v17, off
	v_lshl_add_u64 v[14:15], s[80:81], 0, v[12:13]
	v_cvt_pk_bf16_f32 v17, v16, s0
	v_mul_f32_e32 v10, v10, v16
	global_store_short v[14:15], v17, off
	v_lshl_add_u64 v[14:15], s[82:83], 0, v[12:13]
	v_cvt_pk_bf16_f32 v10, v10, s0
	global_store_short v[14:15], v10, off
	v_lshl_add_u64 v[14:15], s[84:85], 0, v[12:13]
	v_cvt_pk_bf16_f32 v8, v8, s0
	global_store_short v[14:15], v8, off
	v_sub_f32_e32 v8, v130, v83
	v_fma_f32 v8, v8, v2, v83
	v_sub_f32_e32 v10, v111, v83
	v_fmac_f32_e32 v8, v10, v4
	v_mul_f32_e32 v10, v8, v3
	v_mul_f32_e32 v7, 0xbf1b459e, v7
	v_mul_f32_e32 v14, v10, v10
	v_mul_f32_e32 v7, 0x3fb8aa3b, v7
	s_nop 1
	v_mov_b32_dpp v14, v14 quad_perm:[1,0,3,2] row_mask:0xf bank_mask:0xf
	v_exp_f32_e32 v7, v7
	v_lshl_add_u64 v[12:13], s[86:87], 0, v[12:13]
	v_mul_f32_e32 v11, 0xbfb8aa3b, v11
	v_exp_f32_e32 v11, v11
	v_cvt_pk_bf16_f32 v7, v7, s0
	s_waitcnt lgkmcnt(0)
	v_fmac_f32_e32 v14, v10, v10
	global_store_short v[12:13], v7, off
	s_nop 1
	v_mov_b32_dpp v13, v14 quad_perm:[2,3,0,1] row_mask:0xf bank_mask:0xf
	v_sub_f32_e32 v7, v145, v147
	v_mul_f32_e32 v9, 0xbfb8aa3b, v9
	v_fma_f32 v12, v7, v112, v147
	v_sub_f32_e32 v7, v116, v147
	s_waitcnt lgkmcnt(0)
	v_add_f32_e32 v13, v14, v13
	s_nop 1
	v_mov_b32_dpp v14, v13 row_half_mirror row_mask:0xf bank_mask:0xf
	v_exp_f32_e32 v9, v9
	v_fmac_f32_e32 v12, v7, v110
	v_sub_f32_e32 v7, v146, v148
	v_fma_f32 v15, v7, v108, v148
	s_waitcnt lgkmcnt(0)
	v_add_f32_e32 v13, v13, v14
	s_nop 1
	v_mov_b32_dpp v14, v13 row_mirror row_mask:0xf bank_mask:0xf
	v_sub_f32_e32 v7, v114, v148
	v_fmac_f32_e32 v15, v7, v5
	v_add_f32_e32 v7, 1.0, v11
	v_add_f32_e32 v9, 1.0, v9
	s_waitcnt lgkmcnt(0)
	v_add_f32_e32 v11, v13, v14
	v_mov_b32_e32 v13, v11
	s_nop 1
	v_permlane16_swap_b32_e32 v13, v11
	v_rcp_f32_e32 v9, v9
	v_mul_f32_e32 v6, 0xbfb8aa3b, v6
	v_exp_f32_e32 v6, v6
	v_rcp_f32_e32 v14, v7
	v_mul_f32_e32 v7, 0xbf1b459e, v9
	s_waitcnt lgkmcnt(0)
	v_add_f32_e32 v9, v11, v13
	v_mov_b32_e32 v11, v9
	s_nop 1
	v_permlane32_swap_b32_e32 v11, v9
	v_add_f32_e32 v6, 1.0, v6
	v_rcp_f32_e32 v6, v6
	v_mul_f32_e32 v7, 0x3fb8aa3b, v7
	v_exp_f32_e32 v13, v7
	s_waitcnt lgkmcnt(0)
	v_add_f32_e32 v7, v9, v11
	v_add_f32_e32 v7, 0x2b8cbccc, v7
	v_rsq_f32_e32 v7, v7
	v_mul_f32_e32 v6, 0xbf1b459e, v6
	v_mul_f32_e32 v6, 0x3fb8aa3b, v6
	v_exp_f32_e32 v11, v6
	v_add_f32_e32 v6, -1.0, v14
	v_fma_f32 v6, v6, v81, 1.0
	v_ashrrev_i32_e32 v85, 31, v84
	v_mul_f32_e32 v10, v10, v7
	v_mul_f32_e32 v16, v8, v6
	v_lshlrev_b64 v[6:7], 9, v[84:85]
	v_or_b32_e32 v6, v6, v31
	v_lshl_add_u64 v[8:9], s[74:75], 0, v[6:7]
	v_cvt_pk_bf16_f32 v12, v12, s0
	global_store_short v[8:9], v12, off
	v_lshl_add_u64 v[8:9], s[76:77], 0, v[6:7]
	v_cvt_pk_bf16_f32 v12, v16, s0
	global_store_short v[8:9], v12, off
	v_lshl_add_u64 v[8:9], s[78:79], 0, v[6:7]
	v_cvt_pk_bf16_f32 v12, v15, s0
	global_store_short v[8:9], v12, off
	v_lshl_add_u64 v[8:9], s[80:81], 0, v[6:7]
	v_cvt_pk_bf16_f32 v12, v10, s0
	v_mul_f32_e32 v10, v14, v10
	global_store_short v[8:9], v12, off
	v_lshl_add_u64 v[8:9], s[82:83], 0, v[6:7]
	v_cvt_pk_bf16_f32 v10, v10, s0
	global_store_short v[8:9], v10, off
	v_lshl_add_u64 v[8:9], s[84:85], 0, v[6:7]
	v_cvt_pk_bf16_f32 v10, v13, s0
	global_store_short v[8:9], v10, off
	v_sub_f32_e32 v9, v83, v111
	v_fma_f32 v9, v9, v2, v111
	v_sub_f32_e32 v10, v34, v111
	v_fmac_f32_e32 v9, v10, v4
	v_mul_f32_e32 v10, v9, v3
	v_cvt_pk_bf16_f32 v8, v11, s0
	v_mul_f32_e32 v11, v10, v10
	s_nop 1
	v_mov_b32_dpp v11, v11 quad_perm:[1,0,3,2] row_mask:0xf bank_mask:0xf
	v_lshl_add_u64 v[6:7], s[86:87], 0, v[6:7]
	global_store_short v[6:7], v8, off
	v_mul_f32_e32 v14, 0xbfb8aa3b, v94
	v_sub_f32_e32 v6, v147, v116
	s_waitcnt lgkmcnt(0)
	v_fmac_f32_e32 v11, v10, v10
	s_nop 1
	v_mov_b32_dpp v7, v11 quad_perm:[2,3,0,1] row_mask:0xf bank_mask:0xf
	v_exp_f32_e32 v14, v14
	v_fma_f32 v12, v6, v112, v116
	v_sub_f32_e32 v6, v109, v116
	v_fmac_f32_e32 v12, v6, v110
	s_waitcnt lgkmcnt(0)
	v_add_f32_e32 v7, v11, v7
	s_nop 1
	v_mov_b32_dpp v8, v7 row_half_mirror row_mask:0xf bank_mask:0xf
	v_mul_f32_e32 v11, 0xbfb8aa3b, v96
	v_exp_f32_e32 v11, v11
	v_sub_f32_e32 v6, v148, v114
	v_fma_f32 v13, v6, v108, v114
	s_waitcnt lgkmcnt(0)
	v_add_f32_e32 v7, v7, v8
	s_nop 1
	v_mov_b32_dpp v8, v7 row_mirror row_mask:0xf bank_mask:0xf
	v_sub_f32_e32 v6, v79, v114
	v_fmac_f32_e32 v13, v6, v5
	v_add_f32_e32 v6, 1.0, v11
	v_add_f32_e32 v11, 1.0, v14
	v_rcp_f32_e32 v11, v11
	s_waitcnt lgkmcnt(0)
	v_add_f32_e32 v7, v7, v8
	v_mov_b32_e32 v8, v7
	s_nop 1
	v_permlane16_swap_b32_e32 v8, v7
	v_rcp_f32_e32 v14, v6
	v_mul_f32_e32 v6, 0xbf1b459e, v11
	v_mul_f32_e32 v11, 0xbfb8aa3b, v91
	v_exp_f32_e32 v11, v11
	s_waitcnt lgkmcnt(0)
	v_add_f32_e32 v7, v7, v8
	v_mov_b32_e32 v8, v7
	s_nop 1
	v_permlane32_swap_b32_e32 v8, v7
	v_mul_f32_e32 v6, 0x3fb8aa3b, v6
	v_exp_f32_e32 v15, v6
	v_add_f32_e32 v6, 1.0, v11
	v_rcp_f32_e32 v6, v6
	s_waitcnt lgkmcnt(0)
	v_add_f32_e32 v7, v7, v8
	v_add_f32_e32 v7, 0x2b8cbccc, v7
	v_rsq_f32_e32 v7, v7
	v_mul_f32_e32 v6, 0xbf1b459e, v6
	v_mul_f32_e32 v6, 0x3fb8aa3b, v6
	v_exp_f32_e32 v11, v6
	v_add_f32_e32 v6, -1.0, v14
	v_fma_f32 v6, v6, v81, 1.0
	v_ashrrev_i32_e32 v83, 31, v82
	v_mul_f32_e32 v10, v10, v7
	v_mul_f32_e32 v16, v9, v6
	v_lshlrev_b64 v[6:7], 9, v[82:83]
	v_or_b32_e32 v6, v6, v31
	v_lshl_add_u64 v[8:9], s[74:75], 0, v[6:7]
	v_cvt_pk_bf16_f32 v12, v12, s0
	global_store_short v[8:9], v12, off
	v_lshl_add_u64 v[8:9], s[76:77], 0, v[6:7]
	v_cvt_pk_bf16_f32 v12, v16, s0
	global_store_short v[8:9], v12, off
	v_lshl_add_u64 v[8:9], s[78:79], 0, v[6:7]
	v_cvt_pk_bf16_f32 v12, v13, s0
	global_store_short v[8:9], v12, off
	v_lshl_add_u64 v[8:9], s[80:81], 0, v[6:7]
	v_cvt_pk_bf16_f32 v12, v10, s0
	v_mul_f32_e32 v10, v14, v10
	global_store_short v[8:9], v12, off
	v_lshl_add_u64 v[8:9], s[82:83], 0, v[6:7]
	v_cvt_pk_bf16_f32 v10, v10, s0
	global_store_short v[8:9], v10, off
	v_lshl_add_u64 v[8:9], s[84:85], 0, v[6:7]
	v_cvt_pk_bf16_f32 v10, v15, s0
	global_store_short v[8:9], v10, off
	v_lshl_add_u64 v[6:7], s[86:87], 0, v[6:7]
	v_cvt_pk_bf16_f32 v8, v11, s0
	v_cndmask_b32_e64 v113, 0, v113, s[50:51]
	global_store_short v[6:7], v8, off
	v_sub_f32_e32 v6, v111, v34
	v_sub_f32_e32 v7, v113, v34
	v_fmac_f32_e32 v34, v6, v2
	v_fmac_f32_e32 v34, v7, v4
	v_mul_f32_e32 v2, v34, v3
	v_mul_f32_e32 v3, v2, v2
	s_nop 1
	v_mov_b32_dpp v3, v3 quad_perm:[1,0,3,2] row_mask:0xf bank_mask:0xf
	global_load_dword v122, v[44:45], off
	v_sub_f32_e32 v4, v116, v109
	v_sub_f32_e32 v6, v117, v109
	v_fmac_f32_e32 v109, v4, v112
	s_waitcnt lgkmcnt(0)
	v_fmac_f32_e32 v3, v2, v2
	s_nop 1
	v_mov_b32_dpp v4, v3 quad_perm:[2,3,0,1] row_mask:0xf bank_mask:0xf
	v_fmac_f32_e32 v109, v6, v110
	v_sub_f32_e32 v6, v114, v79
	v_sub_f32_e32 v7, v115, v79
	v_fmac_f32_e32 v79, v6, v108
	s_waitcnt lgkmcnt(0)
	v_add_f32_e32 v3, v3, v4
	s_nop 1
	v_mov_b32_dpp v4, v3 row_half_mirror row_mask:0xf bank_mask:0xf
	v_mul_f32_e32 v6, 0xbfb8aa3b, v97
	v_mul_f32_e32 v8, 0xbfb8aa3b, v95
	v_exp_f32_e32 v6, v6
	v_exp_f32_e32 v8, v8
	s_waitcnt lgkmcnt(0)
	v_add_f32_e32 v3, v3, v4
	s_nop 1
	v_mov_b32_dpp v4, v3 row_mirror row_mask:0xf bank_mask:0xf
	v_fmac_f32_e32 v79, v7, v5
	v_add_f32_e32 v5, 1.0, v6
	v_add_f32_e32 v6, 1.0, v8
	v_rcp_f32_e32 v6, v6
	s_waitcnt lgkmcnt(0)
	v_add_f32_e32 v3, v3, v4
	v_mov_b32_e32 v4, v3
	s_nop 1
	v_permlane16_swap_b32_e32 v4, v3
	v_rcp_f32_e32 v7, v5
	v_mul_f32_e32 v5, 0xbf1b459e, v6
	v_mul_f32_e32 v6, 0xbfb8aa3b, v90
	v_exp_f32_e32 v6, v6
	s_waitcnt lgkmcnt(0)
	v_add_f32_e32 v3, v3, v4
	v_mov_b32_e32 v4, v3
	s_nop 1
	v_permlane32_swap_b32_e32 v4, v3
	v_mul_f32_e32 v5, 0x3fb8aa3b, v5
	v_exp_f32_e32 v8, v5
	v_add_f32_e32 v5, 1.0, v6
	v_rcp_f32_e32 v5, v5
	s_waitcnt lgkmcnt(0)
	v_add_f32_e32 v3, v3, v4
	v_add_f32_e32 v3, 0x2b8cbccc, v3
	v_rsq_f32_e32 v3, v3
	v_mul_f32_e32 v4, 0xbf1b459e, v5
	v_mul_f32_e32 v4, 0x3fb8aa3b, v4
	v_exp_f32_e32 v6, v4
	v_mul_f32_e32 v9, v2, v3
	v_add_f32_e32 v2, -1.0, v7
	v_fma_f32 v2, v2, v81, 1.0
	v_ashrrev_i32_e32 v81, 31, v80
	v_mul_f32_e32 v10, v34, v2
	v_lshlrev_b64 v[2:3], 9, v[80:81]
	v_or_b32_e32 v2, v2, v31
	v_lshl_add_u64 v[4:5], s[74:75], 0, v[2:3]
	v_cvt_pk_bf16_f32 v11, v109, s0
	global_store_short v[4:5], v11, off
	v_lshl_add_u64 v[4:5], s[76:77], 0, v[2:3]
	v_cvt_pk_bf16_f32 v10, v10, s0
	global_store_short v[4:5], v10, off
	v_lshl_add_u64 v[4:5], s[78:79], 0, v[2:3]
	v_cvt_pk_bf16_f32 v10, v79, s0
	global_store_short v[4:5], v10, off
	v_lshl_add_u64 v[4:5], s[80:81], 0, v[2:3]
	v_cvt_pk_bf16_f32 v10, v9, s0
	v_mul_f32_e32 v7, v7, v9
	global_store_short v[4:5], v10, off
	v_lshl_add_u64 v[4:5], s[82:83], 0, v[2:3]
	v_cvt_pk_bf16_f32 v7, v7, s0
	global_store_short v[4:5], v7, off
	v_lshl_add_u64 v[4:5], s[84:85], 0, v[2:3]
	v_cvt_pk_bf16_f32 v7, v8, s0
	global_store_short v[4:5], v7, off
	v_lshl_add_u64 v[2:3], s[86:87], 0, v[2:3]
	v_cvt_pk_bf16_f32 v4, v6, s0
	global_store_short v[2:3], v4, off
	ds_read2st64_b32 v[116:117], v141 offset1:2
	ds_read_b128 v[2:5], v142 offset:384
	ds_read2st64_b32 v[118:119], v141 offset0:4 offset1:6
	ds_read_b128 v[6:9], v142 offset:400
	ds_read_b128 v[10:13], v142 offset:416
	ds_read_b128 v[14:17], v142 offset:432
	ds_read_b128 v[80:83], v142 offset:896
	s_waitcnt lgkmcnt(5)
	v_mul_f32_e32 v3, v117, v3
	v_fmac_f32_e32 v3, v116, v2
	s_waitcnt lgkmcnt(4)
	v_mul_f32_e32 v2, v119, v5
	v_fmac_f32_e32 v2, v118, v4
	ds_read_b128 v[84:87], v142 offset:1408
	v_add_f32_e32 v2, v3, v2
	ds_read_b128 v[88:91], v142 offset:1920
	ds_read_b128 v[92:95], v142 offset:2432
	ds_read_b128 v[96:99], v142 offset:2944
	s_waitcnt vmcnt(7)
	v_add_f32_e32 v34, v122, v2
	ds_read_b128 v[2:5], v142 offset:912
	s_waitcnt lgkmcnt(5)
	v_mul_f32_e32 v79, v117, v81
	v_fmac_f32_e32 v79, v116, v80
	v_mul_f32_e32 v80, v119, v83
	v_fmac_f32_e32 v80, v118, v82
	v_add_f32_e32 v79, v79, v80
	ds_read_b128 v[80:83], v142 offset:1424
	s_waitcnt lgkmcnt(5)
	v_mul_f32_e32 v85, v117, v85
	v_fmac_f32_e32 v85, v116, v84
	v_mul_f32_e32 v84, v119, v87
	v_fmac_f32_e32 v84, v118, v86
	v_add_f32_e32 v84, v85, v84
	v_add_f32_e32 v120, v122, v84
	ds_read_b128 v[84:87], v142 offset:1936
	s_waitcnt lgkmcnt(5)
	v_mul_f32_e32 v89, v117, v89
	v_fmac_f32_e32 v89, v116, v88
	v_mul_f32_e32 v88, v119, v91
	v_fmac_f32_e32 v88, v118, v90
	v_add_f32_e32 v88, v89, v88
	v_add_f32_e32 v121, v122, v88
	ds_read_b128 v[88:91], v142 offset:2448
	s_waitcnt lgkmcnt(5)
	v_mul_f32_e32 v93, v117, v93
	v_fmac_f32_e32 v93, v116, v92
	v_mul_f32_e32 v92, v119, v95
	v_fmac_f32_e32 v92, v118, v94
	v_add_f32_e32 v92, v93, v92
	ds_read_b128 v[100:103], v142 offset:3456
	v_add_f32_e32 v123, v122, v92
	ds_read_b128 v[92:95], v142 offset:2960
	s_waitcnt lgkmcnt(6)
	v_mul_f32_e32 v97, v117, v97
	v_fmac_f32_e32 v97, v116, v96
	v_mul_f32_e32 v96, v119, v99
	v_fmac_f32_e32 v96, v118, v98
	v_add_f32_e32 v96, v97, v96
	v_add_f32_e32 v124, v122, v96
	ds_read_b128 v[96:99], v142 offset:3472
	s_waitcnt lgkmcnt(2)
	v_mul_f32_e32 v101, v117, v101
	v_fmac_f32_e32 v101, v116, v100
	v_mul_f32_e32 v100, v119, v103
	v_fmac_f32_e32 v100, v118, v102
	v_add_f32_e32 v104, v101, v100
	ds_read_b128 v[100:103], v143 offset:384
	v_add_f32_e32 v125, v122, v104
	ds_read_b128 v[104:107], v143 offset:400
	ds_read_b128 v[108:111], v143 offset:416
	ds_read_b128 v[112:115], v143 offset:432
	v_add_f32_e32 v79, v122, v79
	s_mov_b32 s2, 0xbfb8aa3b
	s_waitcnt lgkmcnt(3)
	v_mul_f32_e32 v117, v117, v101
	v_fmac_f32_e32 v117, v116, v100
	v_mul_f32_e32 v116, v119, v103
	ds_read2st64_b32 v[100:101], v141 offset0:8 offset1:10
	v_fmac_f32_e32 v116, v118, v102
	ds_read2st64_b32 v[102:103], v141 offset0:12 offset1:14
	v_add_f32_e32 v116, v117, v116
	v_add_f32_e32 v116, v122, v116
	s_waitcnt lgkmcnt(1)
	v_mul_f32_e32 v7, v101, v7
	v_mul_f32_e32 v3, v101, v3
	v_fmac_f32_e32 v7, v100, v6
	s_waitcnt lgkmcnt(0)
	v_mul_f32_e32 v6, v103, v9
	v_fmac_f32_e32 v3, v100, v2
	v_mul_f32_e32 v2, v103, v5
	v_fmac_f32_e32 v6, v102, v8
	v_fmac_f32_e32 v2, v102, v4
	v_add_f32_e32 v6, v7, v6
	v_add_f32_e32 v2, v3, v2
	v_add_f32_e32 v6, v34, v6
	v_add_f32_e32 v34, v79, v2
	v_mul_f32_e32 v2, v101, v81
	v_mul_f32_e32 v3, v103, v83
	v_fmac_f32_e32 v2, v100, v80
	v_fmac_f32_e32 v3, v102, v82
	v_add_f32_e32 v2, v2, v3
	v_add_f32_e32 v79, v120, v2
	v_mul_f32_e32 v2, v101, v85
	v_mul_f32_e32 v3, v103, v87
	v_fmac_f32_e32 v2, v100, v84
	v_fmac_f32_e32 v3, v102, v86
	v_add_f32_e32 v2, v2, v3
	v_add_f32_e32 v117, v121, v2
	v_mul_f32_e32 v2, v101, v89
	v_mul_f32_e32 v3, v103, v91
	v_fmac_f32_e32 v2, v100, v88
	v_fmac_f32_e32 v3, v102, v90
	v_add_f32_e32 v2, v2, v3
	v_add_f32_e32 v118, v123, v2
	v_mul_f32_e32 v2, v101, v93
	v_mul_f32_e32 v3, v103, v95
	v_fmac_f32_e32 v2, v100, v92
	v_fmac_f32_e32 v3, v102, v94
	v_add_f32_e32 v2, v2, v3
	v_add_f32_e32 v119, v124, v2
	v_mul_f32_e32 v2, v101, v97
	v_mul_f32_e32 v3, v103, v99
	v_fmac_f32_e32 v2, v100, v96
	v_fmac_f32_e32 v3, v102, v98
	v_add_f32_e32 v2, v2, v3
	ds_read2st64_b32 v[96:97], v141 offset0:16 offset1:18
	ds_read2st64_b32 v[98:99], v141 offset0:20 offset1:22
	v_add_f32_e32 v120, v125, v2
	v_mul_f32_e32 v2, v101, v105
	v_mul_f32_e32 v3, v103, v107
	v_fmac_f32_e32 v2, v100, v104
	v_fmac_f32_e32 v3, v102, v106
	v_add_f32_e32 v2, v2, v3
	v_add_f32_e32 v100, v116, v2
	ds_read_b128 v[2:5], v142 offset:928
	s_waitcnt lgkmcnt(2)
	v_mul_f32_e32 v7, v97, v11
	s_waitcnt lgkmcnt(1)
	v_mul_f32_e32 v8, v99, v13
	v_fmac_f32_e32 v7, v96, v10
	v_fmac_f32_e32 v8, v98, v12
	v_add_f32_e32 v7, v7, v8
	v_add_f32_e32 v101, v6, v7
	ds_read_b128 v[6:9], v142 offset:1440
	ds_read_b128 v[10:13], v142 offset:944
	s_waitcnt lgkmcnt(2)
	v_mul_f32_e32 v3, v97, v3
	v_fmac_f32_e32 v3, v96, v2
	v_mul_f32_e32 v2, v99, v5
	v_fmac_f32_e32 v2, v98, v4
	v_add_f32_e32 v2, v3, v2
	v_add_f32_e32 v34, v34, v2
	ds_read_b128 v[2:5], v142 offset:1456
	s_waitcnt lgkmcnt(2)
	v_mul_f32_e32 v7, v97, v7
	ds_read_b128 v[80:83], v142 offset:1952
	ds_read_b128 v[84:87], v142 offset:1968
	v_fmac_f32_e32 v7, v96, v6
	v_mul_f32_e32 v6, v99, v9
	v_fmac_f32_e32 v6, v98, v8
	v_add_f32_e32 v6, v7, v6
	v_add_f32_e32 v79, v79, v6
	ds_read_b128 v[6:9], v142 offset:2464
	s_waitcnt lgkmcnt(2)
	v_mul_f32_e32 v81, v97, v81
	v_fmac_f32_e32 v81, v96, v80
	v_mul_f32_e32 v80, v99, v83
	v_fmac_f32_e32 v80, v98, v82
	v_add_f32_e32 v80, v81, v80
	v_add_f32_e32 v102, v117, v80
	ds_read_b128 v[80:83], v142 offset:2480
	s_waitcnt lgkmcnt(1)
	v_mul_f32_e32 v7, v97, v7
	ds_read_b128 v[88:91], v142 offset:2976
	ds_read_b128 v[92:95], v142 offset:2992
	v_fmac_f32_e32 v7, v96, v6
	v_mul_f32_e32 v6, v99, v9
	v_fmac_f32_e32 v6, v98, v8
	v_add_f32_e32 v6, v7, v6
	v_add_f32_e32 v103, v118, v6
	ds_read_b128 v[6:9], v142 offset:3488
	s_waitcnt lgkmcnt(2)
	v_mul_f32_e32 v89, v97, v89
	v_fmac_f32_e32 v89, v96, v88
	v_mul_f32_e32 v88, v99, v91
	v_fmac_f32_e32 v88, v98, v90
	v_add_f32_e32 v88, v89, v88
	v_add_f32_e32 v104, v119, v88
	ds_read_b128 v[88:91], v142 offset:3504
	s_waitcnt lgkmcnt(1)
	v_mul_f32_e32 v7, v97, v7
	v_fmac_f32_e32 v7, v96, v6
	v_mul_f32_e32 v6, v99, v9
	v_fmac_f32_e32 v6, v98, v8
	v_add_f32_e32 v6, v7, v6
	v_add_f32_e32 v105, v120, v6
	v_mul_f32_e32 v6, v97, v109
	v_mul_f32_e32 v7, v99, v111
	v_fmac_f32_e32 v6, v96, v108
	ds_read2st64_b32 v[96:97], v141 offset0:24 offset1:26
	v_fmac_f32_e32 v7, v98, v110
	ds_read2st64_b32 v[98:99], v141 offset0:28 offset1:30
	v_add_f32_e32 v6, v6, v7
	v_add_f32_e32 v100, v100, v6
	s_waitcnt lgkmcnt(1)
	v_mul_f32_e32 v6, v97, v15
	v_fmac_f32_e32 v6, v96, v14
	s_waitcnt lgkmcnt(0)
	v_mul_f32_e32 v7, v99, v17
	v_fmac_f32_e32 v7, v98, v16
	v_mul_f32_e32 v3, v97, v3
	v_add_f32_e32 v6, v6, v7
	v_fmac_f32_e32 v3, v96, v2
	v_mul_f32_e32 v2, v99, v5
	v_add_f32_e32 v9, v101, v6
	v_mul_f32_e32 v6, v97, v11
	v_mul_f32_e32 v7, v99, v13
	v_fmac_f32_e32 v2, v98, v4
	v_fmac_f32_e32 v6, v96, v10
	v_fmac_f32_e32 v7, v98, v12
	v_add_f32_e32 v2, v3, v2
	v_add_f32_e32 v6, v6, v7
	v_add_f32_e32 v7, v79, v2
	v_mul_f32_e32 v2, v97, v85
	v_mul_f32_e32 v3, v99, v87
	v_fmac_f32_e32 v2, v96, v84
	v_fmac_f32_e32 v3, v98, v86
	v_add_f32_e32 v2, v2, v3
	v_add_f32_e32 v8, v34, v6
	v_add_f32_e32 v6, v102, v2
	v_mul_f32_e32 v2, v97, v81
	v_mul_f32_e32 v3, v99, v83
	v_fmac_f32_e32 v2, v96, v80
	v_fmac_f32_e32 v3, v98, v82
	v_add_f32_e32 v2, v2, v3
	v_add_f32_e32 v5, v103, v2
	v_mul_f32_e32 v2, v97, v93
	v_mul_f32_e32 v3, v99, v95
	v_fmac_f32_e32 v2, v96, v92
	v_fmac_f32_e32 v3, v98, v94
	v_add_f32_e32 v2, v2, v3
	v_mul_f32_e64 v11, |v9|, s2
	v_add_f32_e32 v3, v104, v2
	v_mul_f32_e32 v2, v97, v89
	v_mul_f32_e32 v4, v99, v91
	v_exp_f32_e32 v11, v11
	v_fmac_f32_e32 v2, v96, v88
	v_fmac_f32_e32 v4, v98, v90
	v_add_f32_e32 v2, v2, v4
	v_mul_f32_e32 v4, v97, v113
	v_mul_f32_e32 v10, v99, v115
	v_fmac_f32_e32 v4, v96, v112
	v_fmac_f32_e32 v10, v98, v114
	v_add_f32_e32 v4, v4, v10
	v_add_f32_e32 v10, 1.0, v11
	v_log_f32_e32 v10, v10
	v_max_f32_e64 v9, -v9, 0
	s_ashr_i32 s89, s88, 31
	v_lshl_add_u64 v[12:13], v[46:47], 0, s[88:89]
	v_fmac_f32_e32 v9, 0x3f317218, v10
	v_mul_f32_e64 v10, |v8|, s2
	v_exp_f32_e32 v14, v10
	v_lshlrev_b64 v[10:11], 9, v[12:13]
	v_add_f32_e32 v4, v100, v4
	v_mul_f32_e32 v9, 0xbd800000, v9
	v_lshl_add_u64 v[100:101], v[48:49], 0, v[10:11]
	global_store_dword v[100:101], v9, off
	v_add_f32_e32 v9, 1.0, v14
	v_log_f32_e32 v9, v9
	v_mul_f32_e64 v10, |v7|, s2
	v_exp_f32_e32 v10, v10
	v_max_f32_e64 v8, -v8, 0
	v_fmac_f32_e32 v8, 0x3f317218, v9
	v_mul_f32_e32 v8, 0xbd800000, v8
	global_store_dword v[100:101], v8, off offset:512
	v_add_f32_e32 v8, 1.0, v10
	v_log_f32_e32 v8, v8
	v_mul_f32_e64 v9, |v6|, s2
	v_exp_f32_e32 v9, v9
	v_max_f32_e64 v7, -v7, 0
	v_fmac_f32_e32 v7, 0x3f317218, v8
	v_mul_f32_e32 v7, 0xbd800000, v7
	global_store_dword v[100:101], v7, off offset:1024
	v_add_f32_e32 v7, 1.0, v9
	v_log_f32_e32 v7, v7
	v_mul_f32_e64 v8, |v5|, s2
	v_exp_f32_e32 v8, v8
	v_max_f32_e64 v6, -v6, 0
	v_fmac_f32_e32 v6, 0x3f317218, v7
	v_mul_f32_e32 v6, 0xbd800000, v6
	global_store_dword v[100:101], v6, off offset:1536
	v_add_f32_e32 v6, 1.0, v8
	v_log_f32_e32 v6, v6
	v_mul_f32_e64 v7, |v3|, s2
	v_exp_f32_e32 v7, v7
	v_max_f32_e64 v5, -v5, 0
	v_fmac_f32_e32 v5, 0x3f317218, v6
	v_add_f32_e32 v2, v105, v2
	v_mul_f32_e32 v5, 0xbd800000, v5
	global_store_dword v[100:101], v5, off offset:2048
	v_add_f32_e32 v5, 1.0, v7
	v_mul_f32_e64 v6, |v2|, s2
	v_log_f32_e32 v5, v5
	v_exp_f32_e32 v6, v6
	v_max_f32_e64 v3, -v3, 0
	s_add_i32 s4, s88, -2
	v_fmac_f32_e32 v3, 0x3f317218, v5
	v_add_f32_e32 v5, 1.0, v6
	v_mul_f32_e64 v6, |v4|, s2
	v_exp_f32_e32 v6, v6
	v_log_f32_e32 v5, v5
	v_mul_f32_e32 v3, 0xbd800000, v3
	v_mad_i64_i32 v[102:103], s[2:3], s88, v202, v[76:77]
	s_cmp_ge_i32 s4, s1
	global_store_dword v[100:101], v3, off offset:2560
	v_add_f32_e32 v3, 1.0, v6
	s_cselect_b64 s[2:3], -1, 0
	s_cmp_lt_i32 s4, s0
	v_max_f32_e64 v2, -v2, 0
	v_log_f32_e32 v3, v3
	s_cselect_b64 s[4:5], -1, 0
	v_fmac_f32_e32 v2, 0x3f317218, v5
	s_and_b64 vcc, s[2:3], s[4:5]
	v_mul_f32_e32 v2, 0xbd800000, v2
	s_and_b64 s[2:3], vcc, exec
	global_store_dword v[100:101], v2, off offset:3072
	v_max_f32_e64 v2, -v4, 0
	s_cselect_b32 s3, -1, 0
	s_cselect_b32 s2, 0xffffcc00, 0
	s_add_i32 s4, s88, -1
	v_fmac_f32_e32 v2, 0x3f317218, v3
	s_cmp_ge_i32 s4, s1
	v_mul_f32_e32 v34, 0xbd800000, v2
	v_lshl_add_u64 v[2:3], v[102:103], 0, s[2:3]
	s_cselect_b64 s[2:3], -1, 0
	s_cmp_lt_i32 s4, s0
	s_cselect_b64 s[4:5], -1, 0
	s_and_b64 s[2:3], s[2:3], s[4:5]
	s_and_b64 s[4:5], s[2:3], exec
	s_cselect_b32 s5, -1, 0
	s_cselect_b32 s4, 0xffffe600, 0
	s_cmp_ge_i32 s88, s1
	v_lshl_add_u64 v[4:5], v[102:103], 0, s[4:5]
	s_cselect_b64 s[4:5], -1, 0
	s_cmp_lt_i32 s88, s0
	s_cselect_b64 s[6:7], -1, 0
	s_and_b64 s[4:5], s[4:5], s[6:7]
	s_or_b32 s10, s88, 1
	s_cmp_ge_i32 s10, s1
	s_cselect_b64 s[6:7], -1, 0
	s_cmp_lt_i32 s10, s0
	s_cselect_b64 s[8:9], -1, 0
	s_and_b64 s[40:41], s[6:7], s[8:9]
	s_and_b64 s[6:7], s[40:41], exec
	s_cselect_b32 s6, 0x1a00, 0
	s_mov_b32 s72, 0
	s_or_b32 s14, s88, 2
	s_mov_b32 s73, 1
	s_mov_b32 s7, s72
	s_cmp_ge_i32 s14, s1
	v_lshl_add_u64 v[6:7], v[102:103], 0, s[6:7]
	s_cselect_b64 s[6:7], -1, 0
	s_cmp_lt_i32 s14, s0
	s_cselect_b64 s[8:9], -1, 0
	s_and_b64 s[42:43], s[6:7], s[8:9]
	s_and_b64 s[6:7], s[42:43], exec
	s_cselect_b32 s6, 0x3400, 0
	s_mov_b32 s7, s72
	v_lshl_add_u64 v[8:9], v[102:103], 0, s[6:7]
	s_or_b32 s6, s88, 3
	s_cmp_ge_i32 s6, s1
	s_cselect_b64 s[8:9], -1, 0
	s_cmp_lt_i32 s6, s0
	s_cselect_b64 s[18:19], -1, 0
	s_and_b64 s[44:45], s[8:9], s[18:19]
	s_and_b64 s[8:9], s[44:45], exec
	s_cselect_b32 s8, 0x4e00, 0
	s_mov_b32 s9, s72
	v_lshl_add_u64 v[10:11], v[102:103], 0, s[8:9]
	s_or_b32 s8, s88, 4
	s_cmp_ge_i32 s8, s1
	s_cselect_b64 s[18:19], -1, 0
	s_cmp_lt_i32 s8, s0
	s_cselect_b64 s[22:23], -1, 0
	s_and_b64 s[46:47], s[18:19], s[22:23]
	s_and_b64 s[18:19], s[46:47], exec
	s_cselect_b32 s18, 0x6800, 0
	s_or_b32 s34, s88, 5
	s_mov_b32 s19, s72
	s_cmp_ge_i32 s34, s1
	v_lshl_add_u64 v[12:13], v[102:103], 0, s[18:19]
	s_cselect_b64 s[18:19], -1, 0
	s_cmp_lt_i32 s34, s0
	s_cselect_b64 s[22:23], -1, 0
	s_and_b64 s[48:49], s[18:19], s[22:23]
	s_and_b64 s[18:19], s[48:49], exec
	s_cselect_b32 s18, 0x8200, 0
	s_or_b32 s36, s88, 6
	s_mov_b32 s19, s72
	s_cmp_ge_i32 s36, s1
	v_lshl_add_u64 v[14:15], v[102:103], 0, s[18:19]
	s_cselect_b64 s[18:19], -1, 0
	s_cmp_lt_i32 s36, s0
	s_cselect_b64 s[22:23], -1, 0
	s_and_b64 s[50:51], s[18:19], s[22:23]
	s_and_b64 s[18:19], s[50:51], exec
	s_cselect_b32 s18, 0x9c00, 0
	s_or_b32 s28, s88, 7
	s_mov_b32 s19, s72
	s_cmp_ge_i32 s28, s1
	v_lshl_add_u64 v[16:17], v[102:103], 0, s[18:19]
	s_cselect_b64 s[18:19], -1, 0
	s_cmp_lt_i32 s28, s0
	s_cselect_b64 s[22:23], -1, 0
	s_and_b64 s[52:53], s[18:19], s[22:23]
	s_and_b64 s[18:19], s[52:53], exec
	s_cselect_b32 s18, 0xb600, 0
	s_or_b32 s30, s88, 8
	s_mov_b32 s19, s72
	s_cmp_ge_i32 s30, s1
	v_lshl_add_u64 v[80:81], v[102:103], 0, s[18:19]
	s_cselect_b64 s[18:19], -1, 0
	s_cmp_lt_i32 s30, s0
	s_cselect_b64 s[22:23], -1, 0
	s_and_b64 s[54:55], s[18:19], s[22:23]
	s_and_b64 s[18:19], s[54:55], exec
	s_cselect_b32 s18, 0xd000, 0
	s_or_b32 s24, s88, 9
	s_mov_b32 s19, s72
	s_cmp_ge_i32 s24, s1
	v_lshl_add_u64 v[82:83], v[102:103], 0, s[18:19]
	s_cselect_b64 s[18:19], -1, 0
	s_cmp_lt_i32 s24, s0
	s_cselect_b64 s[22:23], -1, 0
	s_and_b64 s[56:57], s[18:19], s[22:23]
	s_and_b64 s[18:19], s[56:57], exec
	s_cselect_b32 s18, 0xea00, 0
	s_or_b32 s26, s88, 10
	s_mov_b32 s19, s72
	s_cmp_ge_i32 s26, s1
	v_lshl_add_u64 v[84:85], v[102:103], 0, s[18:19]
	s_cselect_b64 s[18:19], -1, 0
	s_cmp_lt_i32 s26, s0
	s_cselect_b64 s[22:23], -1, 0
	s_and_b64 s[58:59], s[18:19], s[22:23]
	s_and_b64 s[18:19], s[58:59], exec
	s_cselect_b32 s18, 0x10400, 0
	s_mov_b32 s19, s72
	v_lshl_add_u64 v[86:87], v[102:103], 0, s[18:19]
	s_or_b32 s18, s88, 11
	s_cmp_ge_i32 s18, s1
	s_cselect_b64 s[22:23], -1, 0
	s_cmp_lt_i32 s18, s0
	s_cselect_b64 s[60:61], -1, 0
	s_and_b64 s[60:61], s[22:23], s[60:61]
	s_and_b64 s[22:23], s[60:61], exec
	s_cselect_b32 s22, 0x11e00, 0
	s_mov_b32 s23, s72
	v_lshl_add_u64 v[88:89], v[102:103], 0, s[22:23]
	s_or_b32 s22, s88, 12
	s_cmp_ge_i32 s22, s1
	s_cselect_b64 s[62:63], -1, 0
	s_cmp_lt_i32 s22, s0
	s_cselect_b64 s[64:65], -1, 0
	s_and_b64 s[62:63], s[62:63], s[64:65]
	s_and_b64 s[64:65], s[62:63], exec
	s_cselect_b32 s64, 0x13800, 0
	s_or_b32 s92, s88, 13
	s_mov_b32 s65, s72
	s_cmp_ge_i32 s92, s1
	v_lshl_add_u64 v[90:91], v[102:103], 0, s[64:65]
	s_cselect_b64 s[64:65], -1, 0
	s_cmp_lt_i32 s92, s0
	s_cselect_b64 s[66:67], -1, 0
	s_and_b64 s[64:65], s[64:65], s[66:67]
	s_and_b64 s[66:67], s[64:65], exec
	s_cselect_b32 s66, 0x15200, 0
	s_or_b32 s94, s88, 14
	s_mov_b32 s67, s72
	s_cmp_ge_i32 s94, s1
	v_lshl_add_u64 v[92:93], v[102:103], 0, s[66:67]
	s_cselect_b64 s[66:67], -1, 0
	s_cmp_lt_i32 s94, s0
	s_cselect_b64 s[68:69], -1, 0
	s_and_b64 s[66:67], s[66:67], s[68:69]
	s_and_b64 s[68:69], s[66:67], exec
	s_cselect_b32 s68, 0x16c00, 0
	s_or_b32 s90, s88, 15
	s_mov_b32 s69, s72
	s_cmp_ge_i32 s90, s1
	v_lshl_add_u64 v[94:95], v[102:103], 0, s[68:69]
	s_cselect_b64 s[68:69], -1, 0
	s_cmp_lt_i32 s90, s0
	s_cselect_b64 s[70:71], -1, 0
	s_and_b64 s[70:71], s[68:69], s[70:71]
	s_and_b64 s[68:69], s[70:71], exec
	s_cselect_b32 s68, 0x18600, 0
	s_add_i32 s7, s88, 16
	s_mov_b32 s69, s72
	s_cmp_ge_i32 s7, s1
	v_lshl_add_u64 v[96:97], v[102:103], 0, s[68:69]
	s_cselect_b64 s[68:69], -1, 0
	s_cmp_lt_i32 s7, s0
	s_cselect_b64 s[0:1], -1, 0
	s_and_b64 s[68:69], s[68:69], s[0:1]
	s_and_b64 s[0:1], s[68:69], exec
	global_load_ushort v79, v[2:3], off
	global_load_ushort v104, v[4:5], off
	global_load_ushort v105, v[102:103], off
	global_load_ushort v106, v[6:7], off
	global_load_ushort v107, v[8:9], off
	global_load_ushort v108, v[10:11], off
	global_load_ushort v109, v[12:13], off
	s_cselect_b32 s0, 0x1a000, 0
	s_mov_b32 s1, s72
	global_load_ushort v118, v[14:15], off
	global_load_ushort v119, v[16:17], off
	global_load_ushort v120, v[80:81], off
	global_load_ushort v121, v[82:83], off
	global_load_ushort v122, v[84:85], off
	global_load_ushort v123, v[86:87], off
	global_load_ushort v124, v[88:89], off
	global_load_ushort v125, v[90:91], off
	global_load_ushort v126, v[92:93], off
	global_load_ushort v127, v[94:95], off
	global_load_ushort v128, v[96:97], off
	v_lshl_add_u64 v[98:99], v[102:103], 0, s[0:1]
	global_store_dword v[100:101], v34, off offset:3584
	global_load_ushort v129, v[98:99], off
	global_load_dword v117, v[52:53], off
	global_load_dword v116, v[50:51], off
	global_load_dword v133, v[54:55], off
	global_load_dword v134, v[56:57], off
	global_load_dword v136, v[58:59], off
	global_load_ushort v132, v[102:103], off offset:1024
	s_lshl_b64 s[0:1], s[88:89], 11
	s_ashr_i32 s11, s10, 31
	s_ashr_i32 s15, s14, 31
	s_ashr_i32 s7, s6, 31
	s_ashr_i32 s9, s8, 31
	s_ashr_i32 s35, s34, 31
	s_ashr_i32 s37, s36, 31
	s_ashr_i32 s29, s28, 31
	s_ashr_i32 s31, s30, 31
	s_ashr_i32 s25, s24, 31
	s_ashr_i32 s27, s26, 31
	s_ashr_i32 s19, s18, 31
	s_ashr_i32 s23, s22, 31
	s_ashr_i32 s93, s92, 31
	s_ashr_i32 s95, s94, 31
	s_ashr_i32 s91, s90, 31
	s_mov_b32 s97, 0xbfb8aa3b
	s_waitcnt vmcnt(25)
	v_lshlrev_b32_e32 v34, 16, v79
	v_cndmask_b32_e32 v79, 0, v34, vcc
	s_waitcnt vmcnt(24)
	v_lshlrev_b32_e32 v34, 16, v104
	v_cndmask_b32_e64 v115, 0, v34, s[2:3]
	s_waitcnt vmcnt(23)
	v_lshlrev_b32_e32 v34, 16, v105
	v_cndmask_b32_e64 v114, 0, v34, s[4:5]
	s_waitcnt vmcnt(22)
	v_lshlrev_b32_e32 v34, 16, v106
	v_cndmask_b32_e64 v113, 0, v34, s[40:41]
	s_waitcnt vmcnt(21)
	v_lshlrev_b32_e32 v34, 16, v107
	s_waitcnt vmcnt(5)
	v_mul_f32_e32 v101, v117, v115
	s_waitcnt vmcnt(4)
	v_fmac_f32_e32 v101, v116, v79
	v_cndmask_b32_e64 v112, 0, v34, s[42:43]
	v_lshlrev_b32_e32 v34, 16, v108
	s_waitcnt vmcnt(3)
	v_fmac_f32_e32 v101, v133, v114
	v_cndmask_b32_e64 v111, 0, v34, s[44:45]
	v_lshlrev_b32_e32 v34, 16, v109
	s_waitcnt vmcnt(2)
	v_fmac_f32_e32 v101, v134, v113
	v_cndmask_b32_e64 v110, 0, v34, s[46:47]
	v_lshlrev_b32_e32 v34, 16, v118
	s_waitcnt vmcnt(1)
	v_add_f32_e32 v118, v136, v101
	v_mul_f32_e32 v101, 0xbfb8aa3b, v118
	v_cndmask_b32_e64 v109, 0, v34, s[48:49]
	v_lshlrev_b32_e32 v34, 16, v119
	v_exp_f32_e32 v119, v101
	v_cndmask_b32_e64 v108, 0, v34, s[50:51]
	v_lshlrev_b32_e32 v34, 16, v120
	v_mul_f32_e32 v120, v117, v114
	v_fmac_f32_e32 v120, v116, v115
	v_fmac_f32_e32 v120, v133, v113
	v_add_f32_e32 v119, 1.0, v119
	v_fmac_f32_e32 v120, v134, v112
	v_rcp_f32_e32 v119, v119
	v_add_f32_e32 v115, v136, v120
	v_mul_f32_e32 v120, 0xbfb8aa3b, v115
	v_exp_f32_e32 v120, v120
	v_lshlrev_b32_e32 v100, 16, v129
	v_mul_f32_e32 v118, v118, v119
	v_cndmask_b32_e64 v145, 0, v100, s[68:69]
	v_lshl_add_u64 v[100:101], v[60:61], 0, s[0:1]
	v_cvt_pk_bf16_f32 v118, v118, s0
	v_cndmask_b32_e64 v107, 0, v34, s[52:53]
	v_lshlrev_b32_e32 v34, 16, v121
	global_store_short v[100:101], v118, off
	v_add_f32_e32 v118, 1.0, v120
	v_cndmask_b32_e64 v105, 0, v34, s[54:55]
	v_lshlrev_b32_e32 v34, 16, v122
	v_rcp_f32_e32 v118, v118
	v_cndmask_b32_e64 v104, 0, v34, s[56:57]
	v_lshlrev_b32_e32 v34, 16, v123
	v_cndmask_b32_e64 v103, 0, v34, s[58:59]
	v_lshlrev_b32_e32 v34, 16, v124
	v_cndmask_b32_e64 v102, 0, v34, s[60:61]
	v_lshlrev_b32_e32 v34, 16, v125
	v_cndmask_b32_e64 v106, 0, v34, s[62:63]
	v_lshlrev_b32_e32 v34, 16, v126
	s_lshl_b64 s[0:1], s[10:11], 11
	v_mul_f32_e32 v115, v115, v118
	v_cndmask_b32_e64 v138, 0, v34, s[64:65]
	v_lshlrev_b32_e32 v34, 16, v127
	v_lshl_add_u64 v[126:127], v[60:61], 0, s[0:1]
	v_cvt_pk_bf16_f32 v115, v115, s0
	global_store_short v[126:127], v115, off
	v_mul_f32_e32 v115, v117, v113
	v_fmac_f32_e32 v115, v116, v114
	v_fmac_f32_e32 v115, v133, v112
	v_fmac_f32_e32 v115, v134, v111
	v_add_f32_e32 v114, v136, v115
	v_mul_f32_e32 v115, 0xbfb8aa3b, v114
	v_exp_f32_e32 v115, v115
	v_mul_f32_e32 v118, v117, v112
	v_fmac_f32_e32 v118, v116, v113
	v_fmac_f32_e32 v118, v133, v111
	v_add_f32_e32 v115, 1.0, v115
	v_fmac_f32_e32 v118, v134, v110
	v_rcp_f32_e32 v115, v115
	v_add_f32_e32 v113, v136, v118
	v_mul_f32_e32 v118, 0xbfb8aa3b, v113
	v_exp_f32_e32 v118, v118
	s_lshl_b64 s[0:1], s[14:15], 11
	v_mul_f32_e32 v114, v114, v115
	v_lshl_add_u64 v[130:131], v[60:61], 0, s[0:1]
	v_cvt_pk_bf16_f32 v114, v114, s0
	global_store_short v[130:131], v114, off
	v_add_f32_e32 v114, 1.0, v118
	v_rcp_f32_e32 v114, v114
	s_lshl_b64 s[0:1], s[6:7], 11
	v_lshl_add_u64 v[122:123], v[60:61], 0, s[0:1]
	v_cndmask_b32_e64 v140, 0, v34, s[66:67]
	v_mul_f32_e32 v113, v113, v114
	v_cvt_pk_bf16_f32 v113, v113, s0
	global_store_short v[122:123], v113, off
	v_mul_f32_e32 v113, v117, v111
	v_fmac_f32_e32 v113, v116, v112
	v_fmac_f32_e32 v113, v133, v110
	v_fmac_f32_e32 v113, v134, v109
	v_add_f32_e32 v112, v136, v113
	v_mul_f32_e32 v113, 0xbfb8aa3b, v112
	v_exp_f32_e32 v113, v113
	v_mul_f32_e32 v114, v117, v110
	v_fmac_f32_e32 v114, v116, v111
	v_fmac_f32_e32 v114, v133, v109
	v_add_f32_e32 v113, 1.0, v113
	v_fmac_f32_e32 v114, v134, v108
	v_rcp_f32_e32 v113, v113
	v_add_f32_e32 v111, v136, v114
	v_mul_f32_e32 v114, 0xbfb8aa3b, v111
	v_exp_f32_e32 v114, v114
	s_lshl_b64 s[0:1], s[8:9], 11
	v_mul_f32_e32 v112, v112, v113
	v_lshlrev_b32_e32 v34, 16, v128
	v_lshl_add_u64 v[128:129], v[60:61], 0, s[0:1]
	v_cvt_pk_bf16_f32 v112, v112, s0
	global_store_short v[128:129], v112, off
	v_add_f32_e32 v112, 1.0, v114
	v_rcp_f32_e32 v112, v112
	s_lshl_b64 s[0:1], s[34:35], 11
	v_lshl_add_u64 v[118:119], v[60:61], 0, s[0:1]
	v_mul_f32_e32 v146, v117, v106
	v_mul_f32_e32 v111, v111, v112
	v_cvt_pk_bf16_f32 v111, v111, s0
	global_store_short v[118:119], v111, off
	v_mul_f32_e32 v111, v117, v109
	v_fmac_f32_e32 v111, v116, v110
	v_fmac_f32_e32 v111, v133, v108
	v_fmac_f32_e32 v111, v134, v107
	v_add_f32_e32 v110, v136, v111
	v_mul_f32_e32 v111, 0xbfb8aa3b, v110
	v_exp_f32_e32 v111, v111
	v_mul_f32_e32 v112, v117, v108
	v_fmac_f32_e32 v112, v116, v109
	v_fmac_f32_e32 v112, v133, v107
	v_add_f32_e32 v111, 1.0, v111
	v_fmac_f32_e32 v112, v134, v105
	v_rcp_f32_e32 v111, v111
	v_add_f32_e32 v109, v136, v112
	v_mul_f32_e32 v112, 0xbfb8aa3b, v109
	v_exp_f32_e32 v112, v112
	s_lshl_b64 s[0:1], s[36:37], 11
	v_mul_f32_e32 v110, v110, v111
	v_lshl_add_u64 v[124:125], v[60:61], 0, s[0:1]
	v_cvt_pk_bf16_f32 v110, v110, s0
	global_store_short v[124:125], v110, off
	v_add_f32_e32 v110, 1.0, v112
	v_rcp_f32_e32 v110, v110
	s_lshl_b64 s[0:1], s[28:29], 11
	v_lshl_add_u64 v[112:113], v[60:61], 0, s[0:1]
	v_fmac_f32_e32 v146, v116, v102
	v_mul_f32_e32 v109, v109, v110
	v_cvt_pk_bf16_f32 v109, v109, s0
	global_store_short v[112:113], v109, off
	v_mul_f32_e32 v109, v117, v107
	v_fmac_f32_e32 v109, v116, v108
	v_fmac_f32_e32 v109, v133, v105
	v_fmac_f32_e32 v109, v134, v104
	v_add_f32_e32 v108, v136, v109
	v_mul_f32_e32 v109, 0xbfb8aa3b, v108
	v_exp_f32_e32 v109, v109
	v_mul_f32_e32 v110, v117, v105
	v_fmac_f32_e32 v110, v116, v107
	v_fmac_f32_e32 v110, v133, v104
	v_add_f32_e32 v109, 1.0, v109
	v_fmac_f32_e32 v110, v134, v103
	v_rcp_f32_e32 v109, v109
	v_add_f32_e32 v107, v136, v110
	v_mul_f32_e32 v110, 0xbfb8aa3b, v107
	v_exp_f32_e32 v110, v110
	s_lshl_b64 s[0:1], s[30:31], 11
	v_mul_f32_e32 v108, v108, v109
	v_lshl_add_u64 v[120:121], v[60:61], 0, s[0:1]
	v_cvt_pk_bf16_f32 v108, v108, s0
	global_store_short v[120:121], v108, off
	v_add_f32_e32 v108, 1.0, v110
	v_rcp_f32_e32 v110, v108
	s_lshl_b64 s[0:1], s[24:25], 11
	v_lshl_add_u64 v[108:109], v[60:61], 0, s[0:1]
	v_fmac_f32_e32 v146, v133, v138
	v_mul_f32_e32 v107, v107, v110
	v_cvt_pk_bf16_f32 v107, v107, s0
	global_store_short v[108:109], v107, off
	v_mul_f32_e32 v107, v117, v104
	v_fmac_f32_e32 v107, v116, v105
	v_fmac_f32_e32 v107, v133, v103
	v_fmac_f32_e32 v107, v134, v102
	v_add_f32_e32 v105, v136, v107
	v_mul_f32_e32 v110, v117, v103
	v_mul_f32_e32 v107, 0xbfb8aa3b, v105
	v_fmac_f32_e32 v110, v116, v104
	v_exp_f32_e32 v107, v107
	v_fmac_f32_e32 v110, v133, v102
	v_fmac_f32_e32 v110, v134, v106
	v_add_f32_e32 v110, v136, v110
	v_mul_f32_e32 v104, 0xbfb8aa3b, v110
	v_add_f32_e32 v107, 1.0, v107
	v_exp_f32_e32 v104, v104
	v_rcp_f32_e32 v107, v107
	s_lshl_b64 s[0:1], s[26:27], 11
	v_lshl_add_u64 v[114:115], v[60:61], 0, s[0:1]
	v_add_f32_e32 v104, 1.0, v104
	v_mul_f32_e32 v105, v105, v107
	v_rcp_f32_e32 v107, v104
	v_cvt_pk_bf16_f32 v105, v105, s0
	s_lshl_b64 s[0:1], s[18:19], 11
	global_store_short v[114:115], v105, off
	v_mul_f32_e32 v107, v110, v107
	v_lshl_add_u64 v[104:105], v[60:61], 0, s[0:1]
	v_cvt_pk_bf16_f32 v107, v107, s0
	global_store_short v[104:105], v107, off
	v_mul_f32_e32 v107, v117, v102
	v_fmac_f32_e32 v107, v116, v103
	v_fmac_f32_e32 v107, v133, v106
	v_fmac_f32_e32 v107, v134, v138
	v_add_f32_e32 v103, v136, v107
	v_mul_f32_e32 v107, 0xbfb8aa3b, v103
	v_exp_f32_e32 v107, v107
	v_fmac_f32_e32 v146, v134, v140
	v_add_f32_e32 v146, v136, v146
	v_mul_f32_e32 v102, 0xbfb8aa3b, v146
	v_add_f32_e32 v107, 1.0, v107
	v_exp_f32_e32 v102, v102
	v_rcp_f32_e32 v107, v107
	s_lshl_b64 s[0:1], s[22:23], 11
	v_lshl_add_u64 v[110:111], v[60:61], 0, s[0:1]
	v_add_f32_e32 v102, 1.0, v102
	v_mul_f32_e32 v103, v103, v107
	v_rcp_f32_e32 v107, v102
	v_cvt_pk_bf16_f32 v103, v103, s0
	s_lshl_b64 s[0:1], s[92:93], 11
	global_store_short v[110:111], v103, off
	v_mul_f32_e32 v107, v146, v107
	v_lshl_add_u64 v[102:103], v[60:61], 0, s[0:1]
	v_cvt_pk_bf16_f32 v107, v107, s0
	global_store_short v[102:103], v107, off
	v_mul_f32_e32 v107, v117, v138
	v_fmac_f32_e32 v107, v116, v106
	v_mul_f32_e32 v117, v117, v140
	v_cndmask_b32_e64 v144, 0, v34, s[70:71]
	v_fmac_f32_e32 v107, v133, v140
	v_fmac_f32_e32 v117, v116, v138
	v_fmac_f32_e32 v107, v134, v144
	v_fmac_f32_e32 v117, v133, v144
	v_add_f32_e32 v146, v136, v107
	v_fmac_f32_e32 v117, v134, v145
	v_mul_f32_e32 v106, 0xbfb8aa3b, v146
	v_add_f32_e32 v133, v136, v117
	v_exp_f32_e32 v147, v106
	v_mul_f32_e32 v116, 0xbfb8aa3b, v133
	v_exp_f32_e32 v116, v116
	s_lshl_b64 s[0:1], s[94:95], 11
	v_add_f32_e32 v147, 1.0, v147
	v_rcp_f32_e32 v147, v147
	v_add_f32_e32 v116, 1.0, v116
	v_rcp_f32_e32 v134, v116
	v_lshl_add_u64 v[106:107], v[60:61], 0, s[0:1]
	v_mul_f32_e32 v117, v146, v147
	v_cvt_pk_bf16_f32 v117, v117, s0
	s_lshl_b64 s[0:1], s[90:91], 11
	v_mul_f32_e32 v133, v133, v134
	global_store_short v[106:107], v117, off
	v_lshl_add_u64 v[116:117], v[60:61], 0, s[0:1]
	v_cvt_pk_bf16_f32 v133, v133, s0
	global_load_dword v34, v[50:51], off offset:2048
	global_load_dword v79, v[58:59], off offset:2048
	s_nop 0
	global_store_short v[116:117], v133, off
	global_load_ushort v2, v[2:3], off offset:1024
	s_nop 0
	global_load_ushort v3, v[4:5], off offset:1024
	s_nop 0
	global_load_ushort v4, v[6:7], off offset:1024
	global_load_ushort v5, v[8:9], off offset:1024
	s_nop 0
	global_load_ushort v6, v[10:11], off offset:1024
	global_load_ushort v7, v[12:13], off offset:1024
	global_load_ushort v8, v[14:15], off offset:1024
	global_load_ushort v9, v[16:17], off offset:1024
	s_nop 0
	global_load_ushort v10, v[80:81], off offset:1024
	global_load_ushort v11, v[82:83], off offset:1024
	global_load_ushort v12, v[84:85], off offset:1024
	global_load_ushort v13, v[86:87], off offset:1024
	global_load_ushort v14, v[88:89], off offset:1024
	global_load_ushort v15, v[90:91], off offset:1024
	global_load_ushort v16, v[92:93], off offset:1024
	global_load_ushort v17, v[94:95], off offset:1024
	global_load_ushort v80, v[96:97], off offset:1024
	global_load_ushort v81, v[98:99], off offset:1024
	global_load_dword v82, v[62:63], off
	global_load_dword v83, v[64:65], off
	global_load_dword v84, v[66:67], off
	s_waitcnt vmcnt(39)
	v_lshlrev_b32_e32 v85, 16, v132
	v_cndmask_b32_e64 v85, 0, v85, s[4:5]
	s_waitcnt vmcnt(20)
	v_lshlrev_b32_e32 v2, 16, v2
	s_waitcnt vmcnt(19)
	v_lshlrev_b32_e32 v3, 16, v3
	v_cndmask_b32_e64 v3, 0, v3, s[2:3]
	v_cndmask_b32_e32 v2, 0, v2, vcc
	s_waitcnt vmcnt(18)
	v_lshlrev_b32_e32 v4, 16, v4
	v_cndmask_b32_e64 v4, 0, v4, s[40:41]
	s_waitcnt vmcnt(17)
	v_lshlrev_b32_e32 v5, 16, v5
	v_cndmask_b32_e64 v5, 0, v5, s[42:43]
	s_waitcnt vmcnt(16)
	v_lshlrev_b32_e32 v6, 16, v6
	v_cndmask_b32_e64 v6, 0, v6, s[44:45]
	s_waitcnt vmcnt(15)
	v_lshlrev_b32_e32 v7, 16, v7
	v_cndmask_b32_e64 v7, 0, v7, s[46:47]
	s_waitcnt vmcnt(14)
	v_lshlrev_b32_e32 v8, 16, v8
	v_cndmask_b32_e64 v8, 0, v8, s[48:49]
	s_waitcnt vmcnt(13)
	v_lshlrev_b32_e32 v9, 16, v9
	v_cndmask_b32_e64 v9, 0, v9, s[50:51]
	s_waitcnt vmcnt(12)
	v_lshlrev_b32_e32 v10, 16, v10
	v_cndmask_b32_e64 v10, 0, v10, s[52:53]
	s_waitcnt vmcnt(2)
	v_mul_f32_e32 v86, v82, v3
	v_fmac_f32_e32 v86, v34, v2
	s_waitcnt vmcnt(1)
	v_fmac_f32_e32 v86, v83, v85
	v_mul_f32_e32 v87, v82, v85
	s_waitcnt vmcnt(0)
	v_fmac_f32_e32 v86, v84, v4
	v_fmac_f32_e32 v87, v34, v3
	v_add_f32_e32 v2, v79, v86
	v_fmac_f32_e32 v87, v83, v4
	v_mul_f32_e32 v86, 0xbfb8aa3b, v2
	v_fmac_f32_e32 v87, v84, v5
	v_exp_f32_e32 v86, v86
	v_add_f32_e32 v3, v79, v87
	v_mul_f32_e32 v87, 0xbfb8aa3b, v3
	v_exp_f32_e32 v87, v87
	v_add_f32_e32 v86, 1.0, v86
	v_rcp_f32_e32 v86, v86
	v_lshlrev_b32_e32 v11, 16, v11
	v_add_f32_e32 v87, 1.0, v87
	v_rcp_f32_e32 v87, v87
	v_mul_f32_e32 v2, v2, v86
	v_cvt_pk_bf16_f32 v2, v2, s0
	global_store_short v[100:101], v2, off offset:1024
	v_mul_f32_e32 v2, v3, v87
	v_mul_f32_e32 v3, v82, v4
	v_fmac_f32_e32 v3, v34, v85
	v_fmac_f32_e32 v3, v83, v5
	v_fmac_f32_e32 v3, v84, v6
	v_add_f32_e32 v3, v79, v3
	v_mul_f32_e32 v85, 0xbfb8aa3b, v3
	v_exp_f32_e32 v85, v85
	v_mul_f32_e32 v86, v82, v5
	v_fmac_f32_e32 v86, v34, v4
	v_fmac_f32_e32 v86, v83, v6
	v_fmac_f32_e32 v86, v84, v7
	v_add_f32_e32 v85, 1.0, v85
	v_add_f32_e32 v4, v79, v86
	v_rcp_f32_e32 v85, v85
	v_mul_f32_e32 v86, 0xbfb8aa3b, v4
	v_exp_f32_e32 v86, v86
	v_cvt_pk_bf16_f32 v2, v2, s0
	v_mul_f32_e32 v3, v3, v85
	v_cvt_pk_bf16_f32 v3, v3, s0
	global_store_short v[126:127], v2, off offset:1024
	v_add_f32_e32 v2, 1.0, v86
	global_store_short v[130:131], v3, off offset:1024
	v_mul_f32_e32 v3, v82, v6
	v_rcp_f32_e32 v2, v2
	v_fmac_f32_e32 v3, v34, v5
	v_fmac_f32_e32 v3, v83, v7
	v_fmac_f32_e32 v3, v84, v8
	v_add_f32_e32 v3, v79, v3
	v_mul_f32_e32 v2, v4, v2
	v_mul_f32_e32 v4, 0xbfb8aa3b, v3
	v_exp_f32_e32 v4, v4
	v_mul_f32_e32 v5, v82, v7
	v_fmac_f32_e32 v5, v34, v6
	v_fmac_f32_e32 v5, v83, v8
	v_add_f32_e32 v4, 1.0, v4
	v_rcp_f32_e32 v4, v4
	v_fmac_f32_e32 v5, v84, v9
	v_add_f32_e32 v5, v79, v5
	v_mul_f32_e32 v6, 0xbfb8aa3b, v5
	v_mul_f32_e32 v3, v3, v4
	v_exp_f32_e32 v6, v6
	v_cvt_pk_bf16_f32 v3, v3, s0
	global_store_short v[128:129], v3, off offset:1024
	v_mul_f32_e32 v3, v82, v8
	v_fmac_f32_e32 v3, v34, v7
	v_cvt_pk_bf16_f32 v2, v2, s0
	v_fmac_f32_e32 v3, v83, v9
	global_store_short v[122:123], v2, off offset:1024
	v_add_f32_e32 v2, 1.0, v6
	v_fmac_f32_e32 v3, v84, v10
	v_rcp_f32_e32 v2, v2
	v_add_f32_e32 v3, v79, v3
	v_mul_f32_e32 v4, 0xbfb8aa3b, v3
	v_exp_f32_e32 v4, v4
	v_mul_f32_e32 v2, v5, v2
	v_mul_f32_e32 v5, v82, v9
	v_fmac_f32_e32 v5, v34, v8
	v_cndmask_b32_e64 v11, 0, v11, s[54:55]
	v_fmac_f32_e32 v5, v83, v10
	v_add_f32_e32 v4, 1.0, v4
	v_fmac_f32_e32 v5, v84, v11
	v_rcp_f32_e32 v4, v4
	v_add_f32_e32 v5, v79, v5
	v_mul_f32_e32 v6, 0xbfb8aa3b, v5
	v_exp_f32_e32 v6, v6
	v_mul_f32_e32 v3, v3, v4
	v_cvt_pk_bf16_f32 v3, v3, s0
	v_cvt_pk_bf16_f32 v2, v2, s0
	global_store_short v[124:125], v3, off offset:1024
	v_mul_f32_e32 v3, v82, v10
	v_lshlrev_b32_e32 v12, 16, v12
	global_store_short v[118:119], v2, off offset:1024
	v_add_f32_e32 v2, 1.0, v6
	v_fmac_f32_e32 v3, v34, v9
	v_cndmask_b32_e64 v12, 0, v12, s[56:57]
	v_rcp_f32_e32 v2, v2
	v_fmac_f32_e32 v3, v83, v11
	v_fmac_f32_e32 v3, v84, v12
	v_add_f32_e32 v3, v79, v3
	v_mul_f32_e32 v4, 0xbfb8aa3b, v3
	v_mul_f32_e32 v2, v5, v2
	v_exp_f32_e32 v4, v4
	v_mul_f32_e32 v5, v82, v11
	v_lshlrev_b32_e32 v13, 16, v13
	v_fmac_f32_e32 v5, v34, v10
	v_cndmask_b32_e64 v13, 0, v13, s[58:59]
	v_fmac_f32_e32 v5, v83, v12
	v_fmac_f32_e32 v5, v84, v13
	v_add_f32_e32 v5, v79, v5
	v_add_f32_e32 v4, 1.0, v4
	v_mul_f32_e32 v6, 0xbfb8aa3b, v5
	v_rcp_f32_e32 v4, v4
	v_exp_f32_e32 v6, v6
	v_cvt_pk_bf16_f32 v2, v2, s0
	global_store_short v[112:113], v2, off offset:1024
	v_mul_f32_e32 v3, v3, v4
	v_add_f32_e32 v2, 1.0, v6
	v_cvt_pk_bf16_f32 v3, v3, s0
	v_rcp_f32_e32 v2, v2
	global_store_short v[120:121], v3, off offset:1024
	v_mul_f32_e32 v3, v82, v12
	v_lshlrev_b32_e32 v14, 16, v14
	v_fmac_f32_e32 v3, v34, v11
	v_cndmask_b32_e64 v14, 0, v14, s[60:61]
	v_fmac_f32_e32 v3, v83, v13
	v_fmac_f32_e32 v3, v84, v14
	v_mul_f32_e32 v2, v5, v2
	v_add_f32_e32 v3, v79, v3
	v_mul_f32_e32 v5, v82, v13
	v_lshlrev_b32_e32 v15, 16, v15
	v_mul_f32_e32 v4, 0xbfb8aa3b, v3
	v_fmac_f32_e32 v5, v34, v12
	v_cndmask_b32_e64 v15, 0, v15, s[62:63]
	v_exp_f32_e32 v4, v4
	v_fmac_f32_e32 v5, v83, v14
	v_fmac_f32_e32 v5, v84, v15
	v_add_f32_e32 v5, v79, v5
	v_mul_f32_e32 v6, 0xbfb8aa3b, v5
	v_exp_f32_e32 v6, v6
	v_add_f32_e32 v4, 1.0, v4
	v_rcp_f32_e32 v4, v4
	v_cvt_pk_bf16_f32 v2, v2, s0
	global_store_short v[108:109], v2, off offset:1024
	v_add_f32_e32 v2, 1.0, v6
	v_rcp_f32_e32 v2, v2
	v_mul_f32_e32 v3, v3, v4
	v_cvt_pk_bf16_f32 v3, v3, s0
	global_store_short v[114:115], v3, off offset:1024
	v_mul_f32_e32 v3, v82, v14
	v_lshlrev_b32_e32 v16, 16, v16
	v_fmac_f32_e32 v3, v34, v13
	v_cndmask_b32_e64 v16, 0, v16, s[64:65]
	v_mul_f32_e32 v2, v5, v2
	v_fmac_f32_e32 v3, v83, v15
	v_mul_f32_e32 v5, v82, v15
	v_lshlrev_b32_e32 v17, 16, v17
	v_fmac_f32_e32 v3, v84, v16
	v_fmac_f32_e32 v5, v34, v14
	v_cndmask_b32_e64 v17, 0, v17, s[66:67]
	v_add_f32_e32 v3, v79, v3
	v_fmac_f32_e32 v5, v83, v16
	v_mul_f32_e32 v4, 0xbfb8aa3b, v3
	v_fmac_f32_e32 v5, v84, v17
	v_exp_f32_e32 v4, v4
	v_add_f32_e32 v5, v79, v5
	v_mul_f32_e32 v6, 0xbfb8aa3b, v5
	v_exp_f32_e32 v6, v6
	v_add_f32_e32 v4, 1.0, v4
	v_cvt_pk_bf16_f32 v2, v2, s0
	v_rcp_f32_e32 v4, v4
	global_store_short v[104:105], v2, off offset:1024
	v_add_f32_e32 v2, 1.0, v6
	v_rcp_f32_e32 v2, v2
	v_mul_f32_e32 v3, v3, v4
	v_cvt_pk_bf16_f32 v3, v3, s0
	v_lshlrev_b32_e32 v80, 16, v80
	global_store_short v[110:111], v3, off offset:1024
	v_mul_f32_e32 v2, v5, v2
	v_mul_f32_e32 v3, v82, v16
	v_mul_f32_e32 v5, v82, v17
	v_cndmask_b32_e64 v80, 0, v80, s[70:71]
	v_lshlrev_b32_e32 v81, 16, v81
	v_fmac_f32_e32 v3, v34, v15
	v_fmac_f32_e32 v5, v34, v16
	v_cndmask_b32_e64 v81, 0, v81, s[68:69]
	v_fmac_f32_e32 v3, v83, v17
	v_fmac_f32_e32 v5, v83, v80
	v_fmac_f32_e32 v3, v84, v80
	v_fmac_f32_e32 v5, v84, v81
	v_add_f32_e32 v3, v79, v3
	v_add_f32_e32 v5, v79, v5
	v_mul_f32_e32 v4, 0xbfb8aa3b, v3
	v_mul_f32_e32 v6, 0xbfb8aa3b, v5
	v_exp_f32_e32 v4, v4
	v_exp_f32_e32 v6, v6
	v_cvt_pk_bf16_f32 v2, v2, s0
	global_store_short v[102:103], v2, off offset:1024
	v_add_f32_e32 v4, 1.0, v4
	v_add_f32_e32 v2, 1.0, v6
	v_rcp_f32_e32 v4, v4
	v_rcp_f32_e32 v2, v2
	v_mul_f32_e32 v3, v3, v4
	v_mul_f32_e32 v2, v5, v2
	v_cvt_pk_bf16_f32 v3, v3, s0
	v_cvt_pk_bf16_f32 v2, v2, s0
	global_store_short v[106:107], v3, off offset:1024
	global_store_short v[116:117], v2, off offset:1024
	s_and_saveexec_b64 s[0:1], s[38:39]
	s_movk_i32 s90, 0x1a00
	s_cbranch_execz .LBB0_247
	v_readlane_b32 s2, v255, 48
	v_readlane_b32 s3, v255, 49
	v_add_u32_e32 v2, s88, v19
	v_mov_b32_e32 v79, v35
	v_mov_b64_e32 v[4:5], s[2:3]
	v_mad_i64_i32 v[4:5], s[2:3], v2, s90, v[4:5]
	v_lshl_add_u64 v[4:5], v[4:5], 0, v[78:79]
	v_add_co_u32_e32 v4, vcc, 0x1000, v4
	s_nop 1
	v_addc_co_u32_e32 v5, vcc, 0, v5, vcc
	global_load_ushort v3, v[4:5], off offset:2432
	s_nop 0
	global_load_dword v4, v[68:69], off
	s_waitcnt vmcnt(1)
	v_lshlrev_b32_e32 v3, 16, v3
	s_waitcnt vmcnt(0)
	v_add_f32_e32 v4, v4, v3
	v_mul_f32_e64 v3, |v4|, s97
	v_exp_f32_e32 v3, v3
	v_max_f32_e32 v4, 0, v4
	v_add_f32_e32 v3, 1.0, v3
	v_log_f32_e32 v5, v3
	v_ashrrev_i32_e32 v3, 31, v2
	v_lshlrev_b64 v[2:3], 6, v[2:3]
	v_lshl_add_u64 v[2:3], v[70:71], 0, v[2:3]
	v_fmac_f32_e32 v4, 0x3f317218, v5
	global_store_dword v[2:3], v4, off
	s_branch .LBB0_247

.LBB0_624:
	v_readlane_b32 s0, v255, 57
	s_movk_i32 s92, 0x2000
	v_readlane_b32 s1, v255, 58
	s_or_b64 exec, exec, s[0:1]
	v_readlane_b32 s0, v255, 50
	v_readlane_b32 s1, v255, 51
	s_and_b64 s[0:1], s[0:1], exec
	s_mov_b32 s0, 0xc000
	s_cselect_b32 s30, s0, 0x4ccc
	v_readlane_b32 s0, v253, 14
	v_readlane_b32 s4, v255, 52
	s_add_i32 s29, s4, s0
	s_lshl_b32 s0, s4, 14
	v_readlane_b32 s80, v255, 40
	s_add_i32 s28, s0, 0
	s_add_i32 s31, s29, 0x3c00
	v_readlane_b32 s81, v255, 41
	v_readlane_b32 s84, v255, 44
	v_readlane_b32 s85, v255, 45
	v_readlane_b32 s86, v255, 46
	v_readlane_b32 s87, v255, 47
	s_cmp_ge_i32 s31, s30
	v_readlane_b32 s82, v255, 42
	v_readlane_b32 s83, v255, 43
	s_waitcnt vmcnt(0) lgkmcnt(0)
	s_barrier
	s_cbranch_scc1 .LBB0_644
	s_mul_hi_i32 s0, s31, 0x2aaaaaab
	s_lshr_b32 s1, s0, 31
	s_ashr_i32 s0, s0, 8
	s_add_i32 s0, s0, s1
	s_mul_i32 s1, s0, 0x600
	s_sub_i32 s3, s31, s1
	s_cmpk_gt_i32 s3, 0x3ff
	s_mov_b64 s[8:9], -1
	s_cbranch_scc0 .LBB0_627
	v_readlane_b32 s4, v255, 37
	s_ashr_i32 s1, s0, 31
	v_readlane_b32 s5, v255, 38
	v_readlane_b32 s36, v252, 48
	s_lshl_b32 s2, s4, 27
	s_lshl_b64 s[4:5], s[0:1], 22
	v_readlane_b32 s40, v252, 52
	v_readlane_b32 s41, v252, 53
	s_add_u32 s1, s40, s4
	s_addc_u32 s5, s41, s5
	s_add_u32 s4, s1, s2
	s_addc_u32 s5, s5, 0
	s_lshl_b32 s1, s3, 1
	s_and_b32 s1, s1, 0x7fffffc0
	s_lshl_b32 s2, s3, 5
	v_readlane_b32 s37, v252, 49
	v_readlane_b32 s38, v252, 50
	v_readlane_b32 s39, v252, 51
	v_readlane_b32 s42, v252, 54
	v_readlane_b32 s43, v252, 55
	s_addk_i32 s1, 0xf800
	s_and_b32 s2, s2, 0x3e0
	s_mov_b64 s[8:9], 0

.LBB0_770:
	s_or_b64 exec, exec, s[0:1]
	v_readlane_b32 s0, v255, 50
	v_readlane_b32 s1, v255, 51
	s_and_b64 s[0:1], s[0:1], exec
	s_mov_b32 s0, 0xc000
	s_cselect_b32 s34, s0, 0x4ccc
	v_readlane_b32 s0, v253, 61
	v_readlane_b32 s1, v255, 52
	s_add_i32 s31, s1, s0
	s_lshl_b32 s0, s1, 14
	s_add_i32 s30, s0, 0
	s_add_i32 s35, s31, 0x3c00
	s_cmp_ge_i32 s35, s34
	s_cbranch_scc1 .LBB0_789
	s_mul_hi_i32 s0, s35, 0x2aaaaaab
	s_lshr_b32 s1, s0, 31
	s_ashr_i32 s0, s0, 8
	s_add_i32 s0, s0, s1
	s_mul_i32 s1, s0, 0x600
	s_sub_i32 s5, s35, s1
	s_cmpk_gt_i32 s5, 0x3ff
	s_mov_b64 s[10:11], -1
	s_cbranch_scc0 .LBB0_773
	s_ashr_i32 s1, s0, 31
	v_readlane_b32 s6, v255, 37
	v_readlane_b32 s36, v252, 48
	s_lshl_b32 s4, s6, 27
	s_lshl_b64 s[8:9], s[0:1], 22
	v_readlane_b32 s40, v252, 52
	v_readlane_b32 s41, v252, 53
	s_add_u32 s1, s40, s8
	s_addc_u32 s9, s41, s9
	s_add_u32 s8, s1, s4
	s_addc_u32 s9, s9, 0
	s_lshl_b32 s1, s5, 1
	s_and_b32 s1, s1, 0x7fffffc0
	s_lshl_b32 s4, s5, 5
	v_readlane_b32 s7, v255, 38
	v_readlane_b32 s37, v252, 49
	v_readlane_b32 s38, v252, 50
	v_readlane_b32 s39, v252, 51
	v_readlane_b32 s42, v252, 54
	v_readlane_b32 s43, v252, 55
	s_addk_i32 s1, 0xf800
	s_and_b32 s4, s4, 0x3e0
	s_mov_b64 s[10:11], 0

.LBB0_1012:
	s_waitcnt lgkmcnt(1)
	v_mul_f32_e32 v4, 0x3fb8aa3b, v6
	v_and_b32_e32 v2, 0xffff0000, v9
	v_exp_f32_e32 v4, v4
	v_mul_f32_e32 v2, 0x3e3504f3, v2
	v_mul_f32_e32 v2, v2, v5
	v_and_b32_e32 v3, 0xffff0000, v7
	v_cvt_pk_bf16_f32 v2, v2, s0
	ds_write_b16 v175, v2 offset:4286
	v_mul_f32_e32 v2, v4, v3
	v_cvt_pk_bf16_f32 v2, v2, s0
	ds_write_b16 v175, v2 offset:6846
	v_add_u32_e32 v2, s18, v132
	s_movk_i32 s0, 0xd00
	v_lshl_add_u64 v[4:5], s[10:11], 0, v[132:133]
	v_mul_lo_u32 v34, v2, s0
	v_lshlrev_b64 v[4:5], 9, v[4:5]
	v_lshl_add_u64 v[2:3], v[34:35], 1, v[140:141]
	v_lshl_add_u64 v[12:13], v[142:143], 0, v[4:5]
	global_load_dwordx4 v[6:9], v[2:3], off
	s_nop 0
	global_load_dwordx4 v[2:5], v[12:13], off offset:16
	s_nop 0
	global_load_dwordx4 v[12:15], v[12:13], off
	ds_read2_b32 v[16:17], v177 offset1:1
	v_add_u32_e32 v18, 0xffc, v176
	ds_read2_b32 v[20:21], v18 offset1:1
	v_mov_b32_e32 v157, v35
	v_mov_b32_e32 v159, v35
	v_mov_b32_e32 v161, v35
	s_movk_i32 s83, 0x110
	s_waitcnt vmcnt(0) lgkmcnt(1)
	v_sub_f32_e32 v12, v16, v12
	s_waitcnt lgkmcnt(0)
	v_sub_f32_e32 v12, v20, v12
	v_cndmask_b32_e64 v12, v12, v16, s[38:39]
	v_mul_f32_e32 v12, 0x3fb8aa3b, v12
	v_exp_f32_e32 v22, v12
	v_sub_f32_e32 v12, v17, v13
	v_sub_f32_e32 v12, v21, v12
	v_cndmask_b32_e64 v12, v12, v17, s[38:39]
	v_mul_f32_e32 v12, 0x3fb8aa3b, v12
	v_exp_f32_e32 v23, v12
	ds_read2_b32 v[12:13], v177 offset0:2 offset1:3
	v_add_u32_e32 v16, 0x1004, v176
	ds_read2_b32 v[32:33], v16 offset1:1
	s_waitcnt lgkmcnt(1)
	v_sub_f32_e32 v14, v12, v14
	s_waitcnt lgkmcnt(0)
	v_sub_f32_e32 v14, v32, v14
	v_cndmask_b32_e64 v12, v14, v12, s[38:39]
	v_mul_f32_e32 v12, 0x3fb8aa3b, v12
	v_exp_f32_e32 v24, v12
	v_sub_f32_e32 v12, v13, v15
	v_sub_f32_e32 v12, v33, v12
	v_cndmask_b32_e64 v12, v12, v13, s[38:39]
	v_mul_f32_e32 v12, 0x3fb8aa3b, v12
	v_exp_f32_e32 v25, v12
	ds_read2_b32 v[12:13], v177 offset0:4 offset1:5
	v_add_u32_e32 v14, 0x100c, v176
	ds_read2_b32 v[36:37], v14 offset1:1
	s_waitcnt lgkmcnt(1)
	v_sub_f32_e32 v2, v12, v2
	s_waitcnt lgkmcnt(0)
	v_sub_f32_e32 v2, v36, v2
	v_cndmask_b32_e64 v2, v2, v12, s[38:39]
	v_mul_f32_e32 v2, 0x3fb8aa3b, v2
	v_exp_f32_e32 v26, v2
	v_sub_f32_e32 v2, v13, v3
	v_sub_f32_e32 v2, v37, v2
	v_cndmask_b32_e64 v2, v2, v13, s[38:39]
	v_mul_f32_e32 v2, 0x3fb8aa3b, v2
	v_exp_f32_e32 v27, v2
	ds_read2_b32 v[2:3], v177 offset0:6 offset1:7
	v_add_u32_e32 v12, 0x1014, v176
	ds_read2_b32 v[38:39], v12 offset1:1
	s_waitcnt lgkmcnt(1)
	v_sub_f32_e32 v4, v2, v4
	s_waitcnt lgkmcnt(0)
	v_sub_f32_e32 v4, v38, v4
	v_cndmask_b32_e64 v2, v4, v2, s[38:39]
	v_mul_f32_e32 v2, 0x3fb8aa3b, v2
	v_exp_f32_e32 v28, v2
	v_sub_f32_e32 v2, v3, v5
	v_sub_f32_e32 v2, v39, v2
	v_cndmask_b32_e64 v2, v2, v3, s[38:39]
	v_mul_f32_e32 v2, 0x3fb8aa3b, v2
	v_exp_f32_e32 v29, v2
	v_add_u32_e32 v2, s18, v144
	v_lshl_add_u64 v[4:5], s[10:11], 0, v[144:145]
	v_mul_lo_u32 v34, v2, s0
	v_lshlrev_b64 v[4:5], 9, v[4:5]
	v_lshl_add_u64 v[2:3], v[34:35], 1, v[140:141]
	v_lshl_add_u64 v[16:17], v[142:143], 0, v[4:5]
	global_load_dwordx4 v[2:5], v[2:3], off
	s_nop 0
	global_load_dwordx4 v[12:15], v[16:17], off offset:16
	s_nop 0
	global_load_dwordx4 v[16:19], v[16:17], off
	ds_read2_b32 v[30:31], v178 offset1:1
	s_mov_b32 s0, 0
	s_mov_b32 s1, 1
	s_mov_b32 s85, s0
	v_lshl_add_u64 v[10:11], v[10:11], 0, s[84:85]
	v_lshl_add_u64 v[40:41], v[10:11], 0, v[156:157]
	s_waitcnt vmcnt(0) lgkmcnt(0)
	v_sub_f32_e32 v16, v30, v16
	v_sub_f32_e32 v16, v20, v16
	v_cndmask_b32_e64 v16, v16, v30, s[38:39]
	v_mul_f32_e32 v16, 0x3fb8aa3b, v16
	v_exp_f32_e32 v30, v16
	v_sub_f32_e32 v16, v31, v17
	v_sub_f32_e32 v16, v21, v16
	v_cndmask_b32_e64 v16, v16, v31, s[38:39]
	v_mul_f32_e32 v16, 0x3fb8aa3b, v16
	v_exp_f32_e32 v31, v16
	ds_read2_b32 v[16:17], v178 offset0:2 offset1:3
	s_waitcnt lgkmcnt(0)
	v_sub_f32_e32 v18, v16, v18
	v_sub_f32_e32 v18, v32, v18
	v_cndmask_b32_e64 v16, v18, v16, s[38:39]
	v_mul_f32_e32 v16, 0x3fb8aa3b, v16
	v_exp_f32_e32 v32, v16
	v_sub_f32_e32 v16, v17, v19
	v_sub_f32_e32 v16, v33, v16
	v_cndmask_b32_e64 v16, v16, v17, s[38:39]
	v_mul_f32_e32 v16, 0x3fb8aa3b, v16
	v_exp_f32_e32 v33, v16
	ds_read2_b32 v[16:17], v178 offset0:4 offset1:5
	s_waitcnt lgkmcnt(0)
	v_sub_f32_e32 v12, v16, v12
	v_sub_f32_e32 v12, v36, v12
	v_cndmask_b32_e64 v12, v12, v16, s[38:39]
	v_mul_f32_e32 v12, 0x3fb8aa3b, v12
	v_exp_f32_e32 v36, v12
	v_sub_f32_e32 v12, v17, v13
	v_sub_f32_e32 v12, v37, v12
	v_cndmask_b32_e64 v12, v12, v17, s[38:39]
	v_mul_f32_e32 v12, 0x3fb8aa3b, v12
	v_exp_f32_e32 v37, v12
	ds_read2_b32 v[12:13], v178 offset0:6 offset1:7
	s_waitcnt lgkmcnt(0)
	v_sub_f32_e32 v14, v12, v14
	v_sub_f32_e32 v14, v38, v14
	v_cndmask_b32_e64 v12, v14, v12, s[38:39]
	v_mul_f32_e32 v12, 0x3fb8aa3b, v12
	v_exp_f32_e32 v38, v12
	v_sub_f32_e32 v12, v13, v15
	v_sub_f32_e32 v12, v39, v12
	v_cndmask_b32_e64 v12, v12, v13, s[38:39]
	v_mul_f32_e32 v12, 0x3fb8aa3b, v12
	v_exp_f32_e32 v39, v12
	global_load_dwordx4 v[10:13], v[40:41], off offset:560
	global_load_dwordx4 v[14:17], v[40:41], off offset:544
	global_load_dwordx4 v[18:21], v[40:41], off offset:528
	s_nop 0
	global_load_dwordx4 v[40:43], v[40:41], off offset:512
	s_waitcnt vmcnt(0)
	v_lshlrev_b32_e32 v34, 16, v40
	v_and_b32_e32 v40, 0xffff0000, v40
	v_cvt_pk_bf16_f32 v34, v34, s0
	v_lshlrev_b32_e32 v44, 16, v41
	ds_write_b16 v228, v34 offset:9376
	v_cvt_pk_bf16_f32 v34, v40, s0
	v_and_b32_e32 v41, 0xffff0000, v41
	ds_write_b16 v228, v34 offset:9456
	v_cvt_pk_bf16_f32 v34, v44, s0
	ds_write_b16 v228, v34 offset:9536
	v_cvt_pk_bf16_f32 v34, v41, s0
	ds_write_b16 v228, v34 offset:9616
	v_lshlrev_b32_e32 v34, 16, v42
	v_and_b32_e32 v40, 0xffff0000, v42
	v_cvt_pk_bf16_f32 v34, v34, s0
	v_lshlrev_b32_e32 v41, 16, v43
	ds_write_b16 v228, v34 offset:9696
	v_cvt_pk_bf16_f32 v34, v40, s0
	v_and_b32_e32 v42, 0xffff0000, v43
	ds_write_b16 v228, v34 offset:9776
	v_cvt_pk_bf16_f32 v34, v41, s0
	ds_write_b16 v228, v34 offset:9856
	v_cvt_pk_bf16_f32 v34, v42, s0
	ds_write_b16 v228, v34 offset:9936
	v_lshlrev_b32_e32 v34, 16, v18
	v_and_b32_e32 v18, 0xffff0000, v18
	v_lshlrev_b32_e32 v40, 16, v19
	v_cvt_pk_bf16_f32 v18, v18, s0
	v_and_b32_e32 v19, 0xffff0000, v19
	ds_write_b16 v228, v18 offset:10096
	v_cvt_pk_bf16_f32 v18, v40, s0
	ds_write_b16 v228, v18 offset:10176
	v_cvt_pk_bf16_f32 v18, v19, s0
	ds_write_b16 v228, v18 offset:10256
	v_lshlrev_b32_e32 v18, 16, v20
	v_and_b32_e32 v19, 0xffff0000, v20
	v_cvt_pk_bf16_f32 v18, v18, s0
	v_lshlrev_b32_e32 v20, 16, v21
	ds_write_b16 v228, v18 offset:10336
	v_cvt_pk_bf16_f32 v18, v19, s0
	v_and_b32_e32 v21, 0xffff0000, v21
	ds_write_b16 v228, v18 offset:10416
	v_cvt_pk_bf16_f32 v18, v20, s0
	ds_write_b16 v228, v18 offset:10496
	v_cvt_pk_bf16_f32 v18, v21, s0
	ds_write_b16 v228, v18 offset:10576
	v_lshlrev_b32_e32 v18, 16, v14
	v_and_b32_e32 v14, 0xffff0000, v14
	v_lshlrev_b32_e32 v19, 16, v15
	v_cvt_pk_bf16_f32 v14, v14, s0
	v_and_b32_e32 v15, 0xffff0000, v15
	ds_write_b16 v228, v14 offset:10736
	v_cvt_pk_bf16_f32 v14, v19, s0
	ds_write_b16 v228, v14 offset:10816
	v_cvt_pk_bf16_f32 v14, v15, s0
	ds_write_b16 v228, v14 offset:10896
	v_lshlrev_b32_e32 v14, 16, v16
	v_and_b32_e32 v15, 0xffff0000, v16
	v_cvt_pk_bf16_f32 v14, v14, s0
	v_lshlrev_b32_e32 v16, 16, v17
	ds_write_b16 v228, v14 offset:10976
	v_cvt_pk_bf16_f32 v14, v15, s0
	v_and_b32_e32 v17, 0xffff0000, v17
	ds_write_b16 v228, v14 offset:11056
	v_cvt_pk_bf16_f32 v14, v16, s0
	ds_write_b16 v228, v14 offset:11136
	v_cvt_pk_bf16_f32 v14, v17, s0
	ds_write_b16 v228, v14 offset:11216
	v_lshlrev_b32_e32 v14, 16, v10
	v_and_b32_e32 v10, 0xffff0000, v10
	v_lshlrev_b32_e32 v15, 16, v11
	v_cvt_pk_bf16_f32 v10, v10, s0
	v_and_b32_e32 v11, 0xffff0000, v11
	ds_write_b16 v228, v10 offset:11376
	v_cvt_pk_bf16_f32 v10, v15, s0
	ds_write_b16 v228, v10 offset:11456
	v_cvt_pk_bf16_f32 v10, v11, s0
	ds_write_b16 v228, v10 offset:11536
	v_lshlrev_b32_e32 v10, 16, v12
	v_and_b32_e32 v11, 0xffff0000, v12
	v_cvt_pk_bf16_f32 v10, v10, s0
	v_lshlrev_b32_e32 v12, 16, v13
	ds_write_b16 v228, v10 offset:11616
	v_cvt_pk_bf16_f32 v10, v11, s0
	v_and_b32_e32 v13, 0xffff0000, v13
	ds_write_b16 v228, v10 offset:11696
	v_cvt_pk_bf16_f32 v10, v12, s0
	v_cvt_pk_bf16_f32 v34, v34, s0
	v_cvt_pk_bf16_f32 v18, v18, s0
	v_cvt_pk_bf16_f32 v14, v14, s0
	ds_write_b16 v228, v10 offset:11776
	v_cvt_pk_bf16_f32 v10, v13, s0
	ds_write_b16 v228, v34 offset:10016
	ds_write_b16 v228, v18 offset:10656
	ds_write_b16 v228, v14 offset:11296
	ds_write_b16 v229, v10 offset:9376
	s_waitcnt lgkmcnt(0)
	ds_read_b128 v[10:13], v180 offset:4256
	ds_read_b128 v[14:17], v180 offset:6816
	s_waitcnt lgkmcnt(0)
	v_mfma_f32_16x16x32_bf16 v[18:21], v[10:13], v[14:17], 0
	ds_read_b128 v[40:43], v180 offset:8096
	ds_read_b128 v[44:47], v180 offset:5536
	s_waitcnt lgkmcnt(0)
	s_nop 5
	v_cvt_pk_bf16_f32 v18, v18, s0
	v_cndmask_b32_e64 v18, 0, v18, s[42:43]
	s_waitcnt lgkmcnt(1)
	v_mfma_f32_16x16x32_bf16 v[10:13], v[10:13], v[40:43], 0
	ds_write_b16 v230, v18 offset:4256
	v_cvt_pk_bf16_f32 v18, v19, s0
	v_cndmask_b32_e64 v18, 0, v18, s[28:29]
	ds_write_b16 v231, v18 offset:4256
	v_cvt_pk_bf16_f32 v18, v20, s0
	v_cndmask_b32_e64 v18, 0, v18, s[30:31]
	ds_write_b16 v231, v18 offset:4336
	v_cvt_pk_bf16_f32 v18, v21, s0
	v_cvt_pk_bf16_f32 v10, v10, s0
	v_cndmask_b32_e64 v18, 0, v18, s[34:35]
	v_cndmask_b32_e64 v10, v10, 0, s[38:39]
	ds_write_b16 v231, v18 offset:4416
	ds_write_b16 v230, v10 offset:4288
	v_cvt_pk_bf16_f32 v10, v11, s0
	v_cndmask_b32_e64 v10, v10, 0, s[38:39]
	s_waitcnt lgkmcnt(5)
	v_mfma_f32_16x16x32_bf16 v[14:17], v[44:47], v[14:17], 0
	ds_write_b16 v231, v10 offset:4288
	v_cvt_pk_bf16_f32 v10, v12, s0
	v_cndmask_b32_e64 v10, v10, 0, s[38:39]
	ds_write_b16 v231, v10 offset:4368
	v_cvt_pk_bf16_f32 v10, v13, s0
	v_cndmask_b32_e64 v10, v10, 0, s[38:39]
	ds_write_b16 v231, v10 offset:4448
	s_nop 0
	v_cvt_pk_bf16_f32 v10, v14, s0
	v_cndmask_b32_e64 v10, 0, v10, s[38:39]
	ds_write_b16 v230, v10 offset:5536
	v_cvt_pk_bf16_f32 v10, v15, s0
	v_cndmask_b32_e64 v10, 0, v10, s[38:39]
	v_mfma_f32_16x16x32_bf16 v[40:43], v[44:47], v[40:43], 0
	ds_write_b16 v231, v10 offset:5536
	v_cvt_pk_bf16_f32 v10, v16, s0
	v_cndmask_b32_e64 v10, 0, v10, s[38:39]
	ds_write_b16 v231, v10 offset:5616
	v_cvt_pk_bf16_f32 v10, v17, s0
	v_cndmask_b32_e64 v10, 0, v10, s[38:39]
	ds_write_b16 v231, v10 offset:5696
	s_nop 0
	v_cvt_pk_bf16_f32 v10, v40, s0
	v_cndmask_b32_e64 v10, 0, v10, s[42:43]
	ds_write_b16 v230, v10 offset:5568
	v_cvt_pk_bf16_f32 v10, v41, s0
	v_cndmask_b32_e64 v10, 0, v10, s[36:37]
	ds_write_b16 v231, v10 offset:5568
	v_cvt_pk_bf16_f32 v10, v42, s0
	v_cndmask_b32_e64 v10, 0, v10, s[86:87]
	ds_write_b16 v231, v10 offset:5648
	v_cvt_pk_bf16_f32 v10, v43, s0
	v_cndmask_b32_e64 v12, 0, v10, s[88:89]
	v_lshlrev_b32_e32 v10, 16, v5
	v_and_b32_e32 v11, 0xffff0000, v5
	s_mov_b32 s0, 0x3e3504f3
	v_pk_mul_f32 v[10:11], v[10:11], s[0:1] op_sel_hi:[1,0]
	ds_write_b16 v231, v12 offset:5728
	v_pk_mul_f32 v[10:11], v[10:11], v[38:39]
	s_waitcnt lgkmcnt(0)
	s_nop 0
	v_cvt_pk_bf16_f32 v5, v10, v11
	v_lshlrev_b32_e32 v10, 16, v4
	v_and_b32_e32 v11, 0xffff0000, v4
	v_pk_mul_f32 v[10:11], v[10:11], s[0:1] op_sel_hi:[1,0]
	s_nop 0
	v_pk_mul_f32 v[10:11], v[10:11], v[36:37]
	s_nop 0
	v_cvt_pk_bf16_f32 v4, v10, v11
	v_lshlrev_b32_e32 v10, 16, v3
	v_and_b32_e32 v11, 0xffff0000, v3
	v_pk_mul_f32 v[10:11], v[10:11], s[0:1] op_sel_hi:[1,0]
	s_nop 0
	v_pk_mul_f32 v[10:11], v[10:11], v[32:33]
	s_nop 0
	v_cvt_pk_bf16_f32 v3, v10, v11
	v_lshlrev_b32_e32 v10, 16, v2
	v_and_b32_e32 v11, 0xffff0000, v2
	v_pk_mul_f32 v[10:11], v[10:11], s[0:1] op_sel_hi:[1,0]
	s_nop 0
	v_pk_mul_f32 v[10:11], v[10:11], v[30:31]
	s_nop 0
	v_cvt_pk_bf16_f32 v2, v10, v11
	v_lshlrev_b32_e32 v10, 16, v9
	v_and_b32_e32 v11, 0xffff0000, v9
	v_pk_mul_f32 v[10:11], v[10:11], s[0:1] op_sel_hi:[1,0]
	s_nop 0
	v_pk_mul_f32 v[10:11], v[10:11], v[28:29]
	s_nop 0
	v_cvt_pk_bf16_f32 v21, v10, v11
	v_lshlrev_b32_e32 v10, 16, v8
	v_and_b32_e32 v11, 0xffff0000, v8
	v_pk_mul_f32 v[8:9], v[10:11], s[0:1] op_sel_hi:[1,0]
	s_nop 0
	v_pk_mul_f32 v[8:9], v[8:9], v[26:27]
	s_nop 0
	v_cvt_pk_bf16_f32 v20, v8, v9
	v_lshlrev_b32_e32 v8, 16, v7
	v_and_b32_e32 v9, 0xffff0000, v7
	v_pk_mul_f32 v[8:9], v[8:9], s[0:1] op_sel_hi:[1,0]
	s_nop 0
	v_pk_mul_f32 v[8:9], v[8:9], v[24:25]
	s_nop 0
	v_cvt_pk_bf16_f32 v19, v8, v9
	v_lshlrev_b32_e32 v8, 16, v6
	v_and_b32_e32 v9, 0xffff0000, v6
	v_pk_mul_f32 v[6:7], v[8:9], s[0:1] op_sel_hi:[1,0]
	s_lshl_b32 s0, s14, 3
	s_add_i32 s0, s24, s0
	s_mul_hi_i32 s1, s0, 0x88
	s_mulk_i32 s0, 0x88
	s_add_u32 s0, s0, s15
	s_addc_u32 s1, s1, 0
	v_pk_mul_f32 v[6:7], v[6:7], v[22:23]
	s_lshl_b64 s[0:1], s[0:1], 12
	v_cvt_pk_bf16_f32 v18, v6, v7
	v_lshl_add_u64 v[6:7], v[146:147], 0, s[0:1]
	v_lshl_add_u64 v[30:31], v[6:7], 0, v[158:159]
	ds_read_b128 v[26:29], v180 offset:4256
	ds_read_b128 v[22:25], v181 offset:9376
	global_load_dwordx4 v[238:241], v[30:31], off
	global_load_dwordx4 v[246:249], v[30:31], off offset:2048
	global_load_dwordx4 v[38:41], v[30:31], off offset:3072
	v_lshl_add_u64 v[242:243], v[6:7], 0, v[160:161]
	global_load_dwordx4 v[242:245], v[242:243], off
	v_lshl_add_u64 v[8:9], s[10:11], 0, v[134:135]
	v_lshlrev_b64 v[16:17], 9, v[8:9]
	s_waitcnt lgkmcnt(0)
	v_mfma_f32_16x16x32_bf16 v[8:11], v[26:29], v[22:25], 0
	v_lshl_add_u64 v[32:33], v[148:149], 0, v[16:17]
	v_lshl_add_u64 v[36:37], v[6:7], 0, v[160:161]
	s_waitcnt vmcnt(0)
	v_mfma_f32_16x16x32_bf16 v[8:11], v[18:21], v[238:241], v[8:11]
	ds_read_b128 v[14:17], v181 offset:10656
	s_nop 6
	v_cvt_pk_bf16_f32 v8, v8, s0
	global_store_short v[32:33], v8, off
	v_cvt_pk_bf16_f32 v8, v9, s0
	global_store_short v[32:33], v8, off offset:512
	v_cvt_pk_bf16_f32 v8, v10, s0
	global_store_short v[32:33], v8, off offset:1024
	v_cvt_pk_bf16_f32 v8, v11, s0
	global_store_short v[32:33], v8, off offset:1536
	s_nop 0
	s_waitcnt lgkmcnt(0)
	v_mfma_f32_16x16x32_bf16 v[8:11], v[26:29], v[14:17], 0
	s_nop 0
	v_mfma_f32_16x16x32_bf16 v[6:9], v[18:21], v[242:245], v[8:11]
	s_nop 5
	ds_read_b128 v[10:13], v181 offset:11936
	s_nop 0
	v_cvt_pk_bf16_f32 v6, v6, s0
	global_store_short v[32:33], v6, off offset:32
	v_cvt_pk_bf16_f32 v6, v7, s0
	global_store_short v[32:33], v6, off offset:544
	v_cvt_pk_bf16_f32 v6, v8, s0
	global_store_short v[32:33], v6, off offset:1056
	v_cvt_pk_bf16_f32 v6, v9, s0
	global_store_short v[32:33], v6, off offset:1568
	s_nop 0
	s_waitcnt lgkmcnt(0)
	v_mfma_f32_16x16x32_bf16 v[6:9], v[26:29], v[10:13], 0
	s_nop 0
	v_mfma_f32_16x16x32_bf16 v[6:9], v[18:21], v[246:249], v[6:9]
	s_nop 7
	v_cvt_pk_bf16_f32 v6, v6, s0
	global_store_short v[32:33], v6, off offset:64
	v_cvt_pk_bf16_f32 v6, v7, s0
	global_store_short v[32:33], v6, off offset:576
	v_cvt_pk_bf16_f32 v6, v8, s0
	global_store_short v[32:33], v6, off offset:1088
	v_cvt_pk_bf16_f32 v6, v9, s0
	global_store_short v[32:33], v6, off offset:1600
	s_nop 0
	ds_read_b128 v[6:9], v181 offset:13216
	s_waitcnt lgkmcnt(0)
	v_mfma_f32_16x16x32_bf16 v[26:29], v[26:29], v[6:9], 0
	s_nop 0
	v_mfma_f32_16x16x32_bf16 v[18:21], v[18:21], v[38:41], v[26:29]
	s_nop 7
	v_cvt_pk_bf16_f32 v18, v18, s0
	global_store_short v[32:33], v18, off offset:96
	v_cvt_pk_bf16_f32 v18, v19, s0
	global_store_short v[32:33], v18, off offset:608
	v_cvt_pk_bf16_f32 v18, v20, s0
	global_store_short v[32:33], v18, off offset:1120
	v_cvt_pk_bf16_f32 v18, v21, s0
	global_store_short v[32:33], v18, off offset:1632
	s_nop 0
	ds_read_b128 v[18:21], v180 offset:5536
	s_waitcnt lgkmcnt(0)
	v_mfma_f32_16x16x32_bf16 v[22:25], v[18:21], v[22:25], 0
	s_nop 0
	v_mfma_f32_16x16x32_bf16 v[24:27], v[2:5], v[238:241], v[22:25]
	s_nop 5
	v_add_co_u32_e32 v22, vcc, s92, v32
	s_nop 0
	v_cvt_pk_bf16_f32 v24, v24, s0
	v_addc_co_u32_e32 v23, vcc, 0, v33, vcc
	global_store_short v[22:23], v24, off
	v_cvt_pk_bf16_f32 v24, v25, s0
	global_store_short v[22:23], v24, off offset:512
	v_cvt_pk_bf16_f32 v24, v26, s0
	global_store_short v[22:23], v24, off offset:1024
	v_cvt_pk_bf16_f32 v24, v27, s0
	global_store_short v[22:23], v24, off offset:1536
	s_nop 0
	v_mfma_f32_16x16x32_bf16 v[14:17], v[18:21], v[14:17], 0
	s_nop 0
	v_mfma_f32_16x16x32_bf16 v[14:17], v[2:5], v[242:245], v[14:17]
	s_nop 7
	v_cvt_pk_bf16_f32 v14, v14, s0
	global_store_short v[22:23], v14, off offset:32
	v_cvt_pk_bf16_f32 v14, v15, s0
	global_store_short v[22:23], v14, off offset:544
	v_cvt_pk_bf16_f32 v14, v16, s0
	global_store_short v[22:23], v14, off offset:1056
	v_cvt_pk_bf16_f32 v14, v17, s0
	global_store_short v[22:23], v14, off offset:1568
	s_nop 0
	v_mfma_f32_16x16x32_bf16 v[10:13], v[18:21], v[10:13], 0
	s_nop 0
	v_mfma_f32_16x16x32_bf16 v[10:13], v[2:5], v[246:249], v[10:13]
	s_nop 7
	v_cvt_pk_bf16_f32 v10, v10, s0
	global_store_short v[22:23], v10, off offset:64
	v_cvt_pk_bf16_f32 v10, v11, s0
	global_store_short v[22:23], v10, off offset:576
	v_cvt_pk_bf16_f32 v10, v12, s0
	global_store_short v[22:23], v10, off offset:1088
	v_cvt_pk_bf16_f32 v10, v13, s0
	global_store_short v[22:23], v10, off offset:1600
	s_nop 0
	v_mfma_f32_16x16x32_bf16 v[6:9], v[18:21], v[6:9], 0
	s_nop 0
	v_mfma_f32_16x16x32_bf16 v[2:5], v[2:5], v[38:41], v[6:9]
	s_nop 7
	v_cvt_pk_bf16_f32 v2, v2, s0
	global_store_short v[22:23], v2, off offset:96
	v_cvt_pk_bf16_f32 v2, v3, s0
	global_store_short v[22:23], v2, off offset:608
	v_cvt_pk_bf16_f32 v2, v4, s0
	global_store_short v[22:23], v2, off offset:1120
	v_cvt_pk_bf16_f32 v2, v5, s0
	global_store_short v[22:23], v2, off offset:1632
	s_waitcnt lgkmcnt(0)
	s_branch .LBB0_933

.LBB0_1233:
	s_lshl_b32 s4, s15, 4
	v_add_u32_e32 v62, s4, v7
	v_ashrrev_i32_e32 v63, 31, v62
	v_lshlrev_b64 v[2:3], 8, v[62:63]
	v_or_b32_e32 v4, v2, v6
	v_mov_b32_e32 v5, v3
	v_lshlrev_b64 v[4:5], 1, v[4:5]
	v_lshl_add_u64 v[2:3], v[2:3], 0, v[8:9]
	v_lshl_add_u64 v[44:45], s[38:39], 0, v[4:5]
	v_lshlrev_b64 v[2:3], 1, v[2:3]
	global_load_ushort v183, v[44:45], off
	v_lshl_add_u64 v[44:45], s[38:39], 0, v[2:3]
	global_load_ushort v163, v[44:45], off
	v_lshl_add_u64 v[44:45], s[40:41], 0, v[4:5]
	v_lshl_add_u64 v[4:5], s[6:7], 0, v[4:5]
	global_load_ushort v181, v[44:45], off
	global_load_ushort v170, v[4:5], off
	v_lshl_add_u64 v[44:45], s[40:41], 0, v[2:3]
	v_lshl_add_u64 v[2:3], s[6:7], 0, v[2:3]
	global_load_ushort v179, v[2:3], off
	v_lshlrev_b64 v[2:3], 9, v[62:63]
	v_lshl_add_u64 v[2:3], s[6:7], 0, v[2:3]
	v_lshlrev_b32_e32 v34, 1, v6
	global_load_ushort v169, v[44:45], off
	v_mad_i64_i32 v[44:45], s[2:3], v62, s90, v[36:37]
	v_lshl_add_u64 v[2:3], v[2:3], 0, v[34:35]
	v_add_co_u32_e64 v2, s[2:3], s24, v2
	v_or_b32_e32 v58, 1, v62
	s_nop 0
	v_addc_co_u32_e64 v3, s[2:3], 0, v3, s[2:3]
	v_ashrrev_i32_e32 v59, 31, v58
	global_load_ushort v184, v[44:45], off offset:1024
	global_load_ushort v171, v[2:3], off
	v_lshlrev_b64 v[2:3], 8, v[58:59]
	v_or_b32_e32 v4, v2, v6
	v_mov_b32_e32 v5, v3
	v_lshlrev_b64 v[4:5], 1, v[4:5]
	v_lshl_add_u64 v[2:3], v[2:3], 0, v[8:9]
	v_lshl_add_u64 v[44:45], s[38:39], 0, v[4:5]
	v_lshlrev_b64 v[2:3], 1, v[2:3]
	global_load_ushort v177, v[44:45], off
	v_lshl_add_u64 v[44:45], s[38:39], 0, v[2:3]
	global_load_ushort v172, v[44:45], off
	v_lshl_add_u64 v[44:45], s[40:41], 0, v[4:5]
	v_lshl_add_u64 v[4:5], s[6:7], 0, v[4:5]
	global_load_ushort v162, v[44:45], off
	global_load_ushort v174, v[4:5], off
	v_lshl_add_u64 v[44:45], s[40:41], 0, v[2:3]
	v_lshl_add_u64 v[2:3], s[6:7], 0, v[2:3]
	global_load_ushort v161, v[2:3], off
	v_lshlrev_b64 v[2:3], 9, v[58:59]
	v_lshl_add_u64 v[2:3], s[6:7], 0, v[2:3]
	global_load_ushort v173, v[44:45], off
	v_mad_i64_i32 v[44:45], s[2:3], v58, s90, v[36:37]
	v_lshl_add_u64 v[2:3], v[2:3], 0, v[34:35]
	v_add_co_u32_e64 v2, s[2:3], s24, v2
	v_or_b32_e32 v56, 2, v62
	s_nop 0
	v_addc_co_u32_e64 v3, s[2:3], 0, v3, s[2:3]
	v_ashrrev_i32_e32 v57, 31, v56
	global_load_ushort v178, v[44:45], off offset:1024
	global_load_ushort v175, v[2:3], off
	v_lshlrev_b64 v[2:3], 8, v[56:57]
	v_or_b32_e32 v4, v2, v6
	v_mov_b32_e32 v5, v3
	v_lshlrev_b64 v[4:5], 1, v[4:5]
	v_lshl_add_u64 v[2:3], v[2:3], 0, v[8:9]
	v_lshl_add_u64 v[44:45], s[38:39], 0, v[4:5]
	v_lshlrev_b64 v[2:3], 1, v[2:3]
	global_load_ushort v159, v[44:45], off
	v_lshl_add_u64 v[44:45], s[38:39], 0, v[2:3]
	global_load_ushort v176, v[44:45], off
	v_lshl_add_u64 v[44:45], s[40:41], 0, v[4:5]
	v_lshl_add_u64 v[4:5], s[6:7], 0, v[4:5]
	global_load_ushort v158, v[44:45], off
	global_load_ushort v182, v[4:5], off
	v_lshl_add_u64 v[44:45], s[40:41], 0, v[2:3]
	v_lshl_add_u64 v[2:3], s[6:7], 0, v[2:3]
	global_load_ushort v157, v[2:3], off
	v_lshlrev_b64 v[2:3], 9, v[56:57]
	v_lshl_add_u64 v[2:3], s[6:7], 0, v[2:3]
	global_load_ushort v180, v[44:45], off
	v_mad_i64_i32 v[44:45], s[2:3], v56, s90, v[36:37]
	v_lshl_add_u64 v[2:3], v[2:3], 0, v[34:35]
	v_add_co_u32_e64 v2, s[2:3], s24, v2
	v_or_b32_e32 v52, 3, v62
	s_nop 0
	v_addc_co_u32_e64 v3, s[2:3], 0, v3, s[2:3]
	v_ashrrev_i32_e32 v53, 31, v52
	global_load_ushort v160, v[44:45], off offset:1024
	global_load_ushort v185, v[2:3], off
	v_lshlrev_b64 v[2:3], 8, v[52:53]
	v_or_b32_e32 v4, v2, v6
	v_mov_b32_e32 v5, v3
	v_lshlrev_b64 v[4:5], 1, v[4:5]
	v_lshl_add_u64 v[2:3], v[2:3], 0, v[8:9]
	v_lshl_add_u64 v[44:45], s[38:39], 0, v[4:5]
	v_lshlrev_b64 v[2:3], 1, v[2:3]
	global_load_ushort v155, v[44:45], off
	v_lshl_add_u64 v[44:45], s[38:39], 0, v[2:3]
	global_load_ushort v186, v[44:45], off
	v_lshl_add_u64 v[44:45], s[40:41], 0, v[4:5]
	v_lshl_add_u64 v[4:5], s[6:7], 0, v[4:5]
	global_load_ushort v154, v[44:45], off
	global_load_ushort v188, v[4:5], off
	v_lshl_add_u64 v[44:45], s[40:41], 0, v[2:3]
	v_lshl_add_u64 v[2:3], s[6:7], 0, v[2:3]
	global_load_ushort v153, v[2:3], off
	v_lshlrev_b64 v[2:3], 9, v[52:53]
	v_lshl_add_u64 v[2:3], s[6:7], 0, v[2:3]
	global_load_ushort v187, v[44:45], off
	v_mad_i64_i32 v[44:45], s[2:3], v52, s90, v[36:37]
	v_lshl_add_u64 v[2:3], v[2:3], 0, v[34:35]
	v_add_co_u32_e64 v2, s[2:3], s24, v2
	v_or_b32_e32 v50, 4, v62
	s_nop 0
	v_addc_co_u32_e64 v3, s[2:3], 0, v3, s[2:3]
	v_ashrrev_i32_e32 v51, 31, v50
	global_load_ushort v156, v[44:45], off offset:1024
	global_load_ushort v189, v[2:3], off
	v_lshlrev_b64 v[2:3], 8, v[50:51]
	v_or_b32_e32 v4, v2, v6
	v_mov_b32_e32 v5, v3
	v_lshlrev_b64 v[4:5], 1, v[4:5]
	v_lshl_add_u64 v[2:3], v[2:3], 0, v[8:9]
	v_lshl_add_u64 v[44:45], s[38:39], 0, v[4:5]
	v_lshlrev_b64 v[2:3], 1, v[2:3]
	global_load_ushort v151, v[44:45], off
	v_lshl_add_u64 v[44:45], s[38:39], 0, v[2:3]
	global_load_ushort v190, v[44:45], off
	v_lshl_add_u64 v[44:45], s[40:41], 0, v[4:5]
	v_lshl_add_u64 v[4:5], s[6:7], 0, v[4:5]
	global_load_ushort v150, v[44:45], off
	global_load_ushort v192, v[4:5], off
	v_lshl_add_u64 v[44:45], s[40:41], 0, v[2:3]
	v_lshl_add_u64 v[2:3], s[6:7], 0, v[2:3]
	global_load_ushort v149, v[2:3], off
	v_lshlrev_b64 v[2:3], 9, v[50:51]
	v_lshl_add_u64 v[2:3], s[6:7], 0, v[2:3]
	global_load_ushort v191, v[44:45], off
	v_mad_i64_i32 v[44:45], s[2:3], v50, s90, v[36:37]
	v_lshl_add_u64 v[2:3], v[2:3], 0, v[34:35]
	v_add_co_u32_e64 v2, s[2:3], s24, v2
	v_or_b32_e32 v48, 5, v62
	s_nop 0
	v_addc_co_u32_e64 v3, s[2:3], 0, v3, s[2:3]
	v_ashrrev_i32_e32 v49, 31, v48
	global_load_ushort v152, v[44:45], off offset:1024
	global_load_ushort v193, v[2:3], off
	v_lshlrev_b64 v[2:3], 8, v[48:49]
	v_or_b32_e32 v4, v2, v6
	v_mov_b32_e32 v5, v3
	v_lshlrev_b64 v[4:5], 1, v[4:5]
	v_lshl_add_u64 v[2:3], v[2:3], 0, v[8:9]
	v_lshl_add_u64 v[44:45], s[38:39], 0, v[4:5]
	v_lshlrev_b64 v[2:3], 1, v[2:3]
	global_load_ushort v147, v[44:45], off
	v_lshl_add_u64 v[44:45], s[38:39], 0, v[2:3]
	global_load_ushort v210, v[44:45], off
	v_lshl_add_u64 v[44:45], s[40:41], 0, v[4:5]
	v_lshl_add_u64 v[4:5], s[6:7], 0, v[4:5]
	global_load_ushort v146, v[44:45], off
	global_load_ushort v212, v[4:5], off
	v_lshl_add_u64 v[44:45], s[40:41], 0, v[2:3]
	v_lshl_add_u64 v[2:3], s[6:7], 0, v[2:3]
	global_load_ushort v145, v[2:3], off
	v_lshlrev_b64 v[2:3], 9, v[48:49]
	v_lshl_add_u64 v[2:3], s[6:7], 0, v[2:3]
	global_load_ushort v211, v[44:45], off
	v_mad_i64_i32 v[44:45], s[2:3], v48, s90, v[36:37]
	v_lshl_add_u64 v[2:3], v[2:3], 0, v[34:35]
	v_add_co_u32_e64 v2, s[2:3], s24, v2
	v_or_b32_e32 v46, 6, v62
	s_nop 0
	v_addc_co_u32_e64 v3, s[2:3], 0, v3, s[2:3]
	v_ashrrev_i32_e32 v47, 31, v46
	global_load_ushort v148, v[44:45], off offset:1024
	global_load_ushort v213, v[2:3], off
	v_lshlrev_b64 v[2:3], 8, v[46:47]
	v_or_b32_e32 v4, v2, v6
	v_mov_b32_e32 v5, v3
	v_lshlrev_b64 v[4:5], 1, v[4:5]
	v_lshl_add_u64 v[2:3], v[2:3], 0, v[8:9]
	v_lshl_add_u64 v[44:45], s[38:39], 0, v[4:5]
	v_lshlrev_b64 v[2:3], 1, v[2:3]
	global_load_ushort v143, v[44:45], off
	v_lshl_add_u64 v[44:45], s[38:39], 0, v[2:3]
	global_load_ushort v214, v[44:45], off
	v_lshl_add_u64 v[44:45], s[40:41], 0, v[4:5]
	v_lshl_add_u64 v[4:5], s[6:7], 0, v[4:5]
	global_load_ushort v142, v[44:45], off
	global_load_ushort v216, v[4:5], off
	v_lshl_add_u64 v[44:45], s[40:41], 0, v[2:3]
	v_lshl_add_u64 v[2:3], s[6:7], 0, v[2:3]
	global_load_ushort v141, v[2:3], off
	v_lshlrev_b64 v[2:3], 9, v[46:47]
	v_lshl_add_u64 v[2:3], s[6:7], 0, v[2:3]
	global_load_ushort v215, v[44:45], off
	v_mad_i64_i32 v[44:45], s[2:3], v46, s90, v[36:37]
	v_lshl_add_u64 v[2:3], v[2:3], 0, v[34:35]
	v_add_co_u32_e64 v2, s[2:3], s24, v2
	global_load_ushort v144, v[44:45], off offset:1024
	s_nop 0
	v_addc_co_u32_e64 v3, s[2:3], 0, v3, s[2:3]
	global_load_ushort v217, v[2:3], off
	v_or_b32_e32 v44, 7, v62
	v_ashrrev_i32_e32 v45, 31, v44
	v_lshlrev_b64 v[2:3], 8, v[44:45]
	v_or_b32_e32 v4, v2, v6
	v_mov_b32_e32 v5, v3
	v_lshlrev_b64 v[4:5], 1, v[4:5]
	v_lshl_add_u64 v[2:3], v[2:3], 0, v[8:9]
	v_lshl_add_u64 v[54:55], s[38:39], 0, v[4:5]
	v_lshlrev_b64 v[2:3], 1, v[2:3]
	global_load_ushort v139, v[54:55], off
	v_lshl_add_u64 v[54:55], s[38:39], 0, v[2:3]
	global_load_ushort v218, v[54:55], off
	v_lshl_add_u64 v[54:55], s[40:41], 0, v[4:5]
	v_lshl_add_u64 v[4:5], s[6:7], 0, v[4:5]
	global_load_ushort v138, v[54:55], off
	global_load_ushort v220, v[4:5], off
	v_lshl_add_u64 v[54:55], s[40:41], 0, v[2:3]
	v_lshl_add_u64 v[2:3], s[6:7], 0, v[2:3]
	global_load_ushort v137, v[2:3], off
	v_lshlrev_b64 v[2:3], 9, v[44:45]
	v_lshl_add_u64 v[2:3], s[6:7], 0, v[2:3]
	global_load_ushort v219, v[54:55], off
	v_mad_i64_i32 v[54:55], s[2:3], v44, s90, v[36:37]
	v_lshl_add_u64 v[2:3], v[2:3], 0, v[34:35]
	s_cmpk_lt_i32 s15, 0x400
	s_mov_b32 s0, 0x7fffff00
	v_add_co_u32_e64 v2, s[2:3], s24, v2
	s_cselect_b32 s1, 0xffffffc0, s0
	s_nop 0
	v_addc_co_u32_e64 v3, s[2:3], 0, v3, s[2:3]
	s_cselect_b32 s18, 64, 0x100
	s_ashr_i32 s5, s4, 31
	s_and_b32 s1, s1, s4
	s_lshl_b64 s[2:3], s[4:5], 10
	s_add_u32 s2, s9, s2
	s_addc_u32 s3, s10, s3
	global_load_ushort v140, v[54:55], off offset:1024
	global_load_ushort v221, v[2:3], off
	v_lshl_add_u64 v[2:3], s[2:3], 0, v[10:11]
	global_load_ushort v135, v[2:3], off
	v_add_co_u32_e64 v2, s[2:3], s24, v2
	s_lshl_b64 s[42:43], s[4:5], 11
	s_nop 0
	v_addc_co_u32_e64 v3, s[2:3], 0, v3, s[2:3]
	global_load_ushort v222, v[2:3], off
	v_lshl_add_u64 v[2:3], v[12:13], 0, s[42:43]
	s_or_b32 s22, s4, 1
	global_load_ushort v136, v[2:3], off
	v_mad_i64_i32 v[2:3], s[2:3], s4, v202, v[38:39]
	s_ashr_i32 s23, s22, 31
	s_lshl_b64 s[2:3], s[22:23], 10
	s_add_u32 s2, s9, s2
	s_addc_u32 s3, s10, s3
	global_load_ushort v223, v[2:3], off offset:3456
	v_lshl_add_u64 v[2:3], s[2:3], 0, v[10:11]
	global_load_ushort v131, v[2:3], off
	v_add_co_u32_e64 v2, s[2:3], s24, v2
	s_lshl_b64 s[44:45], s[22:23], 11
	s_nop 0
	v_addc_co_u32_e64 v3, s[2:3], 0, v3, s[2:3]
	global_load_ushort v132, v[2:3], off
	v_lshl_add_u64 v[2:3], v[12:13], 0, s[44:45]
	global_load_ushort v133, v[2:3], off
	v_mad_i64_i32 v[2:3], s[2:3], s22, v202, v[38:39]
	s_or_b32 s22, s4, 2
	s_ashr_i32 s23, s22, 31
	s_lshl_b64 s[2:3], s[22:23], 10
	s_add_u32 s2, s9, s2
	s_addc_u32 s3, s10, s3
	global_load_ushort v134, v[2:3], off offset:3456
	v_lshl_add_u64 v[2:3], s[2:3], 0, v[10:11]
	global_load_ushort v127, v[2:3], off
	v_add_co_u32_e64 v2, s[2:3], s24, v2
	s_lshl_b64 s[46:47], s[22:23], 11
	s_nop 0
	v_addc_co_u32_e64 v3, s[2:3], 0, v3, s[2:3]
	global_load_ushort v128, v[2:3], off
	v_lshl_add_u64 v[2:3], v[12:13], 0, s[46:47]
	global_load_ushort v129, v[2:3], off
	v_mad_i64_i32 v[2:3], s[2:3], s22, v202, v[38:39]
	s_or_b32 s22, s4, 3
	s_ashr_i32 s23, s22, 31
	s_lshl_b64 s[2:3], s[22:23], 10
	s_add_u32 s2, s9, s2
	s_addc_u32 s3, s10, s3
	global_load_ushort v130, v[2:3], off offset:3456
	v_lshl_add_u64 v[2:3], s[2:3], 0, v[10:11]
	global_load_ushort v123, v[2:3], off
	v_add_co_u32_e64 v2, s[2:3], s24, v2
	s_lshl_b64 s[48:49], s[22:23], 11
	s_nop 0
	v_addc_co_u32_e64 v3, s[2:3], 0, v3, s[2:3]
	global_load_ushort v124, v[2:3], off
	v_lshl_add_u64 v[2:3], v[12:13], 0, s[48:49]
	global_load_ushort v125, v[2:3], off
	v_mad_i64_i32 v[2:3], s[2:3], s22, v202, v[38:39]
	s_or_b32 s22, s4, 4
	s_ashr_i32 s23, s22, 31
	s_lshl_b64 s[2:3], s[22:23], 10
	s_add_u32 s2, s9, s2
	s_addc_u32 s3, s10, s3
	global_load_ushort v126, v[2:3], off offset:3456
	v_lshl_add_u64 v[2:3], s[2:3], 0, v[10:11]
	global_load_ushort v119, v[2:3], off
	v_add_co_u32_e64 v2, s[2:3], s24, v2
	s_lshl_b64 s[50:51], s[22:23], 11
	s_nop 0
	v_addc_co_u32_e64 v3, s[2:3], 0, v3, s[2:3]
	global_load_ushort v120, v[2:3], off
	v_lshl_add_u64 v[2:3], v[12:13], 0, s[50:51]
	global_load_ushort v121, v[2:3], off
	v_mad_i64_i32 v[2:3], s[2:3], s22, v202, v[38:39]
	s_or_b32 s22, s4, 5
	s_ashr_i32 s23, s22, 31
	s_lshl_b64 s[2:3], s[22:23], 10
	s_add_u32 s2, s9, s2
	s_addc_u32 s3, s10, s3
	global_load_ushort v122, v[2:3], off offset:3456
	v_lshl_add_u64 v[2:3], s[2:3], 0, v[10:11]
	global_load_ushort v115, v[2:3], off
	v_add_co_u32_e64 v2, s[2:3], s24, v2
	s_lshl_b64 s[52:53], s[22:23], 11
	s_nop 0
	v_addc_co_u32_e64 v3, s[2:3], 0, v3, s[2:3]
	global_load_ushort v116, v[2:3], off
	v_lshl_add_u64 v[2:3], v[12:13], 0, s[52:53]
	global_load_ushort v117, v[2:3], off
	v_mad_i64_i32 v[2:3], s[2:3], s22, v202, v[38:39]
	s_or_b32 s22, s4, 6
	s_ashr_i32 s23, s22, 31
	s_lshl_b64 s[2:3], s[22:23], 10
	s_add_u32 s2, s9, s2
	s_addc_u32 s3, s10, s3
	global_load_ushort v118, v[2:3], off offset:3456
	v_lshl_add_u64 v[2:3], s[2:3], 0, v[10:11]
	global_load_ushort v111, v[2:3], off
	v_add_co_u32_e64 v2, s[2:3], s24, v2
	s_lshl_b64 s[54:55], s[22:23], 11
	s_nop 0
	v_addc_co_u32_e64 v3, s[2:3], 0, v3, s[2:3]
	global_load_ushort v112, v[2:3], off
	v_lshl_add_u64 v[2:3], v[12:13], 0, s[54:55]
	global_load_ushort v113, v[2:3], off
	v_mad_i64_i32 v[2:3], s[2:3], s22, v202, v[38:39]
	s_or_b32 s22, s4, 7
	s_ashr_i32 s23, s22, 31
	s_lshl_b64 s[2:3], s[22:23], 10
	s_add_u32 s2, s9, s2
	s_addc_u32 s3, s10, s3
	global_load_ushort v114, v[2:3], off offset:3456
	v_lshl_add_u64 v[2:3], s[2:3], 0, v[10:11]
	global_load_ushort v107, v[2:3], off
	v_add_co_u32_e64 v2, s[2:3], s24, v2
	s_lshl_b64 s[56:57], s[22:23], 11
	s_nop 0
	v_addc_co_u32_e64 v3, s[2:3], 0, v3, s[2:3]
	global_load_ushort v108, v[2:3], off
	v_lshl_add_u64 v[2:3], v[12:13], 0, s[56:57]
	global_load_ushort v109, v[2:3], off
	v_mad_i64_i32 v[2:3], s[2:3], s22, v202, v[38:39]
	s_or_b32 s22, s4, 8
	s_ashr_i32 s23, s22, 31
	s_lshl_b64 s[2:3], s[22:23], 10
	s_add_u32 s2, s9, s2
	s_addc_u32 s3, s10, s3
	global_load_ushort v110, v[2:3], off offset:3456
	v_lshl_add_u64 v[2:3], s[2:3], 0, v[10:11]
	global_load_ushort v103, v[2:3], off
	v_add_co_u32_e64 v2, s[2:3], s24, v2
	s_lshl_b64 s[58:59], s[22:23], 11
	s_nop 0
	v_addc_co_u32_e64 v3, s[2:3], 0, v3, s[2:3]
	global_load_ushort v104, v[2:3], off
	v_lshl_add_u64 v[2:3], v[12:13], 0, s[58:59]
	global_load_ushort v105, v[2:3], off
	v_mad_i64_i32 v[2:3], s[2:3], s22, v202, v[38:39]
	s_or_b32 s22, s4, 9
	s_ashr_i32 s23, s22, 31
	s_lshl_b64 s[2:3], s[22:23], 10
	s_add_u32 s2, s9, s2
	s_addc_u32 s3, s10, s3
	global_load_ushort v106, v[2:3], off offset:3456
	v_lshl_add_u64 v[2:3], s[2:3], 0, v[10:11]
	global_load_ushort v99, v[2:3], off
	v_add_co_u32_e64 v2, s[2:3], s24, v2
	s_lshl_b64 s[60:61], s[22:23], 11
	s_nop 0
	v_addc_co_u32_e64 v3, s[2:3], 0, v3, s[2:3]
	global_load_ushort v100, v[2:3], off
	v_lshl_add_u64 v[2:3], v[12:13], 0, s[60:61]
	global_load_ushort v101, v[2:3], off
	v_mad_i64_i32 v[2:3], s[2:3], s22, v202, v[38:39]
	s_or_b32 s22, s4, 10
	s_ashr_i32 s23, s22, 31
	s_lshl_b64 s[2:3], s[22:23], 10
	s_add_u32 s2, s9, s2
	s_addc_u32 s3, s10, s3
	global_load_ushort v102, v[2:3], off offset:3456
	v_lshl_add_u64 v[2:3], s[2:3], 0, v[10:11]
	global_load_ushort v95, v[2:3], off
	v_add_co_u32_e64 v2, s[2:3], s24, v2
	s_lshl_b64 s[62:63], s[22:23], 11
	s_nop 0
	v_addc_co_u32_e64 v3, s[2:3], 0, v3, s[2:3]
	global_load_ushort v96, v[2:3], off
	v_lshl_add_u64 v[2:3], v[12:13], 0, s[62:63]
	global_load_ushort v97, v[2:3], off
	v_mad_i64_i32 v[2:3], s[2:3], s22, v202, v[38:39]
	s_or_b32 s22, s4, 11
	s_ashr_i32 s23, s22, 31
	s_lshl_b64 s[2:3], s[22:23], 10
	s_add_u32 s2, s9, s2
	s_addc_u32 s3, s10, s3
	global_load_ushort v98, v[2:3], off offset:3456
	v_lshl_add_u64 v[2:3], s[2:3], 0, v[10:11]
	global_load_ushort v91, v[2:3], off
	v_add_co_u32_e64 v2, s[2:3], s24, v2
	s_lshl_b64 s[64:65], s[22:23], 11
	s_nop 0
	v_addc_co_u32_e64 v3, s[2:3], 0, v3, s[2:3]
	global_load_ushort v92, v[2:3], off
	v_lshl_add_u64 v[2:3], v[12:13], 0, s[64:65]
	global_load_ushort v93, v[2:3], off
	v_mad_i64_i32 v[2:3], s[2:3], s22, v202, v[38:39]
	s_or_b32 s22, s4, 12
	s_ashr_i32 s23, s22, 31
	s_lshl_b64 s[2:3], s[22:23], 10
	s_add_u32 s2, s9, s2
	s_addc_u32 s3, s10, s3
	global_load_ushort v94, v[2:3], off offset:3456
	v_lshl_add_u64 v[2:3], s[2:3], 0, v[10:11]
	global_load_ushort v87, v[2:3], off
	v_add_co_u32_e64 v2, s[2:3], s24, v2
	s_lshl_b64 s[66:67], s[22:23], 11
	s_nop 0
	v_addc_co_u32_e64 v3, s[2:3], 0, v3, s[2:3]
	global_load_ushort v88, v[2:3], off
	v_lshl_add_u64 v[2:3], v[12:13], 0, s[66:67]
	global_load_ushort v89, v[2:3], off
	v_mad_i64_i32 v[2:3], s[2:3], s22, v202, v[38:39]
	s_or_b32 s22, s4, 13
	s_ashr_i32 s23, s22, 31
	s_lshl_b64 s[2:3], s[22:23], 10
	s_add_u32 s2, s9, s2
	s_addc_u32 s3, s10, s3
	global_load_ushort v90, v[2:3], off offset:3456
	v_lshl_add_u64 v[2:3], s[2:3], 0, v[10:11]
	global_load_ushort v83, v[2:3], off
	v_add_co_u32_e64 v2, s[2:3], s24, v2
	s_lshl_b64 s[68:69], s[22:23], 11
	s_nop 0
	v_addc_co_u32_e64 v3, s[2:3], 0, v3, s[2:3]
	global_load_ushort v84, v[2:3], off
	v_lshl_add_u64 v[2:3], v[12:13], 0, s[68:69]
	global_load_ushort v85, v[2:3], off
	v_mad_i64_i32 v[2:3], s[2:3], s22, v202, v[38:39]
	s_or_b32 s22, s4, 14
	s_ashr_i32 s23, s22, 31
	s_lshl_b64 s[2:3], s[22:23], 10
	s_add_u32 s2, s9, s2
	s_addc_u32 s3, s10, s3
	global_load_ushort v86, v[2:3], off offset:3456
	v_lshl_add_u64 v[2:3], s[2:3], 0, v[10:11]
	global_load_ushort v79, v[2:3], off
	v_add_co_u32_e64 v2, s[2:3], s24, v2
	s_lshl_b64 s[70:71], s[22:23], 11
	s_nop 0
	v_addc_co_u32_e64 v3, s[2:3], 0, v3, s[2:3]
	global_load_ushort v80, v[2:3], off
	v_lshl_add_u64 v[2:3], v[12:13], 0, s[70:71]
	global_load_ushort v81, v[2:3], off
	v_mad_i64_i32 v[2:3], s[2:3], s22, v202, v[38:39]
	s_or_b32 s22, s4, 15
	s_ashr_i32 s23, s22, 31
	s_lshl_b64 s[2:3], s[22:23], 10
	s_add_u32 s2, s9, s2
	s_addc_u32 s3, s10, s3
	global_load_ushort v82, v[2:3], off offset:3456
	v_lshl_add_u64 v[2:3], s[2:3], 0, v[10:11]
	global_load_ushort v34, v[2:3], off
	v_add_co_u32_e64 v2, s[2:3], s24, v2
	s_lshl_b64 s[74:75], s[22:23], 11
	s_nop 0
	v_addc_co_u32_e64 v3, s[2:3], 0, v3, s[2:3]
	global_load_ushort v77, v[2:3], off
	v_lshl_add_u64 v[2:3], v[12:13], 0, s[74:75]
	global_load_ushort v76, v[2:3], off
	v_mad_i64_i32 v[2:3], s[2:3], s22, v202, v[38:39]
	global_load_ushort v78, v[2:3], off offset:3456
	v_add_u32_e32 v2, s4, v1
	s_add_i32 s2, s1, s18
	v_add_u32_e32 v3, 1, v2
	v_cmp_lt_i32_e64 s[4:5], s1, v2
	v_cmp_gt_i32_e64 s[2:3], s2, v3
	v_mad_i64_i32 v[2:3], s[18:19], v2, s90, v[40:41]
	global_load_ushort v54, v[2:3], off offset:3328
	global_load_ushort v194, v[2:3], off offset:3392
	global_load_dword v195, v[14:15], off offset:3456
	global_load_dword v196, v[16:17], off
	global_load_dword v197, v[14:15], off offset:3584
	global_load_dword v198, v[18:19], off
	v_mov_b32_e32 v204, 0xd00
	v_mov_b32_e32 v206, 0xfffff300
	v_cndmask_b32_e64 v204, v204, v206, s[4:5]
	v_cndmask_b32_e64 v205, 0, -1, s[4:5]
	v_lshl_add_u64 v[204:205], v[2:3], 0, v[204:205]
	global_load_ushort v199, v[204:205], off
	v_mov_b32_e32 v204, 0xd00
	v_mov_b32_e32 v206, 0x2700
	v_cndmask_b32_e64 v204, v204, v206, s[2:3]
	v_mov_b32_e32 v205, 0
	v_lshl_add_u64 v[204:205], v[2:3], 0, v[204:205]
	global_load_ushort v207, v[204:205], off
	v_mov_b32_e32 v204, 0xd40
	v_mov_b32_e32 v206, 0xfffff340
	v_cndmask_b32_e64 v204, v204, v206, s[4:5]
	v_cndmask_b32_e64 v205, 0, -1, s[4:5]
	v_lshl_add_u64 v[204:205], v[2:3], 0, v[204:205]
	global_load_ushort v208, v[204:205], off
	v_mov_b32_e32 v204, 0xd40
	v_mov_b32_e32 v206, 0x2740
	v_cndmask_b32_e64 v204, v204, v206, s[2:3]
	v_mov_b32_e32 v205, 0
	v_lshl_add_u64 v[204:205], v[2:3], 0, v[204:205]
	global_load_ushort v68, v[204:205], off
	v_mov_b32_e32 v66, 0
	s_mov_b32 s0, 0
	v_mov_b32_e32 v224, v73
	v_mov_b32_e32 v67, v66
	v_mov_b32_e32 v64, v66
	v_mov_b32_e32 v65, v66
	s_waitcnt vmcnt(0)
	v_lshlrev_b32_e32 v60, 16, v54
	v_lshlrev_b32_e32 v54, 16, v199
	v_cndmask_b32_e64 v61, 0, v54, s[4:5]
	v_sub_f32_e32 v54, v61, v60
	v_lshlrev_b32_e32 v4, 16, v207
	v_cndmask_b32_e64 v4, 0, v4, s[2:3]
	v_sub_f32_e32 v4, v4, v60
	v_fmac_f32_e32 v60, v195, v54
	v_fmac_f32_e32 v60, v196, v4
	v_mul_f32_e32 v4, 0xbfb8aa3b, v60
	v_exp_f32_e32 v4, v4
	v_lshlrev_b32_e32 v61, 16, v194
	v_add_f32_e32 v4, 1.0, v4
	v_rcp_f32_e32 v60, v4
	v_lshlrev_b32_e32 v54, 16, v208
	v_cndmask_b32_e64 v54, 0, v54, s[4:5]
	v_sub_f32_e32 v4, v54, v61
	v_lshlrev_b32_e32 v2, 16, v68
	v_cndmask_b32_e64 v2, 0, v2, s[2:3]
	v_sub_f32_e32 v2, v2, v61
	v_fmac_f32_e32 v61, v197, v4
	v_fmac_f32_e32 v61, v198, v2
	v_mul_f32_e32 v2, 0xbfb8aa3b, v61
	v_exp_f32_e32 v2, v2
	s_mov_b64 s[18:19], 0xd40
	s_movk_i32 s18, 0xf340
	s_mov_b32 s19, -1
	s_mov_b64 s[4:5], 0x2740
	v_add_f32_e32 v2, 1.0, v2
	v_rcp_f32_e32 v2, v2
	v_mov_b32_e32 v55, v66
	v_mov_b32_e32 v54, v66
	v_mov_b32_e32 v61, v66
	ds_write2_b32 v72, v60, v2 offset1:32
	s_waitcnt lgkmcnt(0)
	s_barrier
	v_mov_b32_e32 v60, v66

.LBB0_1325:
	s_lshl_b64 s[0:1], s[0:1], 2
	v_lshl_or_b32 v152, s8, 8, v169
	v_lshl_add_u32 v154, s52, 8, v162
	s_add_u32 s0, s46, s0
	s_addc_u32 s1, s47, s1
	v_ashrrev_i32_e32 v153, 31, v152
	v_ashrrev_i32_e32 v155, 31, v154
	v_lshl_add_u64 v[36:37], v[152:153], 2, s[0:1]
	s_mov_b64 s[0:1], 0x102000
	v_lshlrev_b64 v[156:157], 11, v[154:155]
	v_lshl_add_u64 v[40:41], v[36:37], 0, s[0:1]
	v_add_co_u32_e32 v36, vcc, s63, v36
	v_lshl_add_u64 v[176:177], s[40:41], 0, v[156:157]
	v_lshlrev_b64 v[156:157], 1, v[152:153]
	v_addc_co_u32_e32 v37, vcc, 0, v37, vcc
	v_lshl_add_u64 v[152:153], v[176:177], 0, v[156:157]
	global_load_dwordx4 v[72:75], v[36:37], off
	global_load_dwordx4 v[68:71], v[40:41], off offset:16
	s_nop 0
	global_load_dwordx4 v[36:39], v[40:41], off offset:528
	s_nop 0
	global_load_dwordx4 v[40:43], v[40:41], off offset:512
	s_mov_b32 s8, s42
	s_mov_b32 s52, s51
	s_mov_b64 s[10:11], s[44:45]
	v_or_b32_e32 v180, 16, v154
	v_ashrrev_i32_e32 v181, 31, v180
	v_lshlrev_b64 v[180:181], 11, v[180:181]
	v_lshl_add_u64 v[180:181], s[40:41], 0, v[180:181]
	v_lshl_add_u64 v[180:181], v[180:181], 0, v[156:157]
	v_or_b32_e32 v182, 32, v154
	v_ashrrev_i32_e32 v183, 31, v182
	v_lshlrev_b64 v[182:183], 11, v[182:183]
	v_lshl_add_u64 v[182:183], s[40:41], 0, v[182:183]
	v_lshl_add_u64 v[182:183], v[182:183], 0, v[156:157]
	v_or_b32_e32 v184, 48, v154
	v_ashrrev_i32_e32 v185, 31, v184
	v_lshlrev_b64 v[184:185], 11, v[184:185]
	v_lshl_add_u64 v[184:185], s[40:41], 0, v[184:185]
	v_lshl_add_u64 v[184:185], v[184:185], 0, v[156:157]
	v_lshl_add_u64 v[186:187], v[152:153], 0, s[64:65]
	v_lshl_add_u64 v[188:189], v[152:153], 0, s[66:67]
	v_lshl_add_u64 v[190:191], v[152:153], 0, s[68:69]
	v_lshl_add_u64 v[192:193], v[152:153], 0, s[70:71]
	global_load_dwordx4 v[176:179], v[152:153], off
	global_load_dwordx4 v[194:197], v[152:153], off offset:256
	global_load_dwordx4 v[204:207], v[180:181], off
	global_load_dwordx4 v[208:211], v[180:181], off offset:256
	global_load_dwordx4 v[212:215], v[182:183], off
	global_load_dwordx4 v[216:219], v[182:183], off offset:256
	global_load_dwordx4 v[220:223], v[184:185], off
	global_load_dwordx4 v[224:227], v[184:185], off offset:256
	global_load_dwordx4 v[228:231], v[186:187], off
	global_load_dwordx4 v[232:235], v[186:187], off offset:256
	global_load_dwordx4 v[236:239], v[188:189], off
	s_waitcnt vmcnt(10)
	v_lshlrev_b32_e32 v198, 16, v176
	v_and_b32_e32 v199, 0xffff0000, v176
	v_lshlrev_b32_e32 v176, 16, v177
	v_and_b32_e32 v177, 0xffff0000, v177
	v_pk_fma_f32 v[146:147], v[146:147], v[74:75], v[176:177]
	v_lshlrev_b32_e32 v176, 16, v178
	v_and_b32_e32 v177, 0xffff0000, v178
	v_lshlrev_b32_e32 v178, 16, v179
	v_and_b32_e32 v179, 0xffff0000, v179
	v_pk_fma_f32 v[144:145], v[144:145], v[72:73], v[198:199]
	v_pk_fma_f32 v[178:179], v[142:143], v[70:71], v[178:179]
	v_pk_fma_f32 v[142:143], v[140:141], v[68:69], v[176:177]
	v_cvt_pk_bf16_f32 v140, v144, v145
	v_cvt_pk_bf16_f32 v141, v146, v147
	v_cvt_pk_bf16_f32 v142, v142, v143
	v_cvt_pk_bf16_f32 v143, v178, v179
	global_store_dwordx4 v[152:153], v[140:143], off
	global_load_dwordx4 v[176:179], v[188:189], off offset:256
	s_waitcnt vmcnt(11)
	v_lshlrev_b32_e32 v198, 16, v194
	v_and_b32_e32 v199, 0xffff0000, v194
	v_lshlrev_b32_e32 v194, 16, v195
	v_and_b32_e32 v195, 0xffff0000, v195
	v_pk_fma_f32 v[138:139], v[138:139], v[42:43], v[194:195]
	v_lshlrev_b32_e32 v194, 16, v196
	v_and_b32_e32 v195, 0xffff0000, v196
	v_lshlrev_b32_e32 v196, 16, v197
	v_and_b32_e32 v197, 0xffff0000, v197
	v_pk_fma_f32 v[136:137], v[136:137], v[40:41], v[198:199]
	v_pk_fma_f32 v[196:197], v[134:135], v[38:39], v[196:197]
	v_pk_fma_f32 v[134:135], v[132:133], v[36:37], v[194:195]
	v_cvt_pk_bf16_f32 v132, v136, v137
	v_cvt_pk_bf16_f32 v133, v138, v139
	v_cvt_pk_bf16_f32 v134, v134, v135
	v_cvt_pk_bf16_f32 v135, v196, v197
	global_store_dwordx4 v[152:153], v[132:135], off offset:256
	global_load_dwordx4 v[194:197], v[190:191], off
	s_waitcnt vmcnt(12)
	v_lshlrev_b32_e32 v198, 16, v204
	v_and_b32_e32 v199, 0xffff0000, v204
	v_lshlrev_b32_e32 v204, 16, v205
	v_and_b32_e32 v205, 0xffff0000, v205
	v_pk_fma_f32 v[130:131], v[130:131], v[74:75], v[204:205]
	v_lshlrev_b32_e32 v204, 16, v206
	v_and_b32_e32 v205, 0xffff0000, v206
	v_lshlrev_b32_e32 v206, 16, v207
	v_and_b32_e32 v207, 0xffff0000, v207
	v_pk_fma_f32 v[128:129], v[128:129], v[72:73], v[198:199]
	v_pk_fma_f32 v[206:207], v[126:127], v[70:71], v[206:207]
	v_pk_fma_f32 v[126:127], v[124:125], v[68:69], v[204:205]
	v_cvt_pk_bf16_f32 v124, v128, v129
	v_cvt_pk_bf16_f32 v125, v130, v131
	v_cvt_pk_bf16_f32 v126, v126, v127
	v_cvt_pk_bf16_f32 v127, v206, v207
	global_store_dwordx4 v[180:181], v[124:127], off
	global_load_dwordx4 v[204:207], v[190:191], off offset:256
	s_waitcnt vmcnt(13)
	v_lshlrev_b32_e32 v198, 16, v208
	v_and_b32_e32 v199, 0xffff0000, v208
	v_lshlrev_b32_e32 v208, 16, v209
	v_and_b32_e32 v209, 0xffff0000, v209
	v_pk_fma_f32 v[122:123], v[122:123], v[42:43], v[208:209]
	v_lshlrev_b32_e32 v208, 16, v210
	v_and_b32_e32 v209, 0xffff0000, v210
	v_lshlrev_b32_e32 v210, 16, v211
	v_and_b32_e32 v211, 0xffff0000, v211
	v_pk_fma_f32 v[120:121], v[120:121], v[40:41], v[198:199]
	v_pk_fma_f32 v[210:211], v[118:119], v[38:39], v[210:211]
	v_pk_fma_f32 v[118:119], v[116:117], v[36:37], v[208:209]
	v_cvt_pk_bf16_f32 v116, v120, v121
	v_cvt_pk_bf16_f32 v117, v122, v123
	v_cvt_pk_bf16_f32 v118, v118, v119
	v_cvt_pk_bf16_f32 v119, v210, v211
	global_store_dwordx4 v[180:181], v[116:119], off offset:256
	global_load_dwordx4 v[208:211], v[192:193], off
	s_waitcnt vmcnt(14)
	v_lshlrev_b32_e32 v198, 16, v212
	v_and_b32_e32 v199, 0xffff0000, v212
	v_lshlrev_b32_e32 v212, 16, v213
	v_and_b32_e32 v213, 0xffff0000, v213
	v_pk_fma_f32 v[114:115], v[114:115], v[74:75], v[212:213]
	v_lshlrev_b32_e32 v212, 16, v214
	v_and_b32_e32 v213, 0xffff0000, v214
	v_lshlrev_b32_e32 v214, 16, v215
	v_and_b32_e32 v215, 0xffff0000, v215
	v_pk_fma_f32 v[112:113], v[112:113], v[72:73], v[198:199]
	v_pk_fma_f32 v[214:215], v[110:111], v[70:71], v[214:215]
	v_pk_fma_f32 v[110:111], v[108:109], v[68:69], v[212:213]
	v_cvt_pk_bf16_f32 v108, v112, v113
	v_cvt_pk_bf16_f32 v109, v114, v115
	v_cvt_pk_bf16_f32 v110, v110, v111
	v_cvt_pk_bf16_f32 v111, v214, v215
	global_store_dwordx4 v[182:183], v[108:111], off
	global_load_dwordx4 v[212:215], v[192:193], off offset:256
	s_waitcnt vmcnt(15)
	v_lshlrev_b32_e32 v198, 16, v216
	v_and_b32_e32 v199, 0xffff0000, v216
	v_lshlrev_b32_e32 v216, 16, v217
	v_and_b32_e32 v217, 0xffff0000, v217
	v_pk_fma_f32 v[106:107], v[106:107], v[42:43], v[216:217]
	v_lshlrev_b32_e32 v216, 16, v218
	v_and_b32_e32 v217, 0xffff0000, v218
	v_lshlrev_b32_e32 v218, 16, v219
	v_and_b32_e32 v219, 0xffff0000, v219
	v_pk_fma_f32 v[104:105], v[104:105], v[40:41], v[198:199]
	v_pk_fma_f32 v[218:219], v[102:103], v[38:39], v[218:219]
	v_pk_fma_f32 v[102:103], v[100:101], v[36:37], v[216:217]
	v_cvt_pk_bf16_f32 v100, v104, v105
	v_cvt_pk_bf16_f32 v101, v106, v107
	v_cvt_pk_bf16_f32 v102, v102, v103
	v_cvt_pk_bf16_f32 v103, v218, v219
	global_store_dwordx4 v[182:183], v[100:103], off offset:256
	s_waitcnt vmcnt(15)
	v_lshlrev_b32_e32 v198, 16, v220
	v_and_b32_e32 v199, 0xffff0000, v220
	v_lshlrev_b32_e32 v220, 16, v221
	v_and_b32_e32 v221, 0xffff0000, v221
	v_pk_fma_f32 v[98:99], v[98:99], v[74:75], v[220:221]
	v_lshlrev_b32_e32 v220, 16, v222
	v_and_b32_e32 v221, 0xffff0000, v222
	v_lshlrev_b32_e32 v222, 16, v223
	v_and_b32_e32 v223, 0xffff0000, v223
	v_pk_fma_f32 v[96:97], v[96:97], v[72:73], v[198:199]
	v_pk_fma_f32 v[222:223], v[94:95], v[70:71], v[222:223]
	v_pk_fma_f32 v[94:95], v[92:93], v[68:69], v[220:221]
	v_cvt_pk_bf16_f32 v92, v96, v97
	v_cvt_pk_bf16_f32 v93, v98, v99
	v_cvt_pk_bf16_f32 v94, v94, v95
	v_cvt_pk_bf16_f32 v95, v222, v223
	global_store_dwordx4 v[184:185], v[92:95], off
	s_waitcnt vmcnt(15)
	v_lshlrev_b32_e32 v198, 16, v224
	v_and_b32_e32 v199, 0xffff0000, v224
	v_lshlrev_b32_e32 v224, 16, v225
	v_and_b32_e32 v225, 0xffff0000, v225
	v_pk_fma_f32 v[90:91], v[90:91], v[42:43], v[224:225]
	v_lshlrev_b32_e32 v224, 16, v226
	v_and_b32_e32 v225, 0xffff0000, v226
	v_lshlrev_b32_e32 v226, 16, v227
	v_and_b32_e32 v227, 0xffff0000, v227
	v_pk_fma_f32 v[88:89], v[88:89], v[40:41], v[198:199]
	v_pk_fma_f32 v[226:227], v[86:87], v[38:39], v[226:227]
	v_pk_fma_f32 v[86:87], v[84:85], v[36:37], v[224:225]
	v_cvt_pk_bf16_f32 v84, v88, v89
	v_cvt_pk_bf16_f32 v85, v90, v91
	v_cvt_pk_bf16_f32 v86, v86, v87
	v_cvt_pk_bf16_f32 v87, v226, v227
	global_store_dwordx4 v[184:185], v[84:87], off offset:256
	s_waitcnt vmcnt(15)
	v_lshlrev_b32_e32 v198, 16, v228
	v_and_b32_e32 v199, 0xffff0000, v228
	v_lshlrev_b32_e32 v228, 16, v229
	v_and_b32_e32 v229, 0xffff0000, v229
	v_pk_fma_f32 v[82:83], v[82:83], v[74:75], v[228:229]
	v_lshlrev_b32_e32 v228, 16, v230
	v_and_b32_e32 v229, 0xffff0000, v230
	v_lshlrev_b32_e32 v230, 16, v231
	v_and_b32_e32 v231, 0xffff0000, v231
	v_pk_fma_f32 v[80:81], v[80:81], v[72:73], v[198:199]
	v_pk_fma_f32 v[230:231], v[78:79], v[70:71], v[230:231]
	v_pk_fma_f32 v[78:79], v[76:77], v[68:69], v[228:229]
	v_cvt_pk_bf16_f32 v76, v80, v81
	v_cvt_pk_bf16_f32 v77, v82, v83
	v_cvt_pk_bf16_f32 v78, v78, v79
	v_cvt_pk_bf16_f32 v79, v230, v231
	global_store_dwordx4 v[186:187], v[76:79], off
	s_waitcnt vmcnt(15)
	v_lshlrev_b32_e32 v198, 16, v232
	v_and_b32_e32 v199, 0xffff0000, v232
	v_lshlrev_b32_e32 v232, 16, v233
	v_and_b32_e32 v233, 0xffff0000, v233
	v_pk_fma_f32 v[66:67], v[66:67], v[42:43], v[232:233]
	v_lshlrev_b32_e32 v232, 16, v234
	v_and_b32_e32 v233, 0xffff0000, v234
	v_lshlrev_b32_e32 v234, 16, v235
	v_and_b32_e32 v235, 0xffff0000, v235
	v_pk_fma_f32 v[64:65], v[64:65], v[40:41], v[198:199]
	v_pk_fma_f32 v[234:235], v[62:63], v[38:39], v[234:235]
	v_pk_fma_f32 v[62:63], v[60:61], v[36:37], v[232:233]
	v_cvt_pk_bf16_f32 v60, v64, v65
	v_cvt_pk_bf16_f32 v61, v66, v67
	v_cvt_pk_bf16_f32 v62, v62, v63
	v_cvt_pk_bf16_f32 v63, v234, v235
	global_store_dwordx4 v[186:187], v[60:63], off offset:256
	s_waitcnt vmcnt(15)
	v_lshlrev_b32_e32 v198, 16, v236
	v_and_b32_e32 v199, 0xffff0000, v236
	v_lshlrev_b32_e32 v236, 16, v237
	v_and_b32_e32 v237, 0xffff0000, v237
	v_pk_fma_f32 v[58:59], v[58:59], v[74:75], v[236:237]
	v_lshlrev_b32_e32 v236, 16, v238
	v_and_b32_e32 v237, 0xffff0000, v238
	v_lshlrev_b32_e32 v238, 16, v239
	v_and_b32_e32 v239, 0xffff0000, v239
	v_pk_fma_f32 v[56:57], v[56:57], v[72:73], v[198:199]
	v_pk_fma_f32 v[238:239], v[54:55], v[70:71], v[238:239]
	v_pk_fma_f32 v[54:55], v[52:53], v[68:69], v[236:237]
	v_cvt_pk_bf16_f32 v52, v56, v57
	v_cvt_pk_bf16_f32 v53, v58, v59
	v_cvt_pk_bf16_f32 v54, v54, v55
	v_cvt_pk_bf16_f32 v55, v238, v239
	global_store_dwordx4 v[188:189], v[52:55], off
	s_waitcnt vmcnt(14)
	v_lshlrev_b32_e32 v198, 16, v176
	v_and_b32_e32 v199, 0xffff0000, v176
	v_lshlrev_b32_e32 v176, 16, v177
	v_and_b32_e32 v177, 0xffff0000, v177
	v_pk_fma_f32 v[50:51], v[50:51], v[42:43], v[176:177]
	v_lshlrev_b32_e32 v176, 16, v178
	v_and_b32_e32 v177, 0xffff0000, v178
	v_lshlrev_b32_e32 v178, 16, v179
	v_and_b32_e32 v179, 0xffff0000, v179
	v_pk_fma_f32 v[48:49], v[48:49], v[40:41], v[198:199]
	v_pk_fma_f32 v[178:179], v[46:47], v[38:39], v[178:179]
	v_pk_fma_f32 v[46:47], v[44:45], v[36:37], v[176:177]
	v_cvt_pk_bf16_f32 v44, v48, v49
	v_cvt_pk_bf16_f32 v45, v50, v51
	v_cvt_pk_bf16_f32 v46, v46, v47
	v_cvt_pk_bf16_f32 v47, v178, v179
	global_store_dwordx4 v[188:189], v[44:47], off offset:256
	s_waitcnt vmcnt(13)
	v_lshlrev_b32_e32 v198, 16, v194
	v_and_b32_e32 v199, 0xffff0000, v194
	v_lshlrev_b32_e32 v194, 16, v195
	v_and_b32_e32 v195, 0xffff0000, v195
	v_pk_fma_f32 v[32:33], v[32:33], v[74:75], v[194:195]
	v_lshlrev_b32_e32 v194, 16, v196
	v_and_b32_e32 v195, 0xffff0000, v196
	v_lshlrev_b32_e32 v196, 16, v197
	v_and_b32_e32 v197, 0xffff0000, v197
	v_pk_fma_f32 v[30:31], v[30:31], v[72:73], v[198:199]
	v_pk_fma_f32 v[196:197], v[28:29], v[70:71], v[196:197]
	v_pk_fma_f32 v[28:29], v[26:27], v[68:69], v[194:195]
	v_cvt_pk_bf16_f32 v26, v30, v31
	v_cvt_pk_bf16_f32 v27, v32, v33
	v_cvt_pk_bf16_f32 v28, v28, v29
	v_cvt_pk_bf16_f32 v29, v196, v197
	global_store_dwordx4 v[190:191], v[26:29], off
	s_waitcnt vmcnt(12)
	v_lshlrev_b32_e32 v198, 16, v204
	v_and_b32_e32 v199, 0xffff0000, v204
	v_lshlrev_b32_e32 v204, 16, v205
	v_and_b32_e32 v205, 0xffff0000, v205
	v_pk_fma_f32 v[24:25], v[24:25], v[42:43], v[204:205]
	v_lshlrev_b32_e32 v204, 16, v206
	v_and_b32_e32 v205, 0xffff0000, v206
	v_lshlrev_b32_e32 v206, 16, v207
	v_and_b32_e32 v207, 0xffff0000, v207
	v_pk_fma_f32 v[22:23], v[22:23], v[40:41], v[198:199]
	v_pk_fma_f32 v[206:207], v[20:21], v[38:39], v[206:207]
	v_pk_fma_f32 v[20:21], v[18:19], v[36:37], v[204:205]
	v_cvt_pk_bf16_f32 v18, v22, v23
	v_cvt_pk_bf16_f32 v19, v24, v25
	v_cvt_pk_bf16_f32 v20, v20, v21
	v_cvt_pk_bf16_f32 v21, v206, v207
	global_store_dwordx4 v[190:191], v[18:21], off offset:256
	s_waitcnt vmcnt(11)
	v_lshlrev_b32_e32 v198, 16, v208
	v_and_b32_e32 v199, 0xffff0000, v208
	v_lshlrev_b32_e32 v208, 16, v209
	v_and_b32_e32 v209, 0xffff0000, v209
	v_pk_fma_f32 v[16:17], v[16:17], v[74:75], v[208:209]
	v_lshlrev_b32_e32 v208, 16, v210
	v_and_b32_e32 v209, 0xffff0000, v210
	v_lshlrev_b32_e32 v210, 16, v211
	v_and_b32_e32 v211, 0xffff0000, v211
	v_pk_fma_f32 v[14:15], v[14:15], v[72:73], v[198:199]
	v_pk_fma_f32 v[210:211], v[12:13], v[70:71], v[210:211]
	v_pk_fma_f32 v[12:13], v[10:11], v[68:69], v[208:209]
	v_cvt_pk_bf16_f32 v10, v14, v15
	v_cvt_pk_bf16_f32 v11, v16, v17
	v_cvt_pk_bf16_f32 v12, v12, v13
	v_cvt_pk_bf16_f32 v13, v210, v211
	global_store_dwordx4 v[192:193], v[10:13], off
	s_waitcnt vmcnt(10)
	v_lshlrev_b32_e32 v198, 16, v212
	v_and_b32_e32 v199, 0xffff0000, v212
	v_lshlrev_b32_e32 v212, 16, v213
	v_and_b32_e32 v213, 0xffff0000, v213
	v_pk_fma_f32 v[8:9], v[8:9], v[42:43], v[212:213]
	v_lshlrev_b32_e32 v212, 16, v214
	v_and_b32_e32 v213, 0xffff0000, v214
	v_lshlrev_b32_e32 v214, 16, v215
	v_and_b32_e32 v215, 0xffff0000, v215
	v_pk_fma_f32 v[6:7], v[6:7], v[40:41], v[198:199]
	v_pk_fma_f32 v[214:215], v[4:5], v[38:39], v[214:215]
	v_pk_fma_f32 v[4:5], v[2:3], v[36:37], v[212:213]
	v_cvt_pk_bf16_f32 v2, v6, v7
	v_cvt_pk_bf16_f32 v3, v8, v9
	v_cvt_pk_bf16_f32 v4, v4, v5
	v_cvt_pk_bf16_f32 v5, v214, v215
	global_store_dwordx4 v[192:193], v[2:5], off offset:256
	s_and_b64 vcc, exec, s[38:39]
	v_mov_b32_e32 v42, v174
	v_mov_b32_e32 v40, v173
	v_mov_b32_e32 v38, v172
	v_mov_b32_e32 v36, v171
	s_cbranch_vccnz .LBB0_1335

.LBB0_1418:
	s_ashr_i32 s11, s10, 31
	s_lshl_b64 s[2:3], s[10:11], 11
	v_lshl_add_u64 v[2:3], v[18:19], 0, s[2:3]
	global_load_dwordx2 v[4:5], v[2:3], off
	s_waitcnt lgkmcnt(1)
	global_load_dwordx2 v[8:9], v[2:3], off offset:512
	global_load_dwordx2 v[28:29], v[2:3], off offset:1024
	s_lshr_b32 s2, s11, 20
	global_load_dwordx2 v[2:3], v[2:3], off offset:1536
	s_add_i32 s2, s10, s2
	s_ashr_i32 s2, s2, 12
	s_cmpk_lt_i32 s10, 0x4000
	s_cselect_b32 s2, s2, 4
	s_mul_hi_i32 s3, s2, 0x6000
	s_mulk_i32 s2, 0x6000
	s_add_u32 s2, s1, s2
	s_addc_u32 s3, s8, s3
	s_add_u32 s4, s2, 0x3000
	s_addc_u32 s5, s3, 0
	s_add_u32 s2, s2, 0x4000
	s_addc_u32 s3, s3, 0
	s_lshl_b64 s[6:7], s[10:11], 10
	s_waitcnt vmcnt(1)
	v_lshlrev_b32_e32 v30, 16, v28
	v_and_b32_e32 v31, 0xffff0000, v28
	s_waitcnt vmcnt(0) lgkmcnt(0)
	v_lshlrev_b32_e32 v10, 16, v2
	v_and_b32_e32 v17, 0xffff0000, v2
	v_lshlrev_b32_e32 v12, 16, v3
	v_and_b32_e32 v13, 0xffff0000, v3
	v_lshlrev_b32_e32 v3, 16, v5
	v_lshlrev_b32_e32 v2, 16, v4
	v_and_b32_e32 v5, 0xffff0000, v5
	v_and_b32_e32 v4, 0xffff0000, v4
	v_pk_mul_f32 v[6:7], v[4:5], v[4:5]
	v_mul_f32_e32 v11, v30, v30
	v_pk_fma_f32 v[6:7], v[2:3], v[2:3], v[6:7]
	v_mul_f32_e32 v117, v31, v31
	v_pk_add_f32 v[36:37], v[6:7], v[6:7] op_sel_hi:[0,1]
	v_lshlrev_b32_e32 v7, 16, v9
	v_lshlrev_b32_e32 v6, 16, v8
	v_and_b32_e32 v9, 0xffff0000, v9
	v_and_b32_e32 v8, 0xffff0000, v8
	v_pk_mul_f32 v[32:33], v[8:9], v[8:9]
	v_mov_b32_e32 v116, v10
	v_pk_fma_f32 v[32:33], v[6:7], v[6:7], v[32:33]
	v_pk_add_f32 v[116:117], v[10:11], v[116:117]
	v_pk_add_f32 v[114:115], v[32:33], v[32:33] op_sel_hi:[0,1]
	v_lshlrev_b32_e32 v32, 16, v29
	v_and_b32_e32 v33, 0xffff0000, v29
	v_mul_f32_e32 v28, v32, v32
	v_pk_fma_f32 v[28:29], v[32:33], v[32:33], v[28:29] op_sel_hi:[1,1,0]
	v_mul_f32_e32 v36, v12, v12
	v_mul_f32_e32 v28, v17, v17
	v_mul_f32_e32 v114, v13, v13
	v_mul_f32_e32 v118, v10, v10
	v_mov_b32_e32 v119, v117
	v_pk_add_f32 v[28:29], v[118:119], v[28:29]
	v_pk_add_f32 v[36:37], v[36:37], v[114:115]
	global_load_dwordx4 v[114:117], v[22:23], off
	global_load_dwordx4 v[118:121], v21, s[4:5]
	global_load_dwordx4 v[122:125], v21, s[2:3]
	v_pk_add_f32 v[28:29], v[28:29], v[36:37]
	v_mov_b32_e32 v36, v3
	v_add_f32_e32 v11, v28, v29
	s_nop 1
	v_mov_b32_dpp v27, v11 quad_perm:[1,0,3,2] row_mask:0xf bank_mask:0xf
	v_mov_b32_e32 v3, v4
	v_mov_b32_e32 v37, v5
	v_mov_b32_e32 v126, v7
	v_mov_b32_e32 v127, v9
	s_waitcnt lgkmcnt(0)
	v_add_f32_e32 v11, v11, v27
	s_nop 1
	v_mov_b32_dpp v27, v11 quad_perm:[2,3,0,1] row_mask:0xf bank_mask:0xf
	v_mov_b32_e32 v7, v8
	s_waitcnt lgkmcnt(0)
	v_add_f32_e32 v11, v11, v27
	s_nop 1
	v_mov_b32_dpp v27, v11 row_half_mirror row_mask:0xf bank_mask:0xf
	s_waitcnt lgkmcnt(0)
	v_add_f32_e32 v11, v11, v27
	s_nop 1
	v_mov_b32_dpp v27, v11 row_mirror row_mask:0xf bank_mask:0xf
	s_waitcnt lgkmcnt(0)
	v_add_f32_e32 v11, v11, v27
	v_mov_b32_e32 v27, v11
	s_nop 1
	v_permlane16_swap_b32_e32 v27, v11
	s_waitcnt lgkmcnt(0)
	v_add_f32_e32 v11, v11, v27
	v_mov_b32_e32 v27, v11
	s_nop 1
	v_permlane32_swap_b32_e32 v27, v11
	s_waitcnt lgkmcnt(0)
	v_add_f32_e32 v11, v11, v27
	v_fmamk_f32 v11, v11, 0x3a800000, v165
	v_rsq_f32_e32 v28, v11
	s_nop 0
	v_pk_mul_f32 v[2:3], v[2:3], v[28:29] op_sel_hi:[1,0]
	v_pk_mul_f32 v[36:37], v[36:37], v[28:29] op_sel_hi:[1,0]
	s_waitcnt vmcnt(2)
	v_pk_mul_f32 v[2:3], v[114:115], v[2:3]
	v_pk_mul_f32 v[4:5], v[116:117], v[36:37]
	s_waitcnt vmcnt(0)
	v_pk_add_f32 v[114:115], v[122:123], 1.0 op_sel_hi:[1,0]
	v_pk_add_f32 v[36:37], v[124:125], 1.0 op_sel_hi:[1,0]
	v_pk_fma_f32 v[2:3], v[114:115], v[2:3], v[118:119]
	v_mov_b32_e32 v114, v35
	v_med3_f32 v11, v2, s13, v200
	v_med3_f32 v27, v3, s13, v200
	v_cvt_pk_fp8_f32 v114, v11, v27
	v_pk_fma_f32 v[4:5], v[36:37], v[4:5], v[120:121]
	s_nop 0
	v_med3_f32 v29, v4, s13, v200
	v_med3_f32 v36, v5, s13, v200
	v_cvt_pk_fp8_f32 v114, v29, v36 op_sel:[0,0,1]
	v_lshl_add_u64 v[36:37], v[24:25], 0, s[6:7]
	v_pk_mul_f32 v[126:127], v[126:127], v[28:29] op_sel_hi:[1,0]
	v_pk_mul_f32 v[6:7], v[6:7], v[28:29] op_sel_hi:[1,0]
	global_store_dword v[36:37], v114, off
	global_load_dwordx4 v[114:117], v[22:23], off offset:1024
	s_nop 0
	global_load_dwordx4 v[118:121], v34, s[4:5]
	global_load_dwordx4 v[122:125], v34, s[2:3]
	s_add_i32 s6, s10, 1
	s_ashr_i32 s7, s6, 31
	s_waitcnt vmcnt(2)
	v_pk_mul_f32 v[6:7], v[114:115], v[6:7]
	v_pk_mul_f32 v[8:9], v[116:117], v[126:127]
	s_waitcnt vmcnt(0)
	v_pk_add_f32 v[116:117], v[122:123], 1.0 op_sel_hi:[1,0]
	v_pk_add_f32 v[114:115], v[124:125], 1.0 op_sel_hi:[1,0]
	v_pk_fma_f32 v[6:7], v[116:117], v[6:7], v[118:119]
	v_pk_fma_f32 v[8:9], v[114:115], v[8:9], v[120:121]
	v_med3_f32 v11, v6, s13, v200
	v_med3_f32 v27, v7, s13, v200
	v_mov_b32_e32 v115, v35
	v_cvt_pk_fp8_f32 v115, v11, v27
	v_med3_f32 v29, v8, s13, v200
	v_med3_f32 v114, v9, s13, v200
	v_pk_mul_f32 v[32:33], v[32:33], v[28:29] op_sel_hi:[1,0]
	v_cvt_pk_fp8_f32 v115, v29, v114 op_sel:[0,0,1]
	v_pk_mul_f32 v[30:31], v[30:31], v[28:29] op_sel_hi:[1,0]
	global_store_dword v[36:37], v115, off offset:256
	global_load_dwordx4 v[114:117], v[22:23], off offset:2048
	s_nop 0
	global_load_dwordx4 v[118:121], v109, s[4:5]
	global_load_dwordx4 v[122:125], v109, s[2:3]
	s_waitcnt vmcnt(2)
	v_pk_mul_f32 v[30:31], v[30:31], v[114:115]
	v_pk_mul_f32 v[32:33], v[32:33], v[116:117]
	s_waitcnt vmcnt(0)
	v_pk_add_f32 v[116:117], v[122:123], 1.0 op_sel_hi:[1,0]
	v_pk_add_f32 v[114:115], v[124:125], 1.0 op_sel_hi:[1,0]
	v_pk_fma_f32 v[30:31], v[30:31], v[116:117], v[118:119]
	v_pk_fma_f32 v[32:33], v[32:33], v[114:115], v[120:121]
	v_med3_f32 v11, v30, s13, v200
	v_med3_f32 v27, v31, s13, v200
	v_mov_b32_e32 v115, v35
	v_cvt_pk_fp8_f32 v115, v11, v27
	v_med3_f32 v29, v32, s13, v200
	v_med3_f32 v114, v33, s13, v200
	v_mov_b32_e32 v11, v17
	v_cvt_pk_fp8_f32 v115, v29, v114 op_sel:[0,0,1]
	v_pk_mul_f32 v[10:11], v[10:11], v[28:29] op_sel_hi:[1,0]
	v_pk_mul_f32 v[12:13], v[12:13], v[28:29] op_sel_hi:[1,0]
	global_store_dword v[36:37], v115, off offset:512
	global_load_dwordx4 v[114:117], v[22:23], off offset:3072
	s_nop 0
	global_load_dwordx4 v[118:121], v110, s[4:5]
	global_load_dwordx4 v[122:125], v110, s[2:3]
	s_lshl_b64 s[2:3], s[6:7], 11
	s_waitcnt vmcnt(2)
	v_pk_mul_f32 v[10:11], v[10:11], v[114:115]
	v_pk_mul_f32 v[12:13], v[12:13], v[116:117]
	s_waitcnt vmcnt(0)
	v_pk_add_f32 v[114:115], v[122:123], 1.0 op_sel_hi:[1,0]
	v_pk_add_f32 v[28:29], v[124:125], 1.0 op_sel_hi:[1,0]
	v_pk_fma_f32 v[10:11], v[10:11], v[114:115], v[118:119]
	v_mov_b32_e32 v114, v35
	v_med3_f32 v17, v10, s13, v200
	v_med3_f32 v27, v11, s13, v200
	v_cvt_pk_fp8_f32 v114, v17, v27
	v_pk_fma_f32 v[12:13], v[12:13], v[28:29], v[120:121]
	v_add_u32_e32 v17, s9, v20
	v_med3_f32 v28, v12, s13, v200
	v_med3_f32 v29, v13, s13, v200
	v_cvt_pk_fp8_f32 v114, v28, v29 op_sel:[0,0,1]
	global_store_dword v[36:37], v114, off offset:768
	ds_write_b128 v17, v[2:5]
	ds_write_b128 v17, v[6:9] offset:1024
	ds_write_b128 v17, v[30:33] offset:2048
	ds_write_b128 v17, v[10:13] offset:3072
	v_lshl_add_u64 v[2:3], v[18:19], 0, s[2:3]
	global_load_dwordx2 v[4:5], v[2:3], off
	global_load_dwordx2 v[8:9], v[2:3], off offset:512
	global_load_dwordx2 v[12:13], v[2:3], off offset:1024
	s_lshr_b32 s2, s7, 20
	global_load_dwordx2 v[2:3], v[2:3], off offset:1536
	s_add_i32 s2, s6, s2
	s_ashr_i32 s2, s2, 12
	s_cmpk_lt_i32 s6, 0x4000
	s_cselect_b32 s2, s2, 4
	s_mul_hi_i32 s3, s2, 0x6000
	s_mulk_i32 s2, 0x6000
	s_add_u32 s2, s1, s2
	s_addc_u32 s3, s8, s3
	s_add_u32 s4, s2, 0x3000
	s_addc_u32 s5, s3, 0
	s_add_u32 s2, s2, 0x4000
	s_addc_u32 s3, s3, 0
	s_lshl_b64 s[6:7], s[6:7], 10
	s_waitcnt vmcnt(1)
	v_lshlrev_b32_e32 v10, 16, v12
	v_and_b32_e32 v11, 0xffff0000, v12
	s_waitcnt vmcnt(0)
	v_lshlrev_b32_e32 v28, 16, v2
	v_and_b32_e32 v17, 0xffff0000, v2
	v_lshlrev_b32_e32 v30, 16, v3
	v_and_b32_e32 v31, 0xffff0000, v3
	v_lshlrev_b32_e32 v3, 16, v5
	v_lshlrev_b32_e32 v2, 16, v4
	v_and_b32_e32 v5, 0xffff0000, v5
	v_and_b32_e32 v4, 0xffff0000, v4
	v_pk_mul_f32 v[6:7], v[4:5], v[4:5]
	v_lshlrev_b32_e32 v12, 16, v13
	v_pk_fma_f32 v[6:7], v[2:3], v[2:3], v[6:7]
	v_mul_f32_e32 v29, v10, v10
	v_pk_add_f32 v[32:33], v[6:7], v[6:7] op_sel_hi:[0,1]
	v_lshlrev_b32_e32 v7, 16, v9
	v_lshlrev_b32_e32 v6, 16, v8
	v_and_b32_e32 v9, 0xffff0000, v9
	v_and_b32_e32 v8, 0xffff0000, v8
	v_pk_mul_f32 v[36:37], v[8:9], v[8:9]
	v_mul_f32_e32 v115, v11, v11
	v_pk_fma_f32 v[36:37], v[6:7], v[6:7], v[36:37]
	v_and_b32_e32 v13, 0xffff0000, v13
	v_mul_f32_e32 v32, v12, v12
	v_mov_b32_e32 v114, v28
	v_pk_add_f32 v[36:37], v[36:37], v[36:37] op_sel_hi:[0,1]
	v_pk_fma_f32 v[116:117], v[12:13], v[12:13], v[32:33] op_sel_hi:[1,1,0]
	v_pk_add_f32 v[114:115], v[28:29], v[114:115]
	v_mul_f32_e32 v116, v17, v17
	v_mul_f32_e32 v32, v30, v30
	v_mul_f32_e32 v36, v31, v31
	v_mul_f32_e32 v118, v28, v28
	v_mov_b32_e32 v119, v115
	v_pk_add_f32 v[114:115], v[118:119], v[116:117]
	v_pk_add_f32 v[32:33], v[32:33], v[36:37]
	v_mov_b32_e32 v36, v3
	v_pk_add_f32 v[32:33], v[114:115], v[32:33]
	global_load_dwordx4 v[114:117], v[22:23], off
	global_load_dwordx4 v[118:121], v21, s[4:5]
	global_load_dwordx4 v[122:125], v21, s[2:3]
	v_add_f32_e32 v27, v32, v33
	s_nop 1
	v_mov_b32_dpp v29, v27 quad_perm:[1,0,3,2] row_mask:0xf bank_mask:0xf
	v_mov_b32_e32 v3, v4
	v_mov_b32_e32 v37, v5
	v_mov_b32_e32 v126, v7
	v_mov_b32_e32 v127, v9
	s_waitcnt lgkmcnt(0)
	v_add_f32_e32 v27, v27, v29
	s_nop 1
	v_mov_b32_dpp v29, v27 quad_perm:[2,3,0,1] row_mask:0xf bank_mask:0xf
	v_mov_b32_e32 v7, v8
	s_waitcnt lgkmcnt(0)
	v_add_f32_e32 v27, v27, v29
	s_nop 1
	v_mov_b32_dpp v29, v27 row_half_mirror row_mask:0xf bank_mask:0xf
	s_waitcnt lgkmcnt(0)
	v_add_f32_e32 v27, v27, v29
	s_nop 1
	v_mov_b32_dpp v29, v27 row_mirror row_mask:0xf bank_mask:0xf
	s_waitcnt lgkmcnt(0)
	v_add_f32_e32 v27, v27, v29
	v_mov_b32_e32 v29, v27
	s_nop 1
	v_permlane16_swap_b32_e32 v29, v27
	s_waitcnt lgkmcnt(0)
	v_add_f32_e32 v27, v27, v29
	v_mov_b32_e32 v29, v27
	s_nop 1
	v_permlane32_swap_b32_e32 v29, v27
	s_waitcnt lgkmcnt(0)
	v_add_f32_e32 v27, v27, v29
	v_fmamk_f32 v27, v27, 0x3a800000, v165
	v_rsq_f32_e32 v32, v27
	s_nop 0
	v_pk_mul_f32 v[2:3], v[2:3], v[32:33] op_sel_hi:[1,0]
	v_pk_mul_f32 v[36:37], v[36:37], v[32:33] op_sel_hi:[1,0]
	s_waitcnt vmcnt(2)
	v_pk_mul_f32 v[2:3], v[114:115], v[2:3]
	v_pk_mul_f32 v[4:5], v[116:117], v[36:37]
	s_waitcnt vmcnt(0)
	v_pk_add_f32 v[114:115], v[122:123], 1.0 op_sel_hi:[1,0]
	v_pk_add_f32 v[36:37], v[124:125], 1.0 op_sel_hi:[1,0]
	v_pk_fma_f32 v[2:3], v[114:115], v[2:3], v[118:119]
	v_mov_b32_e32 v114, v35
	v_med3_f32 v27, v2, s13, v200
	v_med3_f32 v29, v3, s13, v200
	v_cvt_pk_fp8_f32 v114, v27, v29
	v_pk_fma_f32 v[4:5], v[36:37], v[4:5], v[120:121]
	s_nop 0
	v_med3_f32 v33, v4, s13, v200
	v_med3_f32 v36, v5, s13, v200
	v_cvt_pk_fp8_f32 v114, v33, v36 op_sel:[0,0,1]
	v_lshl_add_u64 v[36:37], v[24:25], 0, s[6:7]
	v_pk_mul_f32 v[126:127], v[126:127], v[32:33] op_sel_hi:[1,0]
	v_pk_mul_f32 v[6:7], v[6:7], v[32:33] op_sel_hi:[1,0]
	global_store_dword v[36:37], v114, off
	global_load_dwordx4 v[114:117], v[22:23], off offset:1024
	s_nop 0
	global_load_dwordx4 v[118:121], v34, s[4:5]
	global_load_dwordx4 v[122:125], v34, s[2:3]
	s_waitcnt vmcnt(2)
	v_pk_mul_f32 v[6:7], v[114:115], v[6:7]
	v_pk_mul_f32 v[8:9], v[116:117], v[126:127]
	s_waitcnt vmcnt(0)
	v_pk_add_f32 v[116:117], v[122:123], 1.0 op_sel_hi:[1,0]
	v_pk_add_f32 v[114:115], v[124:125], 1.0 op_sel_hi:[1,0]
	v_pk_fma_f32 v[6:7], v[116:117], v[6:7], v[118:119]
	v_pk_fma_f32 v[8:9], v[114:115], v[8:9], v[120:121]
	v_med3_f32 v27, v6, s13, v200
	v_med3_f32 v29, v7, s13, v200
	v_mov_b32_e32 v115, v35
	v_cvt_pk_fp8_f32 v115, v27, v29
	v_med3_f32 v33, v8, s13, v200
	v_med3_f32 v114, v9, s13, v200
	v_pk_mul_f32 v[12:13], v[12:13], v[32:33] op_sel_hi:[1,0]
	v_cvt_pk_fp8_f32 v115, v33, v114 op_sel:[0,0,1]
	v_pk_mul_f32 v[10:11], v[10:11], v[32:33] op_sel_hi:[1,0]
	global_store_dword v[36:37], v115, off offset:256
	global_load_dwordx4 v[114:117], v[22:23], off offset:2048
	s_nop 0
	global_load_dwordx4 v[118:121], v109, s[4:5]
	global_load_dwordx4 v[122:125], v109, s[2:3]
	s_waitcnt vmcnt(2)
	v_pk_mul_f32 v[10:11], v[10:11], v[114:115]
	v_pk_mul_f32 v[12:13], v[12:13], v[116:117]
	s_waitcnt vmcnt(0)
	v_pk_add_f32 v[116:117], v[122:123], 1.0 op_sel_hi:[1,0]
	v_pk_add_f32 v[114:115], v[124:125], 1.0 op_sel_hi:[1,0]
	v_pk_fma_f32 v[10:11], v[10:11], v[116:117], v[118:119]
	v_pk_fma_f32 v[12:13], v[12:13], v[114:115], v[120:121]
	v_med3_f32 v27, v10, s13, v200
	v_med3_f32 v29, v11, s13, v200
	v_mov_b32_e32 v115, v35
	v_cvt_pk_fp8_f32 v115, v27, v29
	v_med3_f32 v33, v12, s13, v200
	v_med3_f32 v114, v13, s13, v200
	v_mov_b32_e32 v29, v17
	v_cvt_pk_fp8_f32 v115, v33, v114 op_sel:[0,0,1]
	v_pk_mul_f32 v[28:29], v[28:29], v[32:33] op_sel_hi:[1,0]
	v_pk_mul_f32 v[30:31], v[30:31], v[32:33] op_sel_hi:[1,0]
	global_store_dword v[36:37], v115, off offset:512
	global_load_dwordx4 v[114:117], v[22:23], off offset:3072
	s_nop 0
	global_load_dwordx4 v[118:121], v110, s[4:5]
	global_load_dwordx4 v[122:125], v110, s[2:3]
	s_waitcnt vmcnt(2)
	v_pk_mul_f32 v[28:29], v[28:29], v[114:115]
	v_pk_mul_f32 v[30:31], v[30:31], v[116:117]
	s_waitcnt vmcnt(0)
	v_pk_add_f32 v[114:115], v[122:123], 1.0 op_sel_hi:[1,0]
	v_pk_add_f32 v[32:33], v[124:125], 1.0 op_sel_hi:[1,0]
	v_pk_fma_f32 v[28:29], v[28:29], v[114:115], v[118:119]
	v_mov_b32_e32 v114, v35
	v_med3_f32 v17, v28, s13, v200
	v_med3_f32 v27, v29, s13, v200
	v_cvt_pk_fp8_f32 v114, v17, v27
	v_pk_fma_f32 v[30:31], v[30:31], v[32:33], v[120:121]
	v_add_u32_e32 v17, s14, v20
	v_med3_f32 v32, v30, s13, v200
	v_med3_f32 v33, v31, s13, v200
	v_cvt_pk_fp8_f32 v114, v32, v33 op_sel:[0,0,1]
	global_store_dword v[36:37], v114, off offset:768
	ds_write_b128 v17, v[2:5]
	ds_write_b128 v17, v[6:9] offset:1024
	ds_write_b128 v17, v[10:13] offset:2048
	ds_write_b128 v17, v[28:31] offset:3072
	s_waitcnt lgkmcnt(0)
	s_barrier
	ds_read2_b32 v[10:11], v111 offset1:4
	ds_read2_b32 v[12:13], v111 offset0:8 offset1:12
	s_waitcnt lgkmcnt(1)
	v_mfma_f32_16x16x4_f32 v[2:5], v10, v39, 0
	v_mfma_f32_16x16x4_f32 v[6:9], v10, v46, 0
	v_mfma_f32_16x16x4_f32 v[2:5], v11, v40, v[2:5]
	v_mfma_f32_16x16x4_f32 v[6:9], v11, v45, v[6:9]
	ds_read2_b32 v[10:11], v111 offset0:16 offset1:20
	s_waitcnt lgkmcnt(1)
	v_mfma_f32_16x16x4_f32 v[2:5], v12, v41, v[2:5]
	v_mfma_f32_16x16x4_f32 v[6:9], v12, v44, v[6:9]
	v_mfma_f32_16x16x4_f32 v[2:5], v13, v42, v[2:5]
	v_mfma_f32_16x16x4_f32 v[6:9], v13, v43, v[6:9]
	s_waitcnt lgkmcnt(0)
	v_mfma_f32_16x16x4_f32 v[2:5], v10, v47, v[2:5]
	v_mfma_f32_16x16x4_f32 v[6:9], v10, v54, v[6:9]
	v_mfma_f32_16x16x4_f32 v[2:5], v11, v48, v[2:5]
	v_mfma_f32_16x16x4_f32 v[6:9], v11, v53, v[6:9]
	ds_read2_b32 v[10:11], v111 offset0:24 offset1:28
	s_waitcnt lgkmcnt(0)
	v_mfma_f32_16x16x4_f32 v[2:5], v10, v49, v[2:5]
	v_mfma_f32_16x16x4_f32 v[6:9], v10, v52, v[6:9]
	v_mfma_f32_16x16x4_f32 v[2:5], v11, v50, v[2:5]
	v_mfma_f32_16x16x4_f32 v[6:9], v11, v51, v[6:9]
	ds_read2_b32 v[10:11], v111 offset0:32 offset1:36
	s_waitcnt lgkmcnt(0)
	v_mfma_f32_16x16x4_f32 v[2:5], v10, v55, v[2:5]
	v_mfma_f32_16x16x4_f32 v[6:9], v10, v62, v[6:9]
	v_mfma_f32_16x16x4_f32 v[2:5], v11, v56, v[2:5]
	v_mfma_f32_16x16x4_f32 v[6:9], v11, v61, v[6:9]
	ds_read2_b32 v[10:11], v111 offset0:40 offset1:44
	s_waitcnt lgkmcnt(0)
	v_mfma_f32_16x16x4_f32 v[2:5], v10, v57, v[2:5]
	v_mfma_f32_16x16x4_f32 v[6:9], v10, v60, v[6:9]
	v_mfma_f32_16x16x4_f32 v[2:5], v11, v58, v[2:5]
	v_mfma_f32_16x16x4_f32 v[6:9], v11, v59, v[6:9]
	ds_read2_b32 v[10:11], v111 offset0:48 offset1:52
	s_waitcnt lgkmcnt(0)
	v_mfma_f32_16x16x4_f32 v[2:5], v10, v63, v[2:5]
	v_mfma_f32_16x16x4_f32 v[6:9], v10, v70, v[6:9]
	v_mfma_f32_16x16x4_f32 v[2:5], v11, v64, v[2:5]
	v_mfma_f32_16x16x4_f32 v[6:9], v11, v69, v[6:9]
	ds_read2_b32 v[10:11], v111 offset0:56 offset1:60
	s_waitcnt lgkmcnt(0)
	v_mfma_f32_16x16x4_f32 v[2:5], v10, v65, v[2:5]
	v_mfma_f32_16x16x4_f32 v[6:9], v10, v68, v[6:9]
	v_mfma_f32_16x16x4_f32 v[2:5], v11, v66, v[2:5]
	v_mfma_f32_16x16x4_f32 v[6:9], v11, v67, v[6:9]
	ds_read2_b32 v[10:11], v111 offset0:64 offset1:68
	s_waitcnt lgkmcnt(0)
	v_mfma_f32_16x16x4_f32 v[2:5], v10, v71, v[2:5]
	v_mfma_f32_16x16x4_f32 v[6:9], v10, v78, v[6:9]
	v_mfma_f32_16x16x4_f32 v[2:5], v11, v72, v[2:5]
	v_mfma_f32_16x16x4_f32 v[6:9], v11, v77, v[6:9]
	ds_read2_b32 v[10:11], v111 offset0:72 offset1:76
	s_waitcnt lgkmcnt(0)
	v_mfma_f32_16x16x4_f32 v[2:5], v10, v73, v[2:5]
	v_mfma_f32_16x16x4_f32 v[6:9], v10, v76, v[6:9]
	v_mfma_f32_16x16x4_f32 v[2:5], v11, v74, v[2:5]
	v_mfma_f32_16x16x4_f32 v[6:9], v11, v75, v[6:9]
	ds_read2_b32 v[10:11], v111 offset0:80 offset1:84
	s_waitcnt lgkmcnt(0)
	v_mfma_f32_16x16x4_f32 v[2:5], v10, v79, v[2:5]
	v_mfma_f32_16x16x4_f32 v[6:9], v10, v86, v[6:9]
	v_mfma_f32_16x16x4_f32 v[2:5], v11, v80, v[2:5]
	v_mfma_f32_16x16x4_f32 v[6:9], v11, v85, v[6:9]
	ds_read2_b32 v[10:11], v111 offset0:88 offset1:92
	s_waitcnt lgkmcnt(0)
	v_mfma_f32_16x16x4_f32 v[2:5], v10, v81, v[2:5]
	v_mfma_f32_16x16x4_f32 v[6:9], v10, v84, v[6:9]
	v_mfma_f32_16x16x4_f32 v[2:5], v11, v82, v[2:5]
	v_mfma_f32_16x16x4_f32 v[6:9], v11, v83, v[6:9]
	ds_read2_b32 v[10:11], v111 offset0:96 offset1:100
	s_waitcnt lgkmcnt(0)
	v_mfma_f32_16x16x4_f32 v[2:5], v10, v87, v[2:5]
	v_mfma_f32_16x16x4_f32 v[6:9], v10, v94, v[6:9]
	v_mfma_f32_16x16x4_f32 v[2:5], v11, v88, v[2:5]
	v_mfma_f32_16x16x4_f32 v[6:9], v11, v93, v[6:9]
	ds_read2_b32 v[10:11], v111 offset0:104 offset1:108
	s_waitcnt lgkmcnt(0)
	v_mfma_f32_16x16x4_f32 v[2:5], v10, v89, v[2:5]
	v_mfma_f32_16x16x4_f32 v[6:9], v10, v92, v[6:9]
	v_mfma_f32_16x16x4_f32 v[2:5], v11, v90, v[2:5]
	v_mfma_f32_16x16x4_f32 v[6:9], v11, v91, v[6:9]
	ds_read2_b32 v[10:11], v111 offset0:112 offset1:116
	s_waitcnt lgkmcnt(0)
	v_mfma_f32_16x16x4_f32 v[2:5], v10, v95, v[2:5]
	v_mfma_f32_16x16x4_f32 v[6:9], v10, v102, v[6:9]
	v_mfma_f32_16x16x4_f32 v[2:5], v11, v96, v[2:5]
	v_mfma_f32_16x16x4_f32 v[6:9], v11, v101, v[6:9]
	ds_read2_b32 v[10:11], v111 offset0:120 offset1:124
	s_waitcnt lgkmcnt(0)
	v_mfma_f32_16x16x4_f32 v[2:5], v10, v97, v[2:5]
	v_mfma_f32_16x16x4_f32 v[6:9], v10, v100, v[6:9]
	v_mfma_f32_16x16x4_f32 v[2:5], v11, v98, v[2:5]
	v_mfma_f32_16x16x4_f32 v[6:9], v11, v99, v[6:9]
	s_nop 9
	ds_write2_b32 v112, v2, v6 offset1:16
	ds_write2_b32 v112, v3, v7 offset0:33 offset1:49
	ds_write2_b32 v112, v4, v8 offset0:66 offset1:82
	ds_write2_b32 v112, v5, v9 offset0:99 offset1:115
	s_waitcnt lgkmcnt(0)
	s_barrier
	ds_read_b32 v2, v113
	ds_read_b32 v3, v113 offset:2112
	s_waitcnt lgkmcnt(1)
	v_add_f32_e32 v2, v38, v2
	s_waitcnt lgkmcnt(0)
	v_add_f32_e32 v2, v2, v3
	ds_read_b32 v3, v113 offset:4224
	s_waitcnt lgkmcnt(0)
	v_add_f32_e32 v2, v2, v3
	ds_read_b32 v3, v113 offset:6336
	s_waitcnt lgkmcnt(0)
	v_add_f32_e32 v2, v2, v3
	ds_read_b32 v3, v113 offset:8448
	s_waitcnt lgkmcnt(0)
	v_add_f32_e32 v2, v2, v3
	ds_read_b32 v3, v113 offset:10560
	s_waitcnt lgkmcnt(0)
	v_add_f32_e32 v2, v2, v3
	ds_read_b32 v3, v113 offset:12672
	s_waitcnt lgkmcnt(0)
	v_add_f32_e32 v2, v2, v3
	ds_read_b32 v3, v113 offset:14784
	s_waitcnt lgkmcnt(0)
	v_add_f32_e32 v2, v2, v3
	v_not_b32_e32 v3, v2
	v_or_b32_e32 v4, 0x80000000, v2
	v_cmp_gt_i32_e64 s[2:3], 0, v2
	s_nop 1
	v_mov_b32_dpp v2, v16 quad_perm:[1,0,3,2] row_mask:0xf bank_mask:0xf
	s_nop 0
	v_cndmask_b32_e64 v17, v4, v3, s[2:3]
	s_nop 1
	v_mov_b32_dpp v3, v17 quad_perm:[1,0,3,2] row_mask:0xf bank_mask:0xf
	s_waitcnt lgkmcnt(0)
	v_cmp_gt_u64_e64 s[2:3], v[2:3], v[16:17]
	s_nop 1
	v_cndmask_b32_e64 v3, v17, v3, s[2:3]
	v_cndmask_b32_e64 v2, v16, v2, s[2:3]
	s_nop 1
	v_mov_b32_dpp v4, v2 quad_perm:[2,3,0,1] row_mask:0xf bank_mask:0xf
	s_nop 1
	v_mov_b32_dpp v5, v3 quad_perm:[2,3,0,1] row_mask:0xf bank_mask:0xf
	s_waitcnt lgkmcnt(0)
	v_cmp_gt_u64_e64 s[2:3], v[4:5], v[2:3]
	s_nop 1
	v_cndmask_b32_e64 v3, v3, v5, s[2:3]
	v_cndmask_b32_e64 v2, v2, v4, s[2:3]
	s_nop 1
	v_mov_b32_dpp v4, v2 row_half_mirror row_mask:0xf bank_mask:0xf
	s_nop 1
	v_mov_b32_dpp v5, v3 row_half_mirror row_mask:0xf bank_mask:0xf
	s_waitcnt lgkmcnt(0)
	v_cmp_gt_u64_e64 s[2:3], v[4:5], v[2:3]
	s_nop 1
	v_cndmask_b32_e64 v3, v3, v5, s[2:3]
	v_cndmask_b32_e64 v2, v2, v4, s[2:3]
	s_nop 1
	v_mov_b32_dpp v4, v2 row_mirror row_mask:0xf bank_mask:0xf
	s_nop 1
	v_mov_b32_dpp v5, v3 row_mirror row_mask:0xf bank_mask:0xf
	s_waitcnt lgkmcnt(0)
	v_cmp_gt_u64_e64 s[2:3], v[4:5], v[2:3]
	s_nop 1
	v_cndmask_b32_e64 v3, v3, v5, s[2:3]
	v_cndmask_b32_e64 v2, v2, v4, s[2:3]
	ds_bpermute_b32 v4, v107, v2
	ds_bpermute_b32 v5, v107, v3
	s_waitcnt lgkmcnt(0)
	v_cmp_gt_u64_e64 s[2:3], v[4:5], v[2:3]
	s_nop 1
	v_cndmask_b32_e64 v2, v2, v4, s[2:3]
	v_sub_u32_e32 v30, 31, v2
	v_cmp_ne_u32_e64 s[4:5], v30, v15
	s_nop 1
	v_cndmask_b32_e64 v11, 0, v17, s[4:5]
	v_cndmask_b32_e64 v10, 0, v16, s[4:5]
	s_nop 1
	v_mov_b32_dpp v6, v10 quad_perm:[1,0,3,2] row_mask:0xf bank_mask:0xf
	s_nop 1
	v_mov_b32_dpp v7, v11 quad_perm:[1,0,3,2] row_mask:0xf bank_mask:0xf
	s_waitcnt lgkmcnt(0)
	v_cmp_gt_u64_e64 s[4:5], v[6:7], v[10:11]
	s_nop 1
	v_cndmask_b32_e64 v7, v11, v7, s[4:5]
	v_cndmask_b32_e64 v6, v10, v6, s[4:5]
	s_nop 1
	v_mov_b32_dpp v8, v6 quad_perm:[2,3,0,1] row_mask:0xf bank_mask:0xf
	s_nop 1
	v_mov_b32_dpp v9, v7 quad_perm:[2,3,0,1] row_mask:0xf bank_mask:0xf
	s_waitcnt lgkmcnt(0)
	v_cmp_gt_u64_e64 s[4:5], v[8:9], v[6:7]
	s_nop 1
	v_cndmask_b32_e64 v7, v7, v9, s[4:5]
	v_cndmask_b32_e64 v6, v6, v8, s[4:5]
	s_nop 1
	v_mov_b32_dpp v8, v6 row_half_mirror row_mask:0xf bank_mask:0xf
	s_nop 1
	v_mov_b32_dpp v9, v7 row_half_mirror row_mask:0xf bank_mask:0xf
	s_waitcnt lgkmcnt(0)
	v_cmp_gt_u64_e64 s[4:5], v[8:9], v[6:7]
	s_nop 1
	v_cndmask_b32_e64 v7, v7, v9, s[4:5]
	v_cndmask_b32_e64 v6, v6, v8, s[4:5]
	s_nop 1
	v_mov_b32_dpp v8, v6 row_mirror row_mask:0xf bank_mask:0xf
	s_nop 1
	v_mov_b32_dpp v9, v7 row_mirror row_mask:0xf bank_mask:0xf
	s_waitcnt lgkmcnt(0)
	v_cmp_gt_u64_e64 s[4:5], v[8:9], v[6:7]
	s_nop 1
	v_cndmask_b32_e64 v7, v7, v9, s[4:5]
	v_cndmask_b32_e64 v6, v6, v8, s[4:5]
	ds_bpermute_b32 v8, v107, v6
	ds_bpermute_b32 v9, v107, v7
	s_waitcnt lgkmcnt(0)
	v_cmp_gt_u64_e64 s[4:5], v[8:9], v[6:7]
	s_nop 1
	v_cndmask_b32_e64 v4, v6, v8, s[4:5]
	v_sub_u32_e32 v17, 31, v4
	v_cmp_ne_u32_e64 s[6:7], v17, v15
	s_nop 1
	v_cndmask_b32_e64 v29, 0, v11, s[6:7]
	v_cndmask_b32_e64 v28, 0, v10, s[6:7]
	s_nop 1
	v_mov_b32_dpp v10, v28 quad_perm:[1,0,3,2] row_mask:0xf bank_mask:0xf
	s_nop 1
	v_mov_b32_dpp v11, v29 quad_perm:[1,0,3,2] row_mask:0xf bank_mask:0xf
	s_waitcnt lgkmcnt(0)
	v_cmp_gt_u64_e64 s[6:7], v[10:11], v[28:29]
	s_nop 1
	v_cndmask_b32_e64 v11, v29, v11, s[6:7]
	v_cndmask_b32_e64 v10, v28, v10, s[6:7]
	s_nop 1
	v_mov_b32_dpp v12, v10 quad_perm:[2,3,0,1] row_mask:0xf bank_mask:0xf
	s_nop 1
	v_mov_b32_dpp v13, v11 quad_perm:[2,3,0,1] row_mask:0xf bank_mask:0xf
	s_waitcnt lgkmcnt(0)
	v_cmp_gt_u64_e64 s[6:7], v[12:13], v[10:11]
	s_nop 1
	v_cndmask_b32_e64 v11, v11, v13, s[6:7]
	v_cndmask_b32_e64 v10, v10, v12, s[6:7]
	s_nop 1
	v_mov_b32_dpp v12, v10 row_half_mirror row_mask:0xf bank_mask:0xf
	s_nop 1
	v_mov_b32_dpp v13, v11 row_half_mirror row_mask:0xf bank_mask:0xf
	s_waitcnt lgkmcnt(0)
	v_cmp_gt_u64_e64 s[6:7], v[12:13], v[10:11]
	s_nop 1
	v_cndmask_b32_e64 v11, v11, v13, s[6:7]
	v_cndmask_b32_e64 v10, v10, v12, s[6:7]
	s_nop 1
	v_mov_b32_dpp v12, v10 row_mirror row_mask:0xf bank_mask:0xf
	s_nop 1
	v_mov_b32_dpp v13, v11 row_mirror row_mask:0xf bank_mask:0xf
	s_waitcnt lgkmcnt(0)
	v_cmp_gt_u64_e64 s[6:7], v[12:13], v[10:11]
	s_nop 1
	v_cndmask_b32_e64 v11, v11, v13, s[6:7]
	v_cndmask_b32_e64 v10, v10, v12, s[6:7]
	ds_bpermute_b32 v12, v107, v10
	ds_bpermute_b32 v13, v107, v11
	s_waitcnt lgkmcnt(0)
	v_cmp_gt_u64_e64 s[40:41], v[12:13], v[10:11]
	s_nop 1
	v_cndmask_b32_e64 v6, v10, v12, s[40:41]
	v_sub_u32_e32 v12, 31, v6
	v_cmp_ne_u32_e64 s[6:7], v12, v15
	s_nop 1
	v_cndmask_b32_e64 v29, 0, v29, s[6:7]
	v_cndmask_b32_e64 v28, 0, v28, s[6:7]
	s_nop 1
	v_mov_b32_dpp v32, v28 quad_perm:[1,0,3,2] row_mask:0xf bank_mask:0xf
	s_nop 1
	v_mov_b32_dpp v33, v29 quad_perm:[1,0,3,2] row_mask:0xf bank_mask:0xf
	s_waitcnt lgkmcnt(0)
	v_cmp_gt_u64_e64 s[6:7], v[32:33], v[28:29]
	s_nop 1
	v_cndmask_b32_e64 v29, v29, v33, s[6:7]
	v_cndmask_b32_e64 v28, v28, v32, s[6:7]
	s_nop 1
	v_mov_b32_dpp v32, v28 quad_perm:[2,3,0,1] row_mask:0xf bank_mask:0xf
	s_nop 1
	v_mov_b32_dpp v33, v29 quad_perm:[2,3,0,1] row_mask:0xf bank_mask:0xf
	s_waitcnt lgkmcnt(0)
	v_cmp_gt_u64_e64 s[6:7], v[32:33], v[28:29]
	s_nop 1
	v_cndmask_b32_e64 v29, v29, v33, s[6:7]
	v_cndmask_b32_e64 v28, v28, v32, s[6:7]
	s_nop 1
	v_mov_b32_dpp v32, v28 row_half_mirror row_mask:0xf bank_mask:0xf
	s_nop 1
	v_mov_b32_dpp v33, v29 row_half_mirror row_mask:0xf bank_mask:0xf
	s_waitcnt lgkmcnt(0)
	v_cmp_gt_u64_e64 s[6:7], v[32:33], v[28:29]
	s_nop 1
	v_cndmask_b32_e64 v29, v29, v33, s[6:7]
	v_cndmask_b32_e64 v28, v28, v32, s[6:7]
	s_nop 1
	v_mov_b32_dpp v32, v28 row_mirror row_mask:0xf bank_mask:0xf
	s_nop 1
	v_mov_b32_dpp v33, v29 row_mirror row_mask:0xf bank_mask:0xf
	s_waitcnt lgkmcnt(0)
	v_cmp_gt_u64_e64 s[6:7], v[32:33], v[28:29]
	s_nop 1
	v_cndmask_b32_e64 v29, v29, v33, s[6:7]
	v_cndmask_b32_e64 v28, v28, v32, s[6:7]
	ds_bpermute_b32 v8, v107, v28
	ds_bpermute_b32 v10, v107, v29
	s_and_saveexec_b64 s[6:7], s[38:39]
	s_cbranch_execz .LBB0_1417
	v_cndmask_b32_e64 v3, v3, v5, s[2:3]
	v_cndmask_b32_e64 v5, v7, v9, s[4:5]
	s_waitcnt lgkmcnt(0)
	v_mov_b32_e32 v9, v10
	v_cmp_gt_u64_e64 s[2:3], v[8:9], v[28:29]
	v_cndmask_b32_e64 v7, v11, v13, s[40:41]
	v_ashrrev_i32_e32 v27, 31, v26
	v_cndmask_b32_e64 v9, v29, v10, s[2:3]
	v_cndmask_b32_e64 v8, v28, v8, s[2:3]
	v_not_b32_e32 v10, v9
	v_cmp_gt_i64_e64 s[2:3], 0, v[8:9]
	v_sub_u32_e32 v31, 31, v8
	s_nop 0
	v_cndmask_b32_e64 v9, v10, |v9|, s[2:3]
	v_not_b32_e32 v10, v7
	v_cmp_gt_i64_e64 s[2:3], 0, v[6:7]
	s_nop 1
	v_cndmask_b32_e64 v6, v10, |v7|, s[2:3]
	v_not_b32_e32 v7, v5
	v_cmp_gt_i64_e64 s[2:3], 0, v[4:5]
	s_nop 1
	v_cndmask_b32_e64 v4, v7, |v5|, s[2:3]
	v_not_b32_e32 v5, v3
	v_cmp_gt_i64_e64 s[2:3], 0, v[2:3]
	s_nop 1
	v_cndmask_b32_e64 v2, v5, |v3|, s[2:3]
	v_sub_f32_e32 v3, v4, v2
	v_mul_f32_e32 v3, 0x3fb8aa3b, v3
	v_exp_f32_e32 v13, v3
	v_sub_f32_e32 v3, v6, v2
	v_mul_f32_e32 v3, 0x3fb8aa3b, v3
	v_sub_f32_e32 v2, v9, v2
	v_exp_f32_e32 v28, v3
	v_mul_f32_e32 v2, 0x3fb8aa3b, v2
	v_exp_f32_e32 v29, v2
	v_add_f32_e32 v2, 1.0, v13
	v_add_f32_e32 v2, v2, v28
	s_add_i32 s2, 0, 0x20840
	v_add_f32_e32 v2, v2, v29
	v_rcp_f32_e32 v32, v2
	v_add_u32_e32 v2, -3, v26
	v_ashrrev_i32_e32 v3, 31, v2
	v_lshlrev_b64 v[2:3], 2, v[2:3]
	v_lshl_add_u64 v[4:5], s[28:29], 0, v[2:3]
	global_store_dword v[4:5], v30, off
	v_add_u32_e32 v4, -2, v26
	v_ashrrev_i32_e32 v5, 31, v4
	v_lshlrev_b64 v[4:5], 2, v[4:5]
	v_lshl_add_u64 v[6:7], s[28:29], 0, v[4:5]
	global_store_dword v[6:7], v17, off
	v_add_u32_e32 v6, -1, v26
	v_ashrrev_i32_e32 v7, 31, v6
	v_lshlrev_b64 v[6:7], 2, v[6:7]
	v_lshl_add_u64 v[8:9], s[28:29], 0, v[6:7]
	global_store_dword v[8:9], v12, off
	v_lshlrev_b64 v[8:9], 2, v[26:27]
	v_lshl_add_u64 v[10:11], s[28:29], 0, v[8:9]
	v_lshl_add_u64 v[2:3], s[42:43], 0, v[2:3]
	global_store_dword v[10:11], v31, off
	global_store_dword v[2:3], v32, off
	v_mul_f32_e32 v10, v13, v32
	v_lshl_add_u64 v[2:3], s[42:43], 0, v[4:5]
	global_store_dword v[2:3], v10, off
	v_mul_f32_e32 v4, v28, v32
	v_lshl_add_u64 v[2:3], s[42:43], 0, v[6:7]
	global_store_dword v[2:3], v4, off
	v_mul_f32_e32 v4, v29, v32
	v_lshl_add_u64 v[2:3], s[42:43], 0, v[8:9]
	global_store_dword v[2:3], v4, off
	v_lshl_add_u32 v2, v30, 2, s2
	ds_add_u32 v2, v250
	v_lshl_add_u32 v2, v17, 2, s2
	ds_add_u32 v2, v250
	v_lshl_add_u32 v2, v12, 2, s2
	ds_add_u32 v2, v250
	v_lshl_add_u32 v2, v31, 2, s2
	ds_add_u32 v2, v250
	s_branch .LBB0_1417

.LBB0_1672:
	s_add_u32 s18, s16, s2
	s_addc_u32 s19, s17, s3
	s_add_u32 s22, s18, 0x2bcec100
	s_addc_u32 s23, s19, 0
	s_add_u32 s59, s11, s2
	s_addc_u32 s60, s57, s3
	s_cmpk_eq_i32 s2, 0x300
	s_cselect_b64 vcc, -1, 0
	s_and_b64 s[18:19], vcc, exec
	s_cselect_b32 s23, s7, s23
	s_cselect_b32 s22, s6, s22
	s_cselect_b32 s19, s0, s60
	s_cselect_b32 s18, s1, s59
	s_add_i32 s60, 0, 0x10000
	v_add_u32_e32 v6, s60, v213
	ds_read_b128 v[10:13], v6
	ds_read_b128 v[14:17], v6 offset:1024
	ds_read_b128 v[2:5], v6 offset:2048
	ds_read_b128 v[6:9], v6 offset:3072
	v_cndmask_b32_e32 v34, v174, v214, vcc
	v_cndmask_b32_e32 v179, v178, v216, vcc
	v_cndmask_b32_e32 v190, v176, v215, vcc
	v_cndmask_b32_e32 v181, v180, v217, vcc
	v_lshl_add_u64 v[18:19], v[184:185], 0, s[2:3]
	s_add_i32 m0, s9, 0xc000
	ds_read_b128 v[192:195], v177
	ds_read_b128 v[196:199], v177 offset:1024
	ds_read_b128 v[218:221], v177 offset:2048
	ds_read_b128 v[222:225], v177 offset:3072
	ds_read_b128 v[226:229], v177 offset:4096
	ds_read_b128 v[230:233], v177 offset:5120
	ds_read_b128 v[242:245], v177 offset:6144
	ds_read_b128 v[246:249], v177 offset:7168
	global_load_lds_dwordx4 v[18:19], off
	v_lshl_add_u64 v[18:19], v[182:183], 0, s[2:3]
	s_add_i32 m0, s9, 0xe000
	s_nop 0
	global_load_lds_dwordx4 v[18:19], off
	s_waitcnt lgkmcnt(8)
	s_barrier
	s_waitcnt lgkmcnt(0)
	s_setprio 1
	s_waitcnt lgkmcnt(0)
	v_mfma_f32_16x16x128_f8f6f4 v[160:163], v[10:17], v[192:199], v[160:163]
	v_mfma_f32_16x16x128_f8f6f4 v[156:159], v[2:9], v[192:199], v[156:159]
	v_mfma_f32_16x16x128_f8f6f4 v[144:147], v[10:17], v[218:225], v[144:147]
	v_mfma_f32_16x16x128_f8f6f4 v[140:143], v[2:9], v[218:225], v[140:143]
	v_mfma_f32_16x16x128_f8f6f4 v[128:131], v[10:17], v[226:233], v[128:131]
	v_mfma_f32_16x16x128_f8f6f4 v[124:127], v[2:9], v[226:233], v[124:127]
	v_mfma_f32_16x16x128_f8f6f4 v[112:115], v[10:17], v[242:249], v[112:115]
	v_mfma_f32_16x16x128_f8f6f4 v[108:111], v[2:9], v[242:249], v[108:111]
	s_setprio 0
	s_barrier
	s_add_i32 s59, 0, 0x14000
	s_add_i32 s60, s60, s44
	v_add_u32_e32 v22, s59, v213
	v_lshl_add_u64 v[186:187], s[18:19], 0, v[170:171]
	s_mov_b32 m0, s60
	ds_read_b128 v[26:29], v22
	ds_read_b128 v[30:33], v22 offset:1024
	ds_read_b128 v[18:21], v22 offset:2048
	ds_read_b128 v[22:25], v22 offset:3072
	global_load_lds_dwordx4 v[186:187], off
	v_lshl_add_u64 v[188:189], s[18:19], 0, v[172:173]
	s_add_i32 m0, s60, 0x2000
	s_nop 0
	global_load_lds_dwordx4 v[188:189], off
	s_barrier
	s_waitcnt lgkmcnt(0)
	s_setprio 1
	s_waitcnt lgkmcnt(0)
	v_mfma_f32_16x16x128_f8f6f4 v[152:155], v[26:33], v[192:199], v[152:155]
	v_mfma_f32_16x16x128_f8f6f4 v[148:151], v[18:25], v[192:199], v[148:151]
	v_mfma_f32_16x16x128_f8f6f4 v[136:139], v[26:33], v[218:225], v[136:139]
	v_mfma_f32_16x16x128_f8f6f4 v[132:135], v[18:25], v[218:225], v[132:135]
	v_mfma_f32_16x16x128_f8f6f4 v[120:123], v[26:33], v[226:233], v[120:123]
	v_mfma_f32_16x16x128_f8f6f4 v[116:119], v[18:25], v[226:233], v[116:119]
	v_mfma_f32_16x16x128_f8f6f4 v[104:107], v[26:33], v[242:249], v[104:107]
	v_mfma_f32_16x16x128_f8f6f4 v[100:103], v[18:25], v[242:249], v[100:103]
	s_setprio 0
	s_mov_b32 m0, s9
	s_barrier
	ds_read_b128 v[218:221], v177 offset:16384
	ds_read_b128 v[222:225], v177 offset:17408
	ds_read_b128 v[226:229], v177 offset:18432
	ds_read_b128 v[230:233], v177 offset:19456
	ds_read_b128 v[242:245], v177 offset:20480
	ds_read_b128 v[246:249], v177 offset:21504
	ds_read_b128 v[234:237], v177 offset:22528
	ds_read_b128 v[238:241], v177 offset:23552
	global_load_lds_dwordx4 v34, s[22:23]
	s_mov_b32 m0, s45
	v_mov_b32_e32 v191, v35
	global_load_lds_dwordx4 v190, s[22:23]
	s_barrier
	s_waitcnt lgkmcnt(0)
	v_lshl_add_u64 v[192:193], s[22:23], 0, v[34:35]
	v_lshl_add_u64 v[190:191], s[22:23], 0, v[190:191]
	s_setprio 1
	s_waitcnt lgkmcnt(0)
	v_mfma_f32_16x16x128_f8f6f4 v[96:99], v[10:17], v[218:225], v[96:99]
	v_mfma_f32_16x16x128_f8f6f4 v[92:95], v[2:9], v[218:225], v[92:95]
	v_mfma_f32_16x16x128_f8f6f4 v[80:83], v[10:17], v[226:233], v[80:83]
	v_mfma_f32_16x16x128_f8f6f4 v[76:79], v[2:9], v[226:233], v[76:79]
	v_mfma_f32_16x16x128_f8f6f4 v[64:67], v[10:17], v[242:249], v[64:67]
	v_mfma_f32_16x16x128_f8f6f4 v[60:63], v[2:9], v[242:249], v[60:63]
	v_mfma_f32_16x16x128_f8f6f4 v[40:43], v[10:17], v[234:241], v[40:43]
	v_mfma_f32_16x16x128_f8f6f4 v[36:39], v[2:9], v[234:241], v[36:39]
	s_setprio 0
	s_barrier
	s_add_u32 s60, s18, 0x20000
	s_addc_u32 s61, s19, 0
	s_add_i32 s59, s59, s44
	v_lshl_add_u64 v[2:3], s[60:61], 0, v[170:171]
	s_mov_b32 m0, s59
	s_nop 0
	global_load_lds_dwordx4 v[2:3], off
	v_lshl_add_u64 v[2:3], s[60:61], 0, v[172:173]
	s_add_i32 m0, s59, 0x2000
	s_nop 0
	global_load_lds_dwordx4 v[2:3], off
	s_waitcnt vmcnt(6)
	s_barrier
	s_setprio 1
	v_mfma_f32_16x16x128_f8f6f4 v[88:91], v[26:33], v[218:225], v[88:91]
	v_mfma_f32_16x16x128_f8f6f4 v[84:87], v[18:25], v[218:225], v[84:87]
	v_mfma_f32_16x16x128_f8f6f4 v[72:75], v[26:33], v[226:233], v[72:75]
	v_mfma_f32_16x16x128_f8f6f4 v[68:71], v[18:25], v[226:233], v[68:71]
	v_mfma_f32_16x16x128_f8f6f4 v[56:59], v[26:33], v[242:249], v[56:59]
	v_mfma_f32_16x16x128_f8f6f4 v[52:55], v[18:25], v[242:249], v[52:55]
	v_mfma_f32_16x16x128_f8f6f4 v[48:51], v[26:33], v[234:241], v[48:51]
	v_mfma_f32_16x16x128_f8f6f4 v[44:47], v[18:25], v[234:241], v[44:47]
	s_setprio 0
	s_add_i32 s59, 0, 0x18000
	v_add_u32_e32 v14, s59, v213
	s_barrier
	ds_read_b128 v[2:5], v14
	ds_read_b128 v[6:9], v14 offset:1024
	ds_read_b128 v[10:13], v14 offset:2048
	ds_read_b128 v[14:17], v14 offset:3072
	s_mov_b32 m0, s46
	ds_read_b128 v[18:21], v177 offset:32768
	ds_read_b128 v[22:25], v177 offset:33792
	ds_read_b128 v[26:29], v177 offset:34816
	ds_read_b128 v[30:33], v177 offset:35840
	ds_read_b128 v[218:221], v177 offset:36864
	ds_read_b128 v[222:225], v177 offset:37888
	ds_read_b128 v[226:229], v177 offset:38912
	ds_read_b128 v[230:233], v177 offset:39936
	global_load_lds_dwordx4 v179, s[22:23]
	s_mov_b32 m0, s47
	s_nop 0
	global_load_lds_dwordx4 v181, s[22:23]
	s_waitcnt lgkmcnt(8)
	s_barrier
	s_waitcnt lgkmcnt(0)
	s_setprio 1
	s_waitcnt lgkmcnt(0)
	v_mfma_f32_16x16x128_f8f6f4 v[160:163], v[2:9], v[18:25], v[160:163]
	v_mfma_f32_16x16x128_f8f6f4 v[156:159], v[10:17], v[18:25], v[156:159]
	v_mfma_f32_16x16x128_f8f6f4 v[144:147], v[2:9], v[26:33], v[144:147]
	v_mfma_f32_16x16x128_f8f6f4 v[140:143], v[10:17], v[26:33], v[140:143]
	v_mfma_f32_16x16x128_f8f6f4 v[128:131], v[2:9], v[218:225], v[128:131]
	v_mfma_f32_16x16x128_f8f6f4 v[124:127], v[10:17], v[218:225], v[124:127]
	v_mfma_f32_16x16x128_f8f6f4 v[112:115], v[2:9], v[226:233], v[112:115]
	v_mfma_f32_16x16x128_f8f6f4 v[108:111], v[10:17], v[226:233], v[108:111]
	s_setprio 0
	s_barrier
	s_add_i32 s22, 0, 0x1c000
	s_add_i32 s23, s59, s44
	v_add_u32_e32 v34, s22, v213
	v_lshl_add_u64 v[186:187], v[186:187], 0, s[20:21]
	s_mov_b32 m0, s23
	ds_read_b128 v[234:237], v34
	ds_read_b128 v[238:241], v34 offset:1024
	ds_read_b128 v[242:245], v34 offset:2048
	ds_read_b128 v[246:249], v34 offset:3072
	global_load_lds_dwordx4 v[186:187], off
	v_lshl_add_u64 v[186:187], v[188:189], 0, s[20:21]
	s_add_i32 m0, s23, 0x2000
	s_nop 0
	global_load_lds_dwordx4 v[186:187], off
	s_barrier
	s_waitcnt lgkmcnt(0)
	s_setprio 1
	s_waitcnt lgkmcnt(0)
	v_mfma_f32_16x16x128_f8f6f4 v[152:155], v[234:241], v[18:25], v[152:155]
	v_mfma_f32_16x16x128_f8f6f4 v[148:151], v[242:249], v[18:25], v[148:151]
	v_mfma_f32_16x16x128_f8f6f4 v[136:139], v[234:241], v[26:33], v[136:139]
	v_mfma_f32_16x16x128_f8f6f4 v[132:135], v[242:249], v[26:33], v[132:135]
	v_mfma_f32_16x16x128_f8f6f4 v[120:123], v[234:241], v[218:225], v[120:123]
	v_mfma_f32_16x16x128_f8f6f4 v[116:119], v[242:249], v[218:225], v[116:119]
	v_mfma_f32_16x16x128_f8f6f4 v[104:107], v[234:241], v[226:233], v[104:107]
	v_mfma_f32_16x16x128_f8f6f4 v[100:103], v[242:249], v[226:233], v[100:103]
	s_setprio 0
	s_mov_b32 m0, s50
	v_lshl_add_u64 v[186:187], v[192:193], 0, s[20:21]
	s_barrier
	ds_read_b128 v[18:21], v177 offset:49152
	ds_read_b128 v[22:25], v177 offset:50176
	ds_read_b128 v[26:29], v177 offset:51200
	ds_read_b128 v[30:33], v177 offset:52224
	ds_read_b128 v[218:221], v177 offset:53248
	ds_read_b128 v[222:225], v177 offset:54272
	ds_read_b128 v[226:229], v177 offset:55296
	ds_read_b128 v[230:233], v177 offset:56320
	global_load_lds_dwordx4 v[186:187], off
	v_lshl_add_u64 v[186:187], v[190:191], 0, s[20:21]
	s_mov_b32 m0, s51
	s_nop 0
	global_load_lds_dwordx4 v[186:187], off
	s_barrier
	s_waitcnt lgkmcnt(0)
	s_setprio 1
	s_waitcnt lgkmcnt(0)
	v_mfma_f32_16x16x128_f8f6f4 v[96:99], v[2:9], v[18:25], v[96:99]
	v_mfma_f32_16x16x128_f8f6f4 v[92:95], v[10:17], v[18:25], v[92:95]
	v_mfma_f32_16x16x128_f8f6f4 v[80:83], v[2:9], v[26:33], v[80:83]
	v_mfma_f32_16x16x128_f8f6f4 v[76:79], v[10:17], v[26:33], v[76:79]
	v_mfma_f32_16x16x128_f8f6f4 v[64:67], v[2:9], v[218:225], v[64:67]
	v_mfma_f32_16x16x128_f8f6f4 v[60:63], v[10:17], v[218:225], v[60:63]
	v_mfma_f32_16x16x128_f8f6f4 v[40:43], v[2:9], v[226:233], v[40:43]
	v_mfma_f32_16x16x128_f8f6f4 v[36:39], v[10:17], v[226:233], v[36:39]
	s_setprio 0
	s_barrier
	s_add_u32 s18, s18, 0x20080
	s_addc_u32 s19, s19, 0
	s_add_i32 s22, s22, s44
	v_lshl_add_u64 v[2:3], s[18:19], 0, v[170:171]
	s_mov_b32 m0, s22
	s_nop 0
	global_load_lds_dwordx4 v[2:3], off
	v_lshl_add_u64 v[2:3], s[18:19], 0, v[172:173]
	s_add_i32 m0, s22, 0x2000
	s_nop 0
	global_load_lds_dwordx4 v[2:3], off
	s_waitcnt vmcnt(6)
	s_barrier
	s_setprio 1
	v_mfma_f32_16x16x128_f8f6f4 v[88:91], v[234:241], v[18:25], v[88:91]
	v_mfma_f32_16x16x128_f8f6f4 v[84:87], v[242:249], v[18:25], v[84:87]
	v_mfma_f32_16x16x128_f8f6f4 v[72:75], v[234:241], v[26:33], v[72:75]
	v_mfma_f32_16x16x128_f8f6f4 v[68:71], v[242:249], v[26:33], v[68:71]
	v_mfma_f32_16x16x128_f8f6f4 v[56:59], v[234:241], v[218:225], v[56:59]
	v_mfma_f32_16x16x128_f8f6f4 v[52:55], v[242:249], v[218:225], v[52:55]
	v_mfma_f32_16x16x128_f8f6f4 v[48:51], v[234:241], v[226:233], v[48:51]
	v_mfma_f32_16x16x128_f8f6f4 v[44:47], v[242:249], v[226:233], v[44:47]
	s_setprio 0
	s_add_i32 s58, s58, 2
	s_add_u32 s2, s2, 0x100
	s_addc_u32 s3, s3, 0
	s_cmp_gt_u32 s58, 5
	s_barrier
	s_cbranch_scc0 .LBB0_1672
	s_ashr_i32 s0, s8, 2
	s_ashr_i32 s1, s0, 31
	s_lshl_b64 s[0:1], s[0:1], 12
	v_lshl_or_b32 v18, s56, 8, v175
	s_add_u32 s0, s48, s0
	v_lshl_add_u32 v24, s55, 8, v212
	s_addc_u32 s1, s49, s1
	v_ashrrev_i32_e32 v19, 31, v18
	v_ashrrev_i32_e32 v25, 31, v24
	s_nop 15
	s_nop 15
	v_lshl_add_u64 v[10:11], v[18:19], 2, s[0:1]
	v_lshl_add_u64 v[20:21], v[24:25], 2, s[40:41]
	global_load_dwordx4 v[6:9], v[10:11], off offset:16
	global_load_dwordx4 v[14:17], v[10:11], off
	global_load_dwordx4 v[2:5], v[10:11], off offset:528
	s_nop 0
	global_load_dwordx4 v[10:13], v[10:11], off offset:512
	v_lshlrev_b64 v[22:23], 11, v[24:25]
	global_load_dword v30, v[20:21], off
	global_load_dword v182, v[20:21], off offset:64
	global_load_dword v183, v[20:21], off offset:128
	global_load_dword v184, v[20:21], off offset:192
	global_load_dword v185, v[20:21], off offset:512
	global_load_dword v186, v[20:21], off offset:576
	global_load_dword v187, v[20:21], off offset:640
	global_load_dword v188, v[20:21], off offset:704
	v_lshl_add_u64 v[26:27], s[28:29], 0, v[22:23]
	v_lshlrev_b64 v[22:23], 1, v[18:19]
	v_lshl_add_u64 v[18:19], v[26:27], 0, v[22:23]
	v_mov_b32_e32 v180, v217
	v_mov_b32_e32 v178, v216
	v_mov_b32_e32 v176, v215
	v_mov_b32_e32 v174, v214
	s_mov_b32 s8, s10
	s_mov_b32 s56, s53
	s_mov_b32 s55, s54
	s_mov_b64 s[18:19], s[14:15]
	s_waitcnt vmcnt(0)
	v_pk_fma_f32 v[156:157], v[156:157], s[12:13], v[6:7] op_sel_hi:[1,0,1]
	v_pk_fma_f32 v[26:27], v[162:163], s[12:13], v[16:17] op_sel_hi:[1,0,1]
	v_pk_fma_f32 v[28:29], v[160:161], s[12:13], v[14:15] op_sel_hi:[1,0,1]
	v_pk_fma_f32 v[148:149], v[148:149], s[12:13], v[2:3] op_sel_hi:[1,0,1]
	v_pk_fma_f32 v[140:141], v[140:141], s[12:13], v[6:7] op_sel_hi:[1,0,1]
	v_pk_mul_f32 v[32:33], v[26:27], v[30:31] op_sel_hi:[1,0]
	v_pk_mul_f32 v[26:27], v[28:29], v[30:31] op_sel_hi:[1,0]
	v_pk_fma_f32 v[28:29], v[158:159], s[12:13], v[8:9] op_sel_hi:[1,0,1]
	v_cvt_pk_bf16_f32 v26, v26, v27
	v_pk_mul_f32 v[158:159], v[28:29], v[30:31] op_sel_hi:[1,0]
	v_pk_mul_f32 v[28:29], v[156:157], v[30:31] op_sel_hi:[1,0]
	v_cvt_pk_bf16_f32 v27, v32, v33
	v_cvt_pk_bf16_f32 v28, v28, v29
	v_cvt_pk_bf16_f32 v29, v158, v159
	global_store_dwordx4 v[18:19], v[26:29], off
	v_pk_fma_f32 v[132:133], v[132:133], s[12:13], v[2:3] op_sel_hi:[1,0,1]
	v_pk_fma_f32 v[124:125], v[124:125], s[12:13], v[6:7] op_sel_hi:[1,0,1]
	v_pk_fma_f32 v[26:27], v[154:155], s[12:13], v[12:13] op_sel_hi:[1,0,1]
	v_pk_fma_f32 v[28:29], v[152:153], s[12:13], v[10:11] op_sel_hi:[1,0,1]
	v_pk_mul_f32 v[32:33], v[26:27], v[30:31] op_sel_hi:[1,0]
	v_pk_mul_f32 v[26:27], v[28:29], v[30:31] op_sel_hi:[1,0]
	v_pk_fma_f32 v[28:29], v[150:151], s[12:13], v[4:5] op_sel_hi:[1,0,1]
	v_cvt_pk_bf16_f32 v26, v26, v27
	v_pk_mul_f32 v[150:151], v[28:29], v[30:31] op_sel_hi:[1,0]
	v_pk_mul_f32 v[28:29], v[148:149], v[30:31] op_sel_hi:[1,0]
	v_cvt_pk_bf16_f32 v27, v32, v33
	v_cvt_pk_bf16_f32 v28, v28, v29
	v_cvt_pk_bf16_f32 v29, v150, v151
	global_store_dwordx4 v[18:19], v[26:29], off offset:256
	v_pk_fma_f32 v[116:117], v[116:117], s[12:13], v[2:3] op_sel_hi:[1,0,1]
	s_nop 0
	v_or_b32_e32 v26, 16, v24
	v_ashrrev_i32_e32 v27, 31, v26
	v_lshl_add_u64 v[28:29], v[26:27], 2, s[40:41]
	v_mov_b32_e32 v30, v182
	v_lshlrev_b64 v[26:27], 11, v[26:27]
	v_lshl_add_u64 v[26:27], s[28:29], 0, v[26:27]
	v_lshl_add_u64 v[32:33], v[26:27], 0, v[22:23]
	v_pk_fma_f32 v[26:27], v[146:147], s[12:13], v[16:17] op_sel_hi:[1,0,1]
	v_pk_fma_f32 v[28:29], v[144:145], s[12:13], v[14:15] op_sel_hi:[1,0,1]
	v_pk_mul_f32 v[144:145], v[26:27], v[30:31] op_sel_hi:[1,0]
	v_pk_mul_f32 v[26:27], v[28:29], v[30:31] op_sel_hi:[1,0]
	v_pk_fma_f32 v[28:29], v[142:143], s[12:13], v[8:9] op_sel_hi:[1,0,1]
	v_cvt_pk_bf16_f32 v26, v26, v27
	v_pk_mul_f32 v[142:143], v[28:29], v[30:31] op_sel_hi:[1,0]
	v_pk_mul_f32 v[28:29], v[140:141], v[30:31] op_sel_hi:[1,0]
	v_cvt_pk_bf16_f32 v27, v144, v145
	v_cvt_pk_bf16_f32 v28, v28, v29
	v_cvt_pk_bf16_f32 v29, v142, v143
	global_store_dwordx4 v[32:33], v[26:29], off
	s_nop 1
	v_pk_fma_f32 v[26:27], v[138:139], s[12:13], v[12:13] op_sel_hi:[1,0,1]
	v_pk_fma_f32 v[28:29], v[136:137], s[12:13], v[10:11] op_sel_hi:[1,0,1]
	v_pk_mul_f32 v[136:137], v[26:27], v[30:31] op_sel_hi:[1,0]
	v_pk_mul_f32 v[26:27], v[28:29], v[30:31] op_sel_hi:[1,0]
	v_pk_fma_f32 v[28:29], v[134:135], s[12:13], v[4:5] op_sel_hi:[1,0,1]
	v_cvt_pk_bf16_f32 v26, v26, v27
	v_pk_mul_f32 v[134:135], v[28:29], v[30:31] op_sel_hi:[1,0]
	v_pk_mul_f32 v[28:29], v[132:133], v[30:31] op_sel_hi:[1,0]
	v_cvt_pk_bf16_f32 v27, v136, v137
	v_cvt_pk_bf16_f32 v28, v28, v29
	v_cvt_pk_bf16_f32 v29, v134, v135
	global_store_dwordx4 v[32:33], v[26:29], off offset:256
	s_nop 1
	v_or_b32_e32 v26, 32, v24
	v_ashrrev_i32_e32 v27, 31, v26
	v_lshl_add_u64 v[28:29], v[26:27], 2, s[40:41]
	v_mov_b32_e32 v30, v183
	v_lshlrev_b64 v[26:27], 11, v[26:27]
	v_lshl_add_u64 v[26:27], s[28:29], 0, v[26:27]
	v_lshl_add_u64 v[32:33], v[26:27], 0, v[22:23]
	v_pk_fma_f32 v[26:27], v[130:131], s[12:13], v[16:17] op_sel_hi:[1,0,1]
	v_pk_fma_f32 v[28:29], v[128:129], s[12:13], v[14:15] op_sel_hi:[1,0,1]
	v_or_b32_e32 v24, 48, v24
	v_ashrrev_i32_e32 v25, 31, v24
	v_pk_mul_f32 v[128:129], v[26:27], v[30:31] op_sel_hi:[1,0]
	v_pk_mul_f32 v[26:27], v[28:29], v[30:31] op_sel_hi:[1,0]
	v_pk_fma_f32 v[28:29], v[126:127], s[12:13], v[8:9] op_sel_hi:[1,0,1]
	v_cvt_pk_bf16_f32 v26, v26, v27
	v_pk_mul_f32 v[126:127], v[28:29], v[30:31] op_sel_hi:[1,0]
	v_pk_mul_f32 v[28:29], v[124:125], v[30:31] op_sel_hi:[1,0]
	v_cvt_pk_bf16_f32 v27, v128, v129
	v_cvt_pk_bf16_f32 v28, v28, v29
	v_cvt_pk_bf16_f32 v29, v126, v127
	global_store_dwordx4 v[32:33], v[26:29], off
	s_nop 1
	v_pk_fma_f32 v[26:27], v[122:123], s[12:13], v[12:13] op_sel_hi:[1,0,1]
	v_pk_fma_f32 v[28:29], v[120:121], s[12:13], v[10:11] op_sel_hi:[1,0,1]
	v_pk_mul_f32 v[120:121], v[26:27], v[30:31] op_sel_hi:[1,0]
	v_pk_mul_f32 v[26:27], v[28:29], v[30:31] op_sel_hi:[1,0]
	v_pk_fma_f32 v[28:29], v[118:119], s[12:13], v[4:5] op_sel_hi:[1,0,1]
	v_cvt_pk_bf16_f32 v26, v26, v27
	v_pk_mul_f32 v[118:119], v[28:29], v[30:31] op_sel_hi:[1,0]
	v_pk_mul_f32 v[28:29], v[116:117], v[30:31] op_sel_hi:[1,0]
	v_cvt_pk_bf16_f32 v27, v120, v121
	v_cvt_pk_bf16_f32 v28, v28, v29
	v_cvt_pk_bf16_f32 v29, v118, v119
	global_store_dwordx4 v[32:33], v[26:29], off offset:256
	v_pk_fma_f32 v[32:33], v[108:109], s[12:13], v[6:7] op_sel_hi:[1,0,1]
	s_nop 0
	v_lshl_add_u64 v[26:27], v[24:25], 2, s[40:41]
	v_mov_b32_e32 v26, v184
	v_lshlrev_b64 v[24:25], 11, v[24:25]
	v_lshl_add_u64 v[24:25], s[28:29], 0, v[24:25]
	v_lshl_add_u64 v[28:29], v[24:25], 0, v[22:23]
	v_pk_fma_f32 v[22:23], v[114:115], s[12:13], v[16:17] op_sel_hi:[1,0,1]
	v_pk_fma_f32 v[24:25], v[112:113], s[12:13], v[14:15] op_sel_hi:[1,0,1]
	v_pk_mul_f32 v[30:31], v[22:23], v[26:27] op_sel_hi:[1,0]
	v_pk_mul_f32 v[22:23], v[24:25], v[26:27] op_sel_hi:[1,0]
	v_pk_fma_f32 v[24:25], v[110:111], s[12:13], v[8:9] op_sel_hi:[1,0,1]
	v_cvt_pk_bf16_f32 v22, v22, v23
	v_pk_mul_f32 v[108:109], v[24:25], v[26:27] op_sel_hi:[1,0]
	v_pk_mul_f32 v[24:25], v[32:33], v[26:27] op_sel_hi:[1,0]
	v_cvt_pk_bf16_f32 v23, v30, v31
	v_cvt_pk_bf16_f32 v24, v24, v25
	v_cvt_pk_bf16_f32 v25, v108, v109
	global_store_dwordx4 v[28:29], v[22:25], off
	v_pk_fma_f32 v[32:33], v[100:101], s[12:13], v[2:3] op_sel_hi:[1,0,1]
	s_nop 0
	v_pk_fma_f32 v[22:23], v[106:107], s[12:13], v[12:13] op_sel_hi:[1,0,1]
	v_pk_fma_f32 v[24:25], v[104:105], s[12:13], v[10:11] op_sel_hi:[1,0,1]
	v_pk_mul_f32 v[30:31], v[22:23], v[26:27] op_sel_hi:[1,0]
	v_pk_mul_f32 v[22:23], v[24:25], v[26:27] op_sel_hi:[1,0]
	v_pk_fma_f32 v[24:25], v[102:103], s[12:13], v[4:5] op_sel_hi:[1,0,1]
	v_cvt_pk_bf16_f32 v22, v22, v23
	v_pk_mul_f32 v[100:101], v[24:25], v[26:27] op_sel_hi:[1,0]
	v_pk_mul_f32 v[24:25], v[32:33], v[26:27] op_sel_hi:[1,0]
	v_cvt_pk_bf16_f32 v23, v30, v31
	v_cvt_pk_bf16_f32 v24, v24, v25
	v_cvt_pk_bf16_f32 v25, v100, v101
	global_store_dwordx4 v[28:29], v[22:25], off offset:256
	v_mov_b32_e32 v26, v185
	v_pk_fma_f32 v[32:33], v[92:93], s[12:13], v[6:7] op_sel_hi:[1,0,1]
	v_pk_fma_f32 v[22:23], v[98:99], s[12:13], v[16:17] op_sel_hi:[1,0,1]
	v_pk_fma_f32 v[24:25], v[96:97], s[12:13], v[14:15] op_sel_hi:[1,0,1]
	v_lshl_add_u64 v[28:29], v[18:19], 0, s[74:75]
	v_pk_mul_f32 v[30:31], v[22:23], v[26:27] op_sel_hi:[1,0]
	v_pk_mul_f32 v[22:23], v[24:25], v[26:27] op_sel_hi:[1,0]
	v_pk_fma_f32 v[24:25], v[94:95], s[12:13], v[8:9] op_sel_hi:[1,0,1]
	v_cvt_pk_bf16_f32 v22, v22, v23
	v_pk_mul_f32 v[92:93], v[24:25], v[26:27] op_sel_hi:[1,0]
	v_pk_mul_f32 v[24:25], v[32:33], v[26:27] op_sel_hi:[1,0]
	v_cvt_pk_bf16_f32 v23, v30, v31
	v_add_co_u32_e32 v30, vcc, s68, v18
	v_cvt_pk_bf16_f32 v24, v24, v25
	v_cvt_pk_bf16_f32 v25, v92, v93
	v_addc_co_u32_e32 v31, vcc, 0, v19, vcc
	global_store_dwordx4 v[30:31], v[22:25], off
	v_pk_fma_f32 v[32:33], v[84:85], s[12:13], v[2:3] op_sel_hi:[1,0,1]
	s_nop 0
	v_pk_fma_f32 v[22:23], v[90:91], s[12:13], v[12:13] op_sel_hi:[1,0,1]
	v_pk_fma_f32 v[24:25], v[88:89], s[12:13], v[10:11] op_sel_hi:[1,0,1]
	v_pk_mul_f32 v[30:31], v[22:23], v[26:27] op_sel_hi:[1,0]
	v_pk_mul_f32 v[22:23], v[24:25], v[26:27] op_sel_hi:[1,0]
	v_pk_fma_f32 v[24:25], v[86:87], s[12:13], v[4:5] op_sel_hi:[1,0,1]
	v_cvt_pk_bf16_f32 v22, v22, v23
	v_pk_mul_f32 v[84:85], v[24:25], v[26:27] op_sel_hi:[1,0]
	v_pk_mul_f32 v[24:25], v[32:33], v[26:27] op_sel_hi:[1,0]
	v_cvt_pk_bf16_f32 v23, v30, v31
	v_cvt_pk_bf16_f32 v24, v24, v25
	v_cvt_pk_bf16_f32 v25, v84, v85
	global_store_dwordx4 v[28:29], v[22:25], off offset:256
	v_mov_b32_e32 v26, v186
	v_pk_fma_f32 v[32:33], v[76:77], s[12:13], v[6:7] op_sel_hi:[1,0,1]
	v_pk_fma_f32 v[22:23], v[82:83], s[12:13], v[16:17] op_sel_hi:[1,0,1]
	v_pk_fma_f32 v[24:25], v[80:81], s[12:13], v[14:15] op_sel_hi:[1,0,1]
	v_lshl_add_u64 v[28:29], v[18:19], 0, s[78:79]
	v_pk_mul_f32 v[30:31], v[22:23], v[26:27] op_sel_hi:[1,0]
	v_pk_mul_f32 v[22:23], v[24:25], v[26:27] op_sel_hi:[1,0]
	v_pk_fma_f32 v[24:25], v[78:79], s[12:13], v[8:9] op_sel_hi:[1,0,1]
	v_cvt_pk_bf16_f32 v22, v22, v23
	v_pk_mul_f32 v[76:77], v[24:25], v[26:27] op_sel_hi:[1,0]
	v_pk_mul_f32 v[24:25], v[32:33], v[26:27] op_sel_hi:[1,0]
	v_cvt_pk_bf16_f32 v23, v30, v31
	v_add_co_u32_e32 v30, vcc, s69, v18
	v_cvt_pk_bf16_f32 v24, v24, v25
	v_cvt_pk_bf16_f32 v25, v76, v77
	v_addc_co_u32_e32 v31, vcc, 0, v19, vcc
	global_store_dwordx4 v[30:31], v[22:25], off
	v_pk_fma_f32 v[32:33], v[68:69], s[12:13], v[2:3] op_sel_hi:[1,0,1]
	s_nop 0
	v_pk_fma_f32 v[22:23], v[74:75], s[12:13], v[12:13] op_sel_hi:[1,0,1]
	v_pk_fma_f32 v[24:25], v[72:73], s[12:13], v[10:11] op_sel_hi:[1,0,1]
	v_pk_mul_f32 v[30:31], v[22:23], v[26:27] op_sel_hi:[1,0]
	v_pk_mul_f32 v[22:23], v[24:25], v[26:27] op_sel_hi:[1,0]
	v_pk_fma_f32 v[24:25], v[70:71], s[12:13], v[4:5] op_sel_hi:[1,0,1]
	v_cvt_pk_bf16_f32 v22, v22, v23
	v_pk_mul_f32 v[68:69], v[24:25], v[26:27] op_sel_hi:[1,0]
	v_pk_mul_f32 v[24:25], v[32:33], v[26:27] op_sel_hi:[1,0]
	v_cvt_pk_bf16_f32 v23, v30, v31
	v_cvt_pk_bf16_f32 v24, v24, v25
	v_cvt_pk_bf16_f32 v25, v68, v69
	global_store_dwordx4 v[28:29], v[22:25], off offset:256
	v_mov_b32_e32 v26, v187
	v_pk_fma_f32 v[32:33], v[60:61], s[12:13], v[6:7] op_sel_hi:[1,0,1]
	v_pk_fma_f32 v[22:23], v[66:67], s[12:13], v[16:17] op_sel_hi:[1,0,1]
	v_pk_fma_f32 v[24:25], v[64:65], s[12:13], v[14:15] op_sel_hi:[1,0,1]
	v_lshl_add_u64 v[28:29], v[18:19], 0, s[82:83]
	v_pk_fma_f32 v[14:15], v[40:41], s[12:13], v[14:15] op_sel_hi:[1,0,1]
	v_pk_fma_f32 v[16:17], v[42:43], s[12:13], v[16:17] op_sel_hi:[1,0,1]
	v_pk_fma_f32 v[6:7], v[36:37], s[12:13], v[6:7] op_sel_hi:[1,0,1]
	v_pk_mul_f32 v[30:31], v[22:23], v[26:27] op_sel_hi:[1,0]
	v_pk_mul_f32 v[22:23], v[24:25], v[26:27] op_sel_hi:[1,0]
	v_pk_fma_f32 v[24:25], v[62:63], s[12:13], v[8:9] op_sel_hi:[1,0,1]
	v_cvt_pk_bf16_f32 v22, v22, v23
	v_pk_mul_f32 v[60:61], v[24:25], v[26:27] op_sel_hi:[1,0]
	v_pk_mul_f32 v[24:25], v[32:33], v[26:27] op_sel_hi:[1,0]
	v_cvt_pk_bf16_f32 v23, v30, v31
	v_add_co_u32_e32 v30, vcc, s70, v18
	v_cvt_pk_bf16_f32 v24, v24, v25
	v_cvt_pk_bf16_f32 v25, v60, v61
	v_addc_co_u32_e32 v31, vcc, 0, v19, vcc
	global_store_dwordx4 v[30:31], v[22:25], off
	v_pk_fma_f32 v[32:33], v[52:53], s[12:13], v[2:3] op_sel_hi:[1,0,1]
	v_pk_fma_f32 v[8:9], v[38:39], s[12:13], v[8:9] op_sel_hi:[1,0,1]
	v_pk_fma_f32 v[22:23], v[58:59], s[12:13], v[12:13] op_sel_hi:[1,0,1]
	v_pk_fma_f32 v[24:25], v[56:57], s[12:13], v[10:11] op_sel_hi:[1,0,1]
	v_pk_mul_f32 v[30:31], v[22:23], v[26:27] op_sel_hi:[1,0]
	v_pk_mul_f32 v[22:23], v[24:25], v[26:27] op_sel_hi:[1,0]
	v_pk_fma_f32 v[24:25], v[54:55], s[12:13], v[4:5] op_sel_hi:[1,0,1]
	v_cvt_pk_bf16_f32 v22, v22, v23
	v_pk_mul_f32 v[52:53], v[24:25], v[26:27] op_sel_hi:[1,0]
	v_pk_mul_f32 v[24:25], v[32:33], v[26:27] op_sel_hi:[1,0]
	v_cvt_pk_bf16_f32 v23, v30, v31
	v_cvt_pk_bf16_f32 v24, v24, v25
	v_cvt_pk_bf16_f32 v25, v52, v53
	global_store_dwordx4 v[28:29], v[22:25], off offset:256
	v_mov_b32_e32 v20, v188
	v_pk_fma_f32 v[4:5], v[46:47], s[12:13], v[4:5] op_sel_hi:[1,0,1]
	v_pk_fma_f32 v[2:3], v[44:45], s[12:13], v[2:3] op_sel_hi:[1,0,1]
	v_lshl_add_u64 v[22:23], v[18:19], 0, s[84:85]
	v_pk_mul_f32 v[14:15], v[14:15], v[20:21] op_sel_hi:[1,0]
	v_pk_mul_f32 v[16:17], v[16:17], v[20:21] op_sel_hi:[1,0]
	v_pk_mul_f32 v[24:25], v[8:9], v[20:21] op_sel_hi:[1,0]
	v_pk_mul_f32 v[8:9], v[6:7], v[20:21] op_sel_hi:[1,0]
	v_cvt_pk_bf16_f32 v6, v14, v15
	v_add_co_u32_e32 v14, vcc, s71, v18
	v_cvt_pk_bf16_f32 v7, v16, v17
	v_cvt_pk_bf16_f32 v8, v8, v9
	v_cvt_pk_bf16_f32 v9, v24, v25
	v_addc_co_u32_e32 v15, vcc, 0, v19, vcc
	global_store_dwordx4 v[14:15], v[6:9], off
	s_and_b64 vcc, exec, s[38:39]
	s_nop 0
	v_pk_fma_f32 v[6:7], v[50:51], s[12:13], v[12:13] op_sel_hi:[1,0,1]
	v_pk_fma_f32 v[8:9], v[48:49], s[12:13], v[10:11] op_sel_hi:[1,0,1]
	v_pk_mul_f32 v[6:7], v[6:7], v[20:21] op_sel_hi:[1,0]
	v_pk_mul_f32 v[8:9], v[8:9], v[20:21] op_sel_hi:[1,0]
	v_pk_mul_f32 v[10:11], v[4:5], v[20:21] op_sel_hi:[1,0]
	v_pk_mul_f32 v[4:5], v[2:3], v[20:21] op_sel_hi:[1,0]
	v_cvt_pk_bf16_f32 v2, v8, v9
	v_cvt_pk_bf16_f32 v3, v6, v7
	v_cvt_pk_bf16_f32 v4, v4, v5
	v_cvt_pk_bf16_f32 v5, v10, v11
	global_store_dwordx4 v[22:23], v[2:5], off offset:256
	s_cbranch_vccz .LBB0_1663
	s_waitcnt vmcnt(0)
	s_cmpk_gt_u32 s25, 0xff
	v_readlane_b32 s52, v255, 32
	s_cbranch_scc1 .LBB0_1676
	s_barrier

.LBB0_1731:
	s_add_u32 s0, s84, s6
	s_addc_u32 s1, s85, s7
	s_add_u32 s8, s0, 0x2bc10000
	s_addc_u32 s9, s1, 0
	v_mov_b32_e32 v11, 0x2bc10000
	global_load_dwordx4 v[2:5], v35, s[8:9] offset:16
	global_load_dwordx4 v[36:39], v11, s[0:1]
	v_lshl_add_u64 v[30:31], s[84:85], 0, v[28:29]
	s_mov_b32 s0, 0x178000
	v_add_co_u32_e32 v32, vcc, s0, v30
	v_lshlrev_b32_e32 v11, 1, v10
	s_nop 0
	v_addc_co_u32_e32 v33, vcc, 0, v31, vcc
	global_load_dwordx2 v[40:41], v[32:33], off
	v_lshlrev_b32_e32 v34, 2, v6
	v_lshlrev_b32_e32 v13, 2, v12
	v_lshlrev_b32_e32 v15, 2, v10
	s_waitcnt vmcnt(0)
	v_lshlrev_b32_e32 v76, 16, v40
	v_and_b32_e32 v77, 0xffff0000, v40
	v_lshlrev_b32_e32 v74, 16, v41
	v_and_b32_e32 v75, 0xffff0000, v41
	v_ashrrev_i32_e32 v41, 31, v36
	v_mov_b32_e32 v40, v36
	v_lshlrev_b64 v[40:41], 11, v[40:41]
	v_lshl_add_u64 v[42:43], v[8:9], 0, v[40:41]
	global_load_dwordx2 v[114:115], v[42:43], off
	v_ashrrev_i32_e32 v43, 31, v37
	v_mov_b32_e32 v42, v37
	v_lshlrev_b64 v[36:37], 11, v[42:43]
	v_lshl_add_u64 v[42:43], v[8:9], 0, v[36:37]
	global_load_dwordx2 v[116:117], v[42:43], off
	v_ashrrev_i32_e32 v43, 31, v38
	v_mov_b32_e32 v42, v38
	v_lshlrev_b64 v[42:43], 11, v[42:43]
	v_lshl_add_u64 v[44:45], v[8:9], 0, v[42:43]
	global_load_dwordx2 v[118:119], v[44:45], off
	v_ashrrev_i32_e32 v45, 31, v39
	v_mov_b32_e32 v44, v39
	v_lshl_add_u64 v[36:37], s[4:5], 0, v[36:37]
	v_lshlrev_b64 v[38:39], 11, v[44:45]
	v_readfirstlane_b32 s10, v36
	v_readfirstlane_b32 s11, v37
	v_lshl_add_u64 v[36:37], s[4:5], 0, v[42:43]
	v_lshl_add_u64 v[40:41], s[4:5], 0, v[40:41]
	v_readfirstlane_b32 s14, v36
	v_readfirstlane_b32 s15, v37
	v_lshl_add_u64 v[36:37], s[4:5], 0, v[38:39]
	v_lshl_add_u64 v[44:45], v[8:9], 0, v[38:39]
	v_readfirstlane_b32 s8, v40
	v_readfirstlane_b32 s9, v41
	v_readfirstlane_b32 s16, v36
	v_readfirstlane_b32 s17, v37
	global_load_dwordx2 v[120:121], v[44:45], off
	s_nop 0
	global_load_dwordx2 v[44:45], v[32:33], off offset:512
	global_load_dwordx2 v[106:107], v11, s[8:9]
	global_load_dwordx2 v[108:109], v11, s[10:11]
	global_load_dwordx2 v[110:111], v11, s[14:15]
	global_load_dwordx2 v[112:113], v11, s[16:17]
	global_load_dwordx2 v[36:37], v[32:33], off offset:1024
	s_waitcnt vmcnt(0)
	v_lshlrev_b32_e32 v122, 16, v120
	v_lshlrev_b32_e32 v80, 16, v44
	v_and_b32_e32 v81, 0xffff0000, v44
	v_lshlrev_b32_e32 v78, 16, v45
	v_and_b32_e32 v79, 0xffff0000, v45
	v_lshlrev_b32_e32 v84, 16, v36
	v_and_b32_e32 v85, 0xffff0000, v36
	v_lshlrev_b32_e32 v82, 16, v37
	v_and_b32_e32 v83, 0xffff0000, v37
	global_load_dwordx2 v[104:105], v1, s[8:9]
	global_load_dwordx2 v[102:103], v1, s[10:11]
	global_load_dwordx2 v[100:101], v1, s[14:15]
	global_load_dwordx2 v[90:91], v1, s[16:17]
	global_load_dwordx2 v[36:37], v[32:33], off offset:1536
	global_load_dwordx2 v[98:99], v7, s[8:9]
	global_load_dwordx2 v[96:97], v7, s[10:11]
	global_load_dwordx2 v[94:95], v7, s[14:15]
	global_load_dwordx2 v[92:93], v7, s[16:17]
	global_load_dwordx2 v[66:67], v[32:33], off offset:2048
	v_and_b32_e32 v123, 0xffff0000, v120
	s_waitcnt vmcnt(0)
	v_lshlrev_b32_e32 v86, 16, v36
	v_and_b32_e32 v87, 0xffff0000, v36
	v_lshlrev_b32_e32 v88, 16, v37
	v_and_b32_e32 v89, 0xffff0000, v37
	v_ashrrev_i32_e32 v37, 31, v2
	v_mov_b32_e32 v36, v2
	v_lshlrev_b64 v[36:37], 11, v[36:37]
	v_lshl_add_u64 v[38:39], v[8:9], 0, v[36:37]
	global_load_dwordx2 v[58:59], v[38:39], off
	v_ashrrev_i32_e32 v39, 31, v3
	v_mov_b32_e32 v38, v3
	v_lshlrev_b64 v[2:3], 11, v[38:39]
	v_lshl_add_u64 v[38:39], v[8:9], 0, v[2:3]
	global_load_dwordx2 v[60:61], v[38:39], off
	v_ashrrev_i32_e32 v39, 31, v4
	v_mov_b32_e32 v38, v4
	v_lshlrev_b64 v[38:39], 11, v[38:39]
	v_lshl_add_u64 v[40:41], v[8:9], 0, v[38:39]
	global_load_dwordx2 v[62:63], v[40:41], off
	v_ashrrev_i32_e32 v41, 31, v5
	v_mov_b32_e32 v40, v5
	v_lshl_add_u64 v[2:3], s[4:5], 0, v[2:3]
	v_lshlrev_b64 v[4:5], 11, v[40:41]
	v_readfirstlane_b32 s8, v2
	v_readfirstlane_b32 s9, v3
	v_lshl_add_u64 v[2:3], s[4:5], 0, v[38:39]
	v_lshl_add_u64 v[36:37], s[4:5], 0, v[36:37]
	v_readfirstlane_b32 s10, v2
	v_readfirstlane_b32 s11, v3
	v_lshl_add_u64 v[2:3], s[4:5], 0, v[4:5]
	v_lshl_add_u64 v[40:41], v[8:9], 0, v[4:5]
	v_readfirstlane_b32 s0, v36
	v_readfirstlane_b32 s1, v37
	v_readfirstlane_b32 s14, v2
	v_readfirstlane_b32 s15, v3
	global_load_dwordx2 v[64:65], v[40:41], off
	global_load_dwordx2 v[68:69], v[32:33], off offset:2560
	global_load_dwordx2 v[52:53], v11, s[8:9]
	global_load_dwordx2 v[50:51], v11, s[0:1]
	global_load_dwordx2 v[54:55], v11, s[10:11]
	global_load_dwordx2 v[56:57], v11, s[14:15]
	global_load_dwordx2 v[70:71], v[32:33], off offset:3072
	global_load_dwordx2 v[48:49], v1, s[0:1]
	global_load_dwordx2 v[46:47], v1, s[8:9]
	global_load_dwordx2 v[44:45], v1, s[10:11]
	global_load_dwordx2 v[42:43], v1, s[14:15]
	global_load_dwordx2 v[72:73], v[32:33], off offset:3584
	global_load_dwordx2 v[40:41], v7, s[0:1]
	global_load_dwordx2 v[38:39], v7, s[8:9]
	global_load_dwordx2 v[36:37], v7, s[10:11]
	s_nop 0
	global_load_dwordx2 v[32:33], v7, s[14:15]
	s_ashr_i32 s0, s2, 31
	s_lshr_b32 s0, s0, 20
	s_add_i32 s0, s2, s0
	s_ashr_i32 s0, s0, 12
	s_cmpk_lt_i32 s2, 0x4000
	v_lshlrev_b32_e32 v2, 16, v114
	v_and_b32_e32 v3, 0xffff0000, v114
	v_lshlrev_b32_e32 v4, 16, v116
	v_and_b32_e32 v5, 0xffff0000, v116
	s_cselect_b32 s0, s0, 4
	v_pk_add_f32 v[2:3], v[2:3], v[4:5]
	v_lshlrev_b32_e32 v4, 16, v118
	v_and_b32_e32 v5, 0xffff0000, v118
	s_mul_i32 s10, s0, 0x6000
	v_pk_add_f32 v[4:5], v[4:5], v[122:123]
	s_mul_hi_i32 s3, s0, 0x6000
	s_add_u32 s8, s18, s10
	v_pk_add_f32 v[2:3], v[2:3], v[4:5]
	v_lshlrev_b32_e32 v4, 16, v115
	v_and_b32_e32 v5, 0xffff0000, v115
	v_lshlrev_b32_e32 v114, 16, v117
	v_and_b32_e32 v115, 0xffff0000, v117
	s_addc_u32 s9, s19, s3
	v_pk_add_f32 v[4:5], v[4:5], v[114:115]
	v_lshlrev_b32_e32 v114, 16, v119
	v_and_b32_e32 v115, 0xffff0000, v119
	v_lshlrev_b32_e32 v116, 16, v121
	v_and_b32_e32 v117, 0xffff0000, v121
	v_pk_add_f32 v[114:115], v[114:115], v[116:117]
	v_lshl_add_u64 v[116:117], s[8:9], 0, v[34:35]
	s_mov_b64 s[0:1], 0x5000
	v_pk_add_f32 v[4:5], v[4:5], v[114:115]
	v_lshl_add_u64 v[114:115], v[116:117], 0, s[0:1]
	v_add_co_u32_e32 v116, vcc, s28, v116
	v_readlane_b32 s8, v255, 48
	s_nop 0
	v_addc_co_u32_e32 v117, vcc, 0, v117, vcc
	global_load_dwordx4 v[116:119], v[116:117], off
	v_readlane_b32 s9, v255, 49
	s_mov_b64 s[0:1], -1
	s_and_b64 vcc, exec, s[8:9]
	v_lshlrev_b32_e32 v11, 2, v14
	s_waitcnt vmcnt(0)
	v_pk_fma_f32 v[74:75], v[4:5], v[118:119], v[74:75]
	v_pk_fma_f32 v[76:77], v[2:3], v[116:117], v[76:77]
	v_lshlrev_b32_e32 v2, 16, v106
	v_and_b32_e32 v3, 0xffff0000, v106
	v_lshlrev_b32_e32 v4, 16, v108
	v_and_b32_e32 v5, 0xffff0000, v108
	v_pk_add_f32 v[2:3], v[2:3], v[4:5]
	v_lshlrev_b32_e32 v4, 16, v110
	v_and_b32_e32 v5, 0xffff0000, v110
	v_lshlrev_b32_e32 v116, 16, v112
	v_and_b32_e32 v117, 0xffff0000, v112
	v_pk_add_f32 v[4:5], v[4:5], v[116:117]
	v_lshlrev_b32_e32 v106, 16, v113
	v_pk_add_f32 v[116:117], v[2:3], v[4:5]
	v_lshlrev_b32_e32 v2, 16, v107
	v_and_b32_e32 v3, 0xffff0000, v107
	v_lshlrev_b32_e32 v4, 16, v109
	v_and_b32_e32 v5, 0xffff0000, v109
	v_pk_add_f32 v[2:3], v[2:3], v[4:5]
	v_lshlrev_b32_e32 v4, 16, v111
	v_and_b32_e32 v5, 0xffff0000, v111
	v_and_b32_e32 v107, 0xffff0000, v113
	v_pk_add_f32 v[4:5], v[4:5], v[106:107]
	s_nop 0
	v_pk_add_f32 v[106:107], v[2:3], v[4:5]
	global_load_dwordx4 v[2:5], v[114:115], off offset:1024
	s_waitcnt vmcnt(0)
	v_pk_fma_f32 v[78:79], v[106:107], v[4:5], v[78:79]
	v_pk_fma_f32 v[80:81], v[116:117], v[2:3], v[80:81]
	v_lshlrev_b32_e32 v2, 16, v104
	v_and_b32_e32 v3, 0xffff0000, v104
	v_lshlrev_b32_e32 v4, 16, v102
	v_and_b32_e32 v5, 0xffff0000, v102
	v_pk_add_f32 v[2:3], v[2:3], v[4:5]
	v_lshlrev_b32_e32 v4, 16, v100
	v_and_b32_e32 v5, 0xffff0000, v100
	v_lshlrev_b32_e32 v106, 16, v90
	v_and_b32_e32 v107, 0xffff0000, v90
	v_pk_add_f32 v[4:5], v[4:5], v[106:107]
	v_lshlrev_b32_e32 v90, 16, v91
	v_pk_add_f32 v[106:107], v[2:3], v[4:5]
	v_lshlrev_b32_e32 v2, 16, v105
	v_and_b32_e32 v3, 0xffff0000, v105
	v_lshlrev_b32_e32 v4, 16, v103
	v_and_b32_e32 v5, 0xffff0000, v103
	v_pk_add_f32 v[2:3], v[2:3], v[4:5]
	v_lshlrev_b32_e32 v4, 16, v101
	v_and_b32_e32 v5, 0xffff0000, v101
	v_and_b32_e32 v91, 0xffff0000, v91
	v_pk_add_f32 v[4:5], v[4:5], v[90:91]
	s_nop 0
	v_pk_add_f32 v[90:91], v[2:3], v[4:5]
	global_load_dwordx4 v[2:5], v[114:115], off offset:2048
	s_waitcnt vmcnt(0)
	v_pk_fma_f32 v[82:83], v[90:91], v[4:5], v[82:83]
	v_pk_fma_f32 v[84:85], v[106:107], v[2:3], v[84:85]
	v_lshlrev_b32_e32 v2, 16, v98
	v_and_b32_e32 v3, 0xffff0000, v98
	v_lshlrev_b32_e32 v4, 16, v96
	v_and_b32_e32 v5, 0xffff0000, v96
	v_pk_add_f32 v[2:3], v[2:3], v[4:5]
	v_lshlrev_b32_e32 v4, 16, v94
	v_and_b32_e32 v5, 0xffff0000, v94
	v_lshlrev_b32_e32 v90, 16, v92
	v_and_b32_e32 v91, 0xffff0000, v92
	v_pk_add_f32 v[4:5], v[4:5], v[90:91]
	v_lshlrev_b32_e32 v92, 16, v93
	v_pk_add_f32 v[90:91], v[2:3], v[4:5]
	v_lshlrev_b32_e32 v2, 16, v99
	v_and_b32_e32 v3, 0xffff0000, v99
	v_lshlrev_b32_e32 v4, 16, v97
	v_and_b32_e32 v5, 0xffff0000, v97
	v_pk_add_f32 v[2:3], v[2:3], v[4:5]
	v_lshlrev_b32_e32 v4, 16, v95
	v_and_b32_e32 v5, 0xffff0000, v95
	v_and_b32_e32 v93, 0xffff0000, v93
	v_pk_add_f32 v[4:5], v[4:5], v[92:93]
	v_pk_mul_f32 v[96:97], v[76:77], v[76:77]
	v_pk_add_f32 v[92:93], v[2:3], v[4:5]
	global_load_dwordx4 v[2:5], v[114:115], off offset:3072
	v_pk_mul_f32 v[94:95], v[80:81], v[80:81]
	s_waitcnt vmcnt(0)
	v_pk_fma_f32 v[88:89], v[92:93], v[4:5], v[88:89]
	v_pk_fma_f32 v[86:87], v[90:91], v[2:3], v[86:87]
	v_mul_f32_e32 v4, v88, v88
	v_mul_f32_e32 v92, v86, v86
	v_mul_f32_e32 v90, v87, v87
	v_mul_f32_e32 v2, v89, v89
	s_cbranch_vccz .LBB0_1733
	s_mov_b64 s[0:1], 0x178000
	v_lshl_add_u64 v[98:99], v[30:31], 0, s[0:1]
	s_mov_b64 s[0:1], 0x178200
	v_cvt_pk_bf16_f32 v106, v76, v77
	v_cvt_pk_bf16_f32 v107, v74, v75
	v_lshl_add_u64 v[100:101], v[30:31], 0, s[0:1]
	s_mov_b64 s[0:1], 0x178400
	global_store_dwordx2 v[98:99], v[106:107], off
	v_cvt_pk_bf16_f32 v98, v80, v81
	v_cvt_pk_bf16_f32 v99, v78, v79
	v_lshl_add_u64 v[102:103], v[30:31], 0, s[0:1]
	s_mov_b64 s[0:1], 0x178600
	global_store_dwordx2 v[100:101], v[98:99], off
	v_cvt_pk_bf16_f32 v98, v84, v85
	v_cvt_pk_bf16_f32 v99, v82, v83
	v_lshl_add_u64 v[104:105], v[30:31], 0, s[0:1]
	global_store_dwordx2 v[102:103], v[98:99], off
	v_cvt_pk_bf16_f32 v98, v86, v87
	v_cvt_pk_bf16_f32 v99, v88, v89
	global_store_dwordx2 v[104:105], v[98:99], off
	v_pk_mul_f32 v[98:99], v[74:75], v[74:75]
	v_mov_b32_e32 v100, v96
	v_mov_b32_e32 v101, v99
	v_pk_mov_b32 v[98:99], v[96:97], v[98:99] op_sel:[1,0]
	s_add_u32 s8, s22, s10
	v_pk_add_f32 v[98:99], v[98:99], v[100:101]
	v_mov_b32_e32 v100, v94
	v_pk_add_f32 v[110:111], v[98:99], v[98:99] op_sel_hi:[0,1]
	v_pk_mul_f32 v[98:99], v[78:79], v[78:79]
	s_addc_u32 s9, s23, s3
	v_mov_b32_e32 v101, v99
	v_pk_mov_b32 v[98:99], v[94:95], v[98:99] op_sel:[1,0]
	s_add_u32 s10, s8, 0x1000
	v_pk_add_f32 v[98:99], v[98:99], v[100:101]
	s_addc_u32 s11, s9, 0
	v_pk_add_f32 v[112:113], v[98:99], v[98:99] op_sel_hi:[0,1]
	v_mul_f32_e32 v98, v84, v84
	v_pk_fma_f32 v[114:115], v[84:85], v[84:85], v[98:99] op_sel_hi:[1,1,0]
	v_mul_f32_e32 v98, v82, v82
	v_pk_fma_f32 v[116:117], v[82:83], v[82:83], v[98:99] op_sel_hi:[1,1,0]
	global_load_dwordx4 v[98:101], v[16:17], off
	global_load_dwordx4 v[102:105], v34, s[8:9]
	global_load_dwordx4 v[106:109], v34, s[10:11]
	v_mov_b32_e32 v5, v111
	v_mov_b32_e32 v3, v113
	v_mov_b32_e32 v93, v115
	v_mov_b32_e32 v91, v117
	v_pk_add_f32 v[110:111], v[4:5], v[2:3]
	v_and_b32_e32 v5, 64, v203
	v_pk_add_f32 v[114:115], v[92:93], v[90:91]
	v_add_u32_e32 v5, 64, v5
	v_xor_b32_e32 v91, 1, v203
	v_cmp_lt_i32_e32 vcc, v91, v5
	v_pk_add_f32 v[110:111], v[114:115], v[110:111]
	s_mov_b32 s0, 0x4578000
	v_cndmask_b32_e32 v91, v203, v91, vcc
	v_add_f32_e32 v3, v110, v111
	v_lshlrev_b32_e32 v91, 2, v91
	s_nop 1
	v_mov_b32_dpp v91, v3 quad_perm:[1,0,3,2] row_mask:0xf bank_mask:0xf
	s_waitcnt lgkmcnt(0)
	v_add_f32_e32 v3, v3, v91
	v_xor_b32_e32 v91, 2, v203
	v_cmp_lt_i32_e32 vcc, v91, v5
	s_waitcnt vmcnt(0)
	v_pk_add_f32 v[108:109], v[108:109], 1.0 op_sel_hi:[1,0]
	v_cndmask_b32_e32 v91, v203, v91, vcc
	v_lshlrev_b32_e32 v91, 2, v91
	s_nop 1
	v_mov_b32_dpp v91, v3 quad_perm:[2,3,0,1] row_mask:0xf bank_mask:0xf
	v_pk_add_f32 v[106:107], v[106:107], 1.0 op_sel_hi:[1,0]
	s_waitcnt lgkmcnt(0)
	v_add_f32_e32 v3, v3, v91
	v_xor_b32_e32 v91, 4, v203
	v_cmp_lt_i32_e32 vcc, v91, v5
	s_nop 1
	v_cndmask_b32_e32 v91, v203, v91, vcc
	v_lshlrev_b32_e32 v91, 2, v91
	s_nop 1
	v_mov_b32_dpp v91, v3 row_half_mirror row_mask:0xf bank_mask:0xf
	s_waitcnt lgkmcnt(0)
	v_add_f32_e32 v3, v3, v91
	v_xor_b32_e32 v91, 8, v203
	v_cmp_lt_i32_e32 vcc, v91, v5
	s_nop 1
	v_cndmask_b32_e32 v91, v203, v91, vcc
	v_lshlrev_b32_e32 v91, 2, v91
	s_nop 1
	v_mov_b32_dpp v91, v3 row_mirror row_mask:0xf bank_mask:0xf
	s_waitcnt lgkmcnt(0)
	v_add_f32_e32 v3, v3, v91
	v_xor_b32_e32 v91, 16, v203
	v_cmp_lt_i32_e32 vcc, v91, v5
	s_nop 1
	v_cndmask_b32_e32 v91, v203, v91, vcc
	v_lshlrev_b32_e32 v91, 2, v91
	v_mov_b32_e32 v91, v3
	s_nop 1
	v_permlane16_swap_b32_e32 v91, v3
	s_waitcnt lgkmcnt(0)
	v_add_f32_e32 v3, v3, v91
	v_xor_b32_e32 v91, 32, v203
	v_cmp_lt_i32_e32 vcc, v91, v5
	s_nop 1
	v_cndmask_b32_e32 v5, v203, v91, vcc
	v_lshlrev_b32_e32 v5, 2, v5
	v_mov_b32_e32 v5, v3
	s_nop 1
	v_permlane32_swap_b32_e32 v5, v3
	s_waitcnt lgkmcnt(0)
	v_add_f32_e32 v3, v3, v5
	v_fmamk_f32 v3, v3, 0x3a800000, v165
	v_rsq_f32_e32 v110, v3
	s_nop 0
	v_pk_mul_f32 v[112:113], v[74:75], v[110:111] op_sel_hi:[1,0]
	v_pk_mul_f32 v[114:115], v[76:77], v[110:111] op_sel_hi:[1,0]
	v_pk_mul_f32 v[100:101], v[100:101], v[112:113]
	v_pk_mul_f32 v[98:99], v[98:99], v[114:115]
	v_pk_fma_f32 v[100:101], v[108:109], v[100:101], v[104:105]
	v_pk_fma_f32 v[98:99], v[106:107], v[98:99], v[102:103]
	v_add_co_u32_e32 v112, vcc, s0, v30
	v_cvt_pk_bf16_f32 v98, v98, v99
	v_cvt_pk_bf16_f32 v99, v100, v101
	v_addc_co_u32_e32 v113, vcc, 0, v31, vcc
	global_store_dwordx2 v[112:113], v[98:99], off
	global_load_dwordx4 v[98:101], v[18:19], off
	s_nop 0
	global_load_dwordx4 v[102:105], v15, s[10:11]
	global_load_dwordx4 v[106:109], v34, s[8:9] offset:1024
	v_pk_mul_f32 v[114:115], v[78:79], v[110:111] op_sel_hi:[1,0]
	v_pk_mul_f32 v[116:117], v[80:81], v[110:111] op_sel_hi:[1,0]
	s_mov_b64 s[0:1], 0
	s_waitcnt vmcnt(2)
	v_pk_mul_f32 v[98:99], v[98:99], v[116:117]
	v_pk_mul_f32 v[100:101], v[100:101], v[114:115]
	s_waitcnt vmcnt(1)
	v_pk_add_f32 v[104:105], v[104:105], 1.0 op_sel_hi:[1,0]
	v_pk_add_f32 v[102:103], v[102:103], 1.0 op_sel_hi:[1,0]
	s_waitcnt vmcnt(0)
	v_pk_fma_f32 v[100:101], v[104:105], v[100:101], v[108:109]
	v_pk_fma_f32 v[98:99], v[102:103], v[98:99], v[106:107]
	v_pk_mul_f32 v[114:115], v[82:83], v[110:111] op_sel_hi:[1,0]
	v_cvt_pk_bf16_f32 v98, v98, v99
	v_cvt_pk_bf16_f32 v99, v100, v101
	global_store_dwordx2 v[112:113], v[98:99], off offset:512
	global_load_dwordx4 v[98:101], v[20:21], off
	s_nop 0
	global_load_dwordx4 v[102:105], v13, s[10:11]
	global_load_dwordx4 v[106:109], v34, s[8:9] offset:2048
	v_pk_mul_f32 v[116:117], v[84:85], v[110:111] op_sel_hi:[1,0]
	s_waitcnt vmcnt(2)
	v_pk_mul_f32 v[100:101], v[114:115], v[100:101]
	v_pk_mul_f32 v[98:99], v[116:117], v[98:99]
	s_waitcnt vmcnt(1)
	v_pk_add_f32 v[104:105], v[104:105], 1.0 op_sel_hi:[1,0]
	v_pk_add_f32 v[102:103], v[102:103], 1.0 op_sel_hi:[1,0]
	s_waitcnt vmcnt(0)
	v_pk_fma_f32 v[100:101], v[100:101], v[104:105], v[108:109]
	v_pk_fma_f32 v[98:99], v[98:99], v[102:103], v[106:107]
	v_pk_mul_f32 v[114:115], v[88:89], v[110:111] op_sel_hi:[1,0]
	v_cvt_pk_bf16_f32 v98, v98, v99
	v_cvt_pk_bf16_f32 v99, v100, v101
	global_store_dwordx2 v[112:113], v[98:99], off offset:1024
	global_load_dwordx4 v[98:101], v[22:23], off
	s_nop 0
	global_load_dwordx4 v[102:105], v11, s[10:11]
	global_load_dwordx4 v[106:109], v34, s[8:9] offset:3072
	v_pk_mul_f32 v[110:111], v[86:87], v[110:111] op_sel_hi:[1,0]
	s_waitcnt vmcnt(2)
	v_pk_mul_f32 v[100:101], v[114:115], v[100:101]
	v_pk_mul_f32 v[98:99], v[110:111], v[98:99]
	s_waitcnt vmcnt(1)
	v_pk_add_f32 v[104:105], v[104:105], 1.0 op_sel_hi:[1,0]
	v_pk_add_f32 v[102:103], v[102:103], 1.0 op_sel_hi:[1,0]
	s_waitcnt vmcnt(0)
	v_pk_fma_f32 v[100:101], v[100:101], v[104:105], v[108:109]
	v_pk_fma_f32 v[98:99], v[98:99], v[102:103], v[106:107]
	s_nop 0
	v_cvt_pk_bf16_f32 v98, v98, v99
	v_cvt_pk_bf16_f32 v99, v100, v101
	global_store_dwordx2 v[112:113], v[98:99], off offset:1536
.LBB0_1733:
	s_andn2_b64 vcc, exec, s[0:1]
	s_cbranch_vccnz .LBB0_1735
	v_pk_mul_f32 v[98:99], v[74:75], v[74:75]
	v_mov_b32_e32 v100, v96
	v_mov_b32_e32 v101, v99
	v_pk_mov_b32 v[96:97], v[96:97], v[98:99] op_sel:[1,0]
	v_pk_mul_f32 v[98:99], v[78:79], v[78:79]
	v_pk_add_f32 v[96:97], v[96:97], v[100:101]
	v_mov_b32_e32 v100, v94
	v_mov_b32_e32 v101, v99
	v_pk_mov_b32 v[94:95], v[94:95], v[98:99] op_sel:[1,0]
	v_pk_add_f32 v[96:97], v[96:97], v[96:97] op_sel:[0,1] op_sel_hi:[1,0]
	v_pk_add_f32 v[94:95], v[94:95], v[100:101]
	v_mov_b32_e32 v97, v92
	v_pk_add_f32 v[92:93], v[94:95], v[94:95] op_sel:[0,1] op_sel_hi:[1,0]
	s_nop 0
	v_mov_b32_e32 v93, v90
	v_pk_add_f32 v[90:91], v[96:97], v[92:93]
	v_mul_f32_e32 v92, v85, v85
	v_pk_fma_f32 v[92:93], v[84:85], v[84:85], v[92:93] op_sel_hi:[1,1,0]
	s_nop 0
	v_mov_b32_e32 v93, v4
	v_mul_f32_e32 v4, v83, v83
	v_pk_fma_f32 v[4:5], v[82:83], v[82:83], v[4:5] op_sel_hi:[1,1,0]
	s_nop 0
	v_mov_b32_e32 v5, v2
	v_pk_add_f32 v[2:3], v[92:93], v[4:5]
	v_xor_b32_e32 v4, 1, v203
	v_pk_add_f32 v[2:3], v[90:91], v[2:3]
	s_nop 0
	v_add_f32_e32 v2, v2, v3
	v_and_b32_e32 v3, 64, v203
	v_add_u32_e32 v3, 64, v3
	v_cmp_lt_i32_e32 vcc, v4, v3
	s_nop 1
	v_cndmask_b32_e32 v4, v203, v4, vcc
	v_lshlrev_b32_e32 v4, 2, v4
	s_nop 1
	v_mov_b32_dpp v4, v2 quad_perm:[1,0,3,2] row_mask:0xf bank_mask:0xf
	s_waitcnt lgkmcnt(0)
	v_add_f32_e32 v2, v2, v4
	v_xor_b32_e32 v4, 2, v203
	v_cmp_lt_i32_e32 vcc, v4, v3
	s_nop 1
	v_cndmask_b32_e32 v4, v203, v4, vcc
	v_lshlrev_b32_e32 v4, 2, v4
	s_nop 1
	v_mov_b32_dpp v4, v2 quad_perm:[2,3,0,1] row_mask:0xf bank_mask:0xf
	s_waitcnt lgkmcnt(0)
	v_add_f32_e32 v2, v2, v4
	v_xor_b32_e32 v4, 4, v203
	v_cmp_lt_i32_e32 vcc, v4, v3
	s_nop 1
	v_cndmask_b32_e32 v4, v203, v4, vcc
	v_lshlrev_b32_e32 v4, 2, v4
	s_nop 1
	v_mov_b32_dpp v4, v2 row_half_mirror row_mask:0xf bank_mask:0xf
	s_waitcnt lgkmcnt(0)
	v_add_f32_e32 v2, v2, v4
	v_xor_b32_e32 v4, 8, v203
	v_cmp_lt_i32_e32 vcc, v4, v3
	s_nop 1
	v_cndmask_b32_e32 v4, v203, v4, vcc
	v_lshlrev_b32_e32 v4, 2, v4
	s_nop 1
	v_mov_b32_dpp v4, v2 row_mirror row_mask:0xf bank_mask:0xf
	s_waitcnt lgkmcnt(0)
	v_add_f32_e32 v2, v2, v4
	v_xor_b32_e32 v4, 16, v203
	v_cmp_lt_i32_e32 vcc, v4, v3
	s_nop 1
	v_cndmask_b32_e32 v4, v203, v4, vcc
	v_lshlrev_b32_e32 v4, 2, v4
	v_mov_b32_e32 v4, v2
	s_nop 1
	v_permlane16_swap_b32_e32 v4, v2
	s_waitcnt lgkmcnt(0)
	v_add_f32_e32 v2, v2, v4
	v_xor_b32_e32 v4, 32, v203
	v_cmp_lt_i32_e32 vcc, v4, v3
	s_nop 1
	v_cndmask_b32_e32 v3, v203, v4, vcc
	v_lshlrev_b32_e32 v3, 2, v3
	v_mov_b32_e32 v3, v2
	s_nop 1
	v_permlane32_swap_b32_e32 v3, v2
	s_waitcnt lgkmcnt(0)
	v_add_f32_e32 v2, v2, v3
	v_fmamk_f32 v2, v2, 0x3a800000, v165
	v_rsq_f32_e32 v90, v2
	global_load_dwordx4 v[2:5], v[24:25], off
	v_pk_mul_f32 v[76:77], v[76:77], v[90:91] op_sel_hi:[1,0]
	v_pk_mul_f32 v[74:75], v[74:75], v[90:91] op_sel_hi:[1,0]
	s_waitcnt vmcnt(0)
	v_pk_mul_f32 v[2:3], v[2:3], v[76:77]
	v_pk_mul_f32 v[4:5], v[4:5], v[74:75]
	global_store_dwordx4 v[26:27], v[2:5], off offset:-4096
	global_load_dwordx4 v[2:5], v[24:25], off offset:1024
	v_pk_mul_f32 v[74:75], v[78:79], v[90:91] op_sel_hi:[1,0]
	v_pk_mul_f32 v[76:77], v[80:81], v[90:91] op_sel_hi:[1,0]
	s_waitcnt vmcnt(0)
	v_pk_mul_f32 v[4:5], v[4:5], v[74:75]
	v_pk_mul_f32 v[2:3], v[2:3], v[76:77]
	global_store_dwordx4 v[26:27], v[2:5], off offset:-3072
	global_load_dwordx4 v[2:5], v[24:25], off offset:2048
	v_pk_mul_f32 v[74:75], v[82:83], v[90:91] op_sel_hi:[1,0]
	v_pk_mul_f32 v[76:77], v[84:85], v[90:91] op_sel_hi:[1,0]
	s_waitcnt vmcnt(0)
	v_pk_mul_f32 v[4:5], v[4:5], v[74:75]
	v_pk_mul_f32 v[2:3], v[2:3], v[76:77]
	global_store_dwordx4 v[26:27], v[2:5], off offset:-2048
	global_load_dwordx4 v[2:5], v[24:25], off offset:3072
	v_pk_mul_f32 v[74:75], v[88:89], v[90:91] op_sel_hi:[1,0]
	v_pk_mul_f32 v[76:77], v[86:87], v[90:91] op_sel_hi:[1,0]
	s_waitcnt vmcnt(0)
	v_pk_mul_f32 v[4:5], v[4:5], v[74:75]
	v_pk_mul_f32 v[2:3], v[2:3], v[76:77]
	global_store_dwordx4 v[26:27], v[2:5], off offset:-1024
.LBB0_1735:
	s_add_i32 s0, s2, 1
	s_ashr_i32 s1, s0, 31
	s_lshr_b32 s1, s1, 20
	s_add_i32 s1, s0, s1
	s_ashr_i32 s1, s1, 12
	v_lshlrev_b32_e32 v78, 16, v66
	v_and_b32_e32 v79, 0xffff0000, v66
	v_lshlrev_b32_e32 v80, 16, v67
	v_and_b32_e32 v81, 0xffff0000, v67
	v_lshlrev_b32_e32 v74, 16, v68
	v_and_b32_e32 v75, 0xffff0000, v68
	v_lshlrev_b32_e32 v76, 16, v69
	v_and_b32_e32 v77, 0xffff0000, v69
	v_lshlrev_b32_e32 v66, 16, v72
	v_and_b32_e32 v67, 0xffff0000, v72
	v_lshlrev_b32_e32 v68, 16, v73
	v_and_b32_e32 v69, 0xffff0000, v73
	s_cmpk_lt_i32 s0, 0x4000
	v_lshlrev_b32_e32 v2, 16, v58
	v_and_b32_e32 v3, 0xffff0000, v58
	v_lshlrev_b32_e32 v72, 16, v60
	v_and_b32_e32 v73, 0xffff0000, v60
	s_cselect_b32 s0, s1, 4
	v_pk_add_f32 v[2:3], v[2:3], v[72:73]
	v_lshlrev_b32_e32 v72, 16, v62
	v_and_b32_e32 v73, 0xffff0000, v62
	v_lshlrev_b32_e32 v82, 16, v64
	v_and_b32_e32 v83, 0xffff0000, v64
	s_mul_i32 s10, s0, 0x6000
	v_pk_add_f32 v[72:73], v[72:73], v[82:83]
	s_mul_hi_i32 s3, s0, 0x6000
	s_add_u32 s8, s18, s10
	v_pk_add_f32 v[72:73], v[2:3], v[72:73]
	v_lshlrev_b32_e32 v2, 16, v59
	v_and_b32_e32 v3, 0xffff0000, v59
	v_lshlrev_b32_e32 v58, 16, v61
	v_and_b32_e32 v59, 0xffff0000, v61
	s_addc_u32 s9, s19, s3
	v_pk_add_f32 v[2:3], v[2:3], v[58:59]
	v_lshlrev_b32_e32 v58, 16, v63
	v_and_b32_e32 v59, 0xffff0000, v63
	v_lshlrev_b32_e32 v60, 16, v65
	v_and_b32_e32 v61, 0xffff0000, v65
	v_pk_add_f32 v[58:59], v[58:59], v[60:61]
	v_lshl_add_u64 v[60:61], s[8:9], 0, v[34:35]
	s_mov_b64 s[0:1], 0x5000
	v_pk_add_f32 v[58:59], v[2:3], v[58:59]
	v_lshl_add_u64 v[2:3], v[60:61], 0, s[0:1]
	v_add_co_u32_e32 v60, vcc, s28, v60
	v_lshlrev_b32_e32 v64, 16, v52
	s_nop 0
	v_addc_co_u32_e32 v61, vcc, 0, v61, vcc
	global_load_dwordx4 v[60:63], v[60:61], off
	v_and_b32_e32 v65, 0xffff0000, v52
	v_lshlrev_b32_e32 v52, 16, v53
	v_and_b32_e32 v53, 0xffff0000, v53
	v_lshlrev_b32_e32 v4, 16, v70
	v_and_b32_e32 v5, 0xffff0000, v70
	v_lshlrev_b32_e32 v70, 16, v71
	v_and_b32_e32 v71, 0xffff0000, v71
	v_readlane_b32 s8, v255, 48
	v_readlane_b32 s9, v255, 49
	s_mov_b64 s[0:1], -1
	s_and_b64 vcc, exec, s[8:9]
	s_waitcnt vmcnt(0)
	v_pk_fma_f32 v[58:59], v[58:59], v[62:63], v[80:81]
	v_lshlrev_b32_e32 v62, 16, v50
	v_and_b32_e32 v63, 0xffff0000, v50
	v_lshlrev_b32_e32 v50, 16, v51
	v_and_b32_e32 v51, 0xffff0000, v51
	v_pk_add_f32 v[62:63], v[62:63], v[64:65]
	v_lshlrev_b32_e32 v64, 16, v54
	v_and_b32_e32 v65, 0xffff0000, v54
	v_pk_add_f32 v[50:51], v[50:51], v[52:53]
	v_lshlrev_b32_e32 v52, 16, v55
	v_and_b32_e32 v53, 0xffff0000, v55
	v_lshlrev_b32_e32 v54, 16, v57
	v_and_b32_e32 v55, 0xffff0000, v57
	v_pk_add_f32 v[52:53], v[52:53], v[54:55]
	v_pk_fma_f32 v[60:61], v[72:73], v[60:61], v[78:79]
	v_pk_add_f32 v[50:51], v[50:51], v[52:53]
	global_load_dwordx4 v[52:55], v[2:3], off offset:1024
	v_lshlrev_b32_e32 v72, 16, v56
	v_and_b32_e32 v73, 0xffff0000, v56
	v_pk_add_f32 v[64:65], v[64:65], v[72:73]
	v_lshlrev_b32_e32 v56, 16, v46
	v_pk_add_f32 v[62:63], v[62:63], v[64:65]
	v_and_b32_e32 v57, 0xffff0000, v46
	v_lshlrev_b32_e32 v46, 16, v47
	v_and_b32_e32 v47, 0xffff0000, v47
	s_waitcnt vmcnt(0)
	v_pk_fma_f32 v[50:51], v[50:51], v[54:55], v[76:77]
	v_lshlrev_b32_e32 v54, 16, v48
	v_and_b32_e32 v55, 0xffff0000, v48
	v_pk_fma_f32 v[52:53], v[62:63], v[52:53], v[74:75]
	v_pk_add_f32 v[54:55], v[54:55], v[56:57]
	v_lshlrev_b32_e32 v56, 16, v44
	v_and_b32_e32 v57, 0xffff0000, v44
	v_lshlrev_b32_e32 v62, 16, v42
	v_and_b32_e32 v63, 0xffff0000, v42
	v_lshlrev_b32_e32 v48, 16, v49
	v_and_b32_e32 v49, 0xffff0000, v49
	v_lshlrev_b32_e32 v44, 16, v45
	v_and_b32_e32 v45, 0xffff0000, v45
	v_lshlrev_b32_e32 v42, 16, v43
	v_and_b32_e32 v43, 0xffff0000, v43
	v_pk_add_f32 v[46:47], v[48:49], v[46:47]
	v_pk_add_f32 v[42:43], v[44:45], v[42:43]
	v_pk_add_f32 v[56:57], v[56:57], v[62:63]
	v_pk_add_f32 v[42:43], v[46:47], v[42:43]
	global_load_dwordx4 v[44:47], v[2:3], off offset:2048
	v_pk_add_f32 v[54:55], v[54:55], v[56:57]
	v_lshlrev_b32_e32 v48, 16, v32
	v_and_b32_e32 v49, 0xffff0000, v32
	v_lshlrev_b32_e32 v32, 16, v33
	v_and_b32_e32 v33, 0xffff0000, v33
	s_waitcnt vmcnt(0)
	v_pk_fma_f32 v[42:43], v[42:43], v[46:47], v[70:71]
	v_pk_fma_f32 v[44:45], v[54:55], v[44:45], v[4:5]
	v_lshlrev_b32_e32 v4, 16, v40
	v_and_b32_e32 v5, 0xffff0000, v40
	v_lshlrev_b32_e32 v46, 16, v38
	v_and_b32_e32 v47, 0xffff0000, v38
	v_pk_add_f32 v[4:5], v[4:5], v[46:47]
	v_lshlrev_b32_e32 v46, 16, v36
	v_and_b32_e32 v47, 0xffff0000, v36
	v_pk_add_f32 v[46:47], v[46:47], v[48:49]
	v_lshlrev_b32_e32 v38, 16, v39
	v_pk_add_f32 v[46:47], v[4:5], v[46:47]
	v_lshlrev_b32_e32 v4, 16, v41
	v_and_b32_e32 v5, 0xffff0000, v41
	v_and_b32_e32 v39, 0xffff0000, v39
	v_lshlrev_b32_e32 v36, 16, v37
	v_and_b32_e32 v37, 0xffff0000, v37
	v_pk_add_f32 v[4:5], v[4:5], v[38:39]
	v_pk_add_f32 v[32:33], v[36:37], v[32:33]
	v_pk_mul_f32 v[48:49], v[60:61], v[60:61]
	v_pk_add_f32 v[32:33], v[4:5], v[32:33]
	global_load_dwordx4 v[2:5], v[2:3], off offset:3072
	s_waitcnt vmcnt(0)
	v_pk_fma_f32 v[32:33], v[32:33], v[4:5], v[68:69]
	v_pk_fma_f32 v[36:37], v[46:47], v[2:3], v[66:67]
	v_mul_f32_e32 v4, v32, v32
	v_mul_f32_e32 v40, v36, v36
	v_mul_f32_e32 v38, v37, v37
	v_mul_f32_e32 v2, v33, v33
	v_pk_mul_f32 v[46:47], v[52:53], v[52:53]
	s_cbranch_vccz .LBB0_1737
	s_mov_b64 s[0:1], 0x178800
	v_lshl_add_u64 v[54:55], v[30:31], 0, s[0:1]
	s_mov_b64 s[0:1], 0x178a00
	v_cvt_pk_bf16_f32 v66, v60, v61
	v_cvt_pk_bf16_f32 v67, v58, v59
	v_lshl_add_u64 v[56:57], v[30:31], 0, s[0:1]
	s_mov_b64 s[0:1], 0x178c00
	global_store_dwordx2 v[54:55], v[66:67], off
	v_cvt_pk_bf16_f32 v54, v52, v53
	v_cvt_pk_bf16_f32 v55, v50, v51
	v_lshl_add_u64 v[62:63], v[30:31], 0, s[0:1]
	s_mov_b64 s[0:1], 0x178e00
	global_store_dwordx2 v[56:57], v[54:55], off
	v_cvt_pk_bf16_f32 v54, v44, v45
	v_cvt_pk_bf16_f32 v55, v42, v43
	v_lshl_add_u64 v[64:65], v[30:31], 0, s[0:1]
	global_store_dwordx2 v[62:63], v[54:55], off
	v_cvt_pk_bf16_f32 v54, v36, v37
	v_cvt_pk_bf16_f32 v55, v32, v33
	global_store_dwordx2 v[64:65], v[54:55], off
	v_pk_mul_f32 v[54:55], v[58:59], v[58:59]
	v_mov_b32_e32 v56, v48
	v_mov_b32_e32 v57, v55
	v_pk_mov_b32 v[54:55], v[48:49], v[54:55] op_sel:[1,0]
	s_add_u32 s8, s22, s10
	v_pk_add_f32 v[54:55], v[54:55], v[56:57]
	v_mov_b32_e32 v56, v46
	v_pk_add_f32 v[70:71], v[54:55], v[54:55] op_sel_hi:[0,1]
	v_pk_mul_f32 v[54:55], v[50:51], v[50:51]
	s_addc_u32 s9, s23, s3
	v_mov_b32_e32 v57, v55
	v_pk_mov_b32 v[54:55], v[46:47], v[54:55] op_sel:[1,0]
	s_add_u32 s10, s8, 0x1000
	v_pk_add_f32 v[54:55], v[54:55], v[56:57]
	s_addc_u32 s11, s9, 0
	v_pk_add_f32 v[72:73], v[54:55], v[54:55] op_sel_hi:[0,1]
	v_mul_f32_e32 v54, v44, v44
	v_pk_fma_f32 v[74:75], v[44:45], v[44:45], v[54:55] op_sel_hi:[1,1,0]
	v_mul_f32_e32 v54, v42, v42
	v_pk_fma_f32 v[76:77], v[42:43], v[42:43], v[54:55] op_sel_hi:[1,1,0]
	global_load_dwordx4 v[54:57], v[16:17], off
	global_load_dwordx4 v[62:65], v34, s[8:9]
	global_load_dwordx4 v[66:69], v34, s[10:11]
	v_mov_b32_e32 v5, v71
	v_mov_b32_e32 v3, v73
	v_mov_b32_e32 v41, v75
	v_mov_b32_e32 v39, v77
	v_pk_add_f32 v[70:71], v[4:5], v[2:3]
	v_and_b32_e32 v5, 64, v203
	v_pk_add_f32 v[74:75], v[40:41], v[38:39]
	v_add_u32_e32 v5, 64, v5
	v_xor_b32_e32 v39, 1, v203
	v_cmp_lt_i32_e32 vcc, v39, v5
	v_pk_add_f32 v[70:71], v[74:75], v[70:71]
	s_mov_b32 s0, 0x4578000
	v_cndmask_b32_e32 v39, v203, v39, vcc
	v_add_f32_e32 v3, v70, v71
	v_lshlrev_b32_e32 v39, 2, v39
	s_nop 1
	v_mov_b32_dpp v39, v3 quad_perm:[1,0,3,2] row_mask:0xf bank_mask:0xf
	s_waitcnt lgkmcnt(0)
	v_add_f32_e32 v3, v3, v39
	v_xor_b32_e32 v39, 2, v203
	v_cmp_lt_i32_e32 vcc, v39, v5
	s_waitcnt vmcnt(0)
	v_pk_add_f32 v[68:69], v[68:69], 1.0 op_sel_hi:[1,0]
	v_cndmask_b32_e32 v39, v203, v39, vcc
	v_lshlrev_b32_e32 v39, 2, v39
	s_nop 1
	v_mov_b32_dpp v39, v3 quad_perm:[2,3,0,1] row_mask:0xf bank_mask:0xf
	v_pk_add_f32 v[66:67], v[66:67], 1.0 op_sel_hi:[1,0]
	s_waitcnt lgkmcnt(0)
	v_add_f32_e32 v3, v3, v39
	v_xor_b32_e32 v39, 4, v203
	v_cmp_lt_i32_e32 vcc, v39, v5
	s_nop 1
	v_cndmask_b32_e32 v39, v203, v39, vcc
	v_lshlrev_b32_e32 v39, 2, v39
	s_nop 1
	v_mov_b32_dpp v39, v3 row_half_mirror row_mask:0xf bank_mask:0xf
	s_waitcnt lgkmcnt(0)
	v_add_f32_e32 v3, v3, v39
	v_xor_b32_e32 v39, 8, v203
	v_cmp_lt_i32_e32 vcc, v39, v5
	s_nop 1
	v_cndmask_b32_e32 v39, v203, v39, vcc
	v_lshlrev_b32_e32 v39, 2, v39
	s_nop 1
	v_mov_b32_dpp v39, v3 row_mirror row_mask:0xf bank_mask:0xf
	s_waitcnt lgkmcnt(0)
	v_add_f32_e32 v3, v3, v39
	v_xor_b32_e32 v39, 16, v203
	v_cmp_lt_i32_e32 vcc, v39, v5
	s_nop 1
	v_cndmask_b32_e32 v39, v203, v39, vcc
	v_lshlrev_b32_e32 v39, 2, v39
	v_mov_b32_e32 v39, v3
	s_nop 1
	v_permlane16_swap_b32_e32 v39, v3
	s_waitcnt lgkmcnt(0)
	v_add_f32_e32 v3, v3, v39
	v_xor_b32_e32 v39, 32, v203
	v_cmp_lt_i32_e32 vcc, v39, v5
	s_nop 1
	v_cndmask_b32_e32 v5, v203, v39, vcc
	v_lshlrev_b32_e32 v5, 2, v5
	v_mov_b32_e32 v5, v3
	s_nop 1
	v_permlane32_swap_b32_e32 v5, v3
	v_add_co_u32_e32 v30, vcc, s0, v30
	s_mov_b64 s[0:1], 0
	s_nop 0
	v_addc_co_u32_e32 v31, vcc, 0, v31, vcc
	s_waitcnt lgkmcnt(0)
	v_add_f32_e32 v3, v3, v5
	v_fmamk_f32 v3, v3, 0x3a800000, v165
	v_rsq_f32_e32 v70, v3
	s_nop 0
	v_pk_mul_f32 v[72:73], v[58:59], v[70:71] op_sel_hi:[1,0]
	v_pk_mul_f32 v[74:75], v[60:61], v[70:71] op_sel_hi:[1,0]
	v_pk_mul_f32 v[56:57], v[56:57], v[72:73]
	v_pk_mul_f32 v[54:55], v[54:55], v[74:75]
	v_pk_fma_f32 v[56:57], v[68:69], v[56:57], v[64:65]
	v_pk_fma_f32 v[54:55], v[66:67], v[54:55], v[62:63]
	v_pk_mul_f32 v[72:73], v[50:51], v[70:71] op_sel_hi:[1,0]
	v_cvt_pk_bf16_f32 v54, v54, v55
	v_cvt_pk_bf16_f32 v55, v56, v57
	global_store_dwordx2 v[30:31], v[54:55], off offset:2048
	global_load_dwordx4 v[54:57], v[18:19], off
	s_nop 0
	global_load_dwordx4 v[62:65], v15, s[10:11]
	global_load_dwordx4 v[66:69], v34, s[8:9] offset:1024
	v_pk_mul_f32 v[74:75], v[52:53], v[70:71] op_sel_hi:[1,0]
	s_waitcnt vmcnt(2)
	v_pk_mul_f32 v[56:57], v[56:57], v[72:73]
	v_pk_mul_f32 v[54:55], v[54:55], v[74:75]
	s_waitcnt vmcnt(1)
	v_pk_add_f32 v[64:65], v[64:65], 1.0 op_sel_hi:[1,0]
	v_pk_add_f32 v[62:63], v[62:63], 1.0 op_sel_hi:[1,0]
	s_waitcnt vmcnt(0)
	v_pk_fma_f32 v[56:57], v[64:65], v[56:57], v[68:69]
	v_pk_fma_f32 v[54:55], v[62:63], v[54:55], v[66:67]
	v_pk_mul_f32 v[72:73], v[42:43], v[70:71] op_sel_hi:[1,0]
	v_cvt_pk_bf16_f32 v54, v54, v55
	v_cvt_pk_bf16_f32 v55, v56, v57
	global_store_dwordx2 v[30:31], v[54:55], off offset:2560
	global_load_dwordx4 v[54:57], v[20:21], off
	s_nop 0
	global_load_dwordx4 v[62:65], v13, s[10:11]
	global_load_dwordx4 v[66:69], v34, s[8:9] offset:2048
	v_pk_mul_f32 v[74:75], v[44:45], v[70:71] op_sel_hi:[1,0]
	s_waitcnt vmcnt(2)
	v_pk_mul_f32 v[56:57], v[72:73], v[56:57]
	v_pk_mul_f32 v[54:55], v[74:75], v[54:55]
	s_waitcnt vmcnt(1)
	v_pk_add_f32 v[64:65], v[64:65], 1.0 op_sel_hi:[1,0]
	v_pk_add_f32 v[62:63], v[62:63], 1.0 op_sel_hi:[1,0]
	s_waitcnt vmcnt(0)
	v_pk_fma_f32 v[56:57], v[56:57], v[64:65], v[68:69]
	v_pk_fma_f32 v[54:55], v[54:55], v[62:63], v[66:67]
	v_pk_mul_f32 v[72:73], v[32:33], v[70:71] op_sel_hi:[1,0]
	v_cvt_pk_bf16_f32 v54, v54, v55
	v_cvt_pk_bf16_f32 v55, v56, v57
	global_store_dwordx2 v[30:31], v[54:55], off offset:3072
	global_load_dwordx4 v[54:57], v[22:23], off
	s_nop 0
	global_load_dwordx4 v[62:65], v11, s[10:11]
	global_load_dwordx4 v[66:69], v34, s[8:9] offset:3072
	v_pk_mul_f32 v[70:71], v[36:37], v[70:71] op_sel_hi:[1,0]
	s_waitcnt vmcnt(2)
	v_pk_mul_f32 v[56:57], v[72:73], v[56:57]
	v_pk_mul_f32 v[54:55], v[70:71], v[54:55]
	s_waitcnt vmcnt(1)
	v_pk_add_f32 v[64:65], v[64:65], 1.0 op_sel_hi:[1,0]
	v_pk_add_f32 v[62:63], v[62:63], 1.0 op_sel_hi:[1,0]
	s_waitcnt vmcnt(0)
	v_pk_fma_f32 v[56:57], v[56:57], v[64:65], v[68:69]
	v_pk_fma_f32 v[54:55], v[54:55], v[62:63], v[66:67]
	s_nop 0
	v_cvt_pk_bf16_f32 v54, v54, v55
	v_cvt_pk_bf16_f32 v55, v56, v57
	global_store_dwordx2 v[30:31], v[54:55], off offset:3584
.LBB0_1737:
	s_andn2_b64 vcc, exec, s[0:1]
	s_cbranch_vccnz .LBB0_1730
	v_pk_mul_f32 v[30:31], v[58:59], v[58:59]
	v_mov_b32_e32 v54, v48
	v_mov_b32_e32 v55, v31
	v_pk_mov_b32 v[30:31], v[48:49], v[30:31] op_sel:[1,0]
	v_pk_mul_f32 v[48:49], v[50:51], v[50:51]
	v_pk_add_f32 v[30:31], v[30:31], v[54:55]
	v_mov_b32_e32 v54, v46
	v_mov_b32_e32 v55, v49
	v_pk_mov_b32 v[46:47], v[46:47], v[48:49] op_sel:[1,0]
	v_pk_add_f32 v[30:31], v[30:31], v[30:31] op_sel:[0,1] op_sel_hi:[1,0]
	v_pk_add_f32 v[46:47], v[46:47], v[54:55]
	v_mov_b32_e32 v31, v40
	v_pk_add_f32 v[40:41], v[46:47], v[46:47] op_sel:[0,1] op_sel_hi:[1,0]
	v_mul_f32_e32 v34, v45, v45
	v_mov_b32_e32 v41, v38
	v_pk_fma_f32 v[38:39], v[44:45], v[44:45], v[34:35] op_sel_hi:[1,1,0]
	v_pk_add_f32 v[30:31], v[30:31], v[40:41]
	v_mov_b32_e32 v39, v4
	v_mul_f32_e32 v4, v43, v43
	v_pk_fma_f32 v[4:5], v[42:43], v[42:43], v[4:5] op_sel_hi:[1,1,0]
	s_nop 0
	v_mov_b32_e32 v5, v2
	v_pk_add_f32 v[2:3], v[38:39], v[4:5]
	v_xor_b32_e32 v4, 1, v203
	v_pk_add_f32 v[2:3], v[30:31], v[2:3]
	s_nop 0
	v_add_f32_e32 v2, v2, v3
	v_and_b32_e32 v3, 64, v203
	v_add_u32_e32 v3, 64, v3
	v_cmp_lt_i32_e32 vcc, v4, v3
	s_nop 1
	v_cndmask_b32_e32 v4, v203, v4, vcc
	v_lshlrev_b32_e32 v4, 2, v4
	s_nop 1
	v_mov_b32_dpp v4, v2 quad_perm:[1,0,3,2] row_mask:0xf bank_mask:0xf
	s_waitcnt lgkmcnt(0)
	v_add_f32_e32 v2, v2, v4
	v_xor_b32_e32 v4, 2, v203
	v_cmp_lt_i32_e32 vcc, v4, v3
	s_nop 1
	v_cndmask_b32_e32 v4, v203, v4, vcc
	v_lshlrev_b32_e32 v4, 2, v4
	s_nop 1
	v_mov_b32_dpp v4, v2 quad_perm:[2,3,0,1] row_mask:0xf bank_mask:0xf
	s_waitcnt lgkmcnt(0)
	v_add_f32_e32 v2, v2, v4
	v_xor_b32_e32 v4, 4, v203
	v_cmp_lt_i32_e32 vcc, v4, v3
	s_nop 1
	v_cndmask_b32_e32 v4, v203, v4, vcc
	v_lshlrev_b32_e32 v4, 2, v4
	s_nop 1
	v_mov_b32_dpp v4, v2 row_half_mirror row_mask:0xf bank_mask:0xf
	s_waitcnt lgkmcnt(0)
	v_add_f32_e32 v2, v2, v4
	v_xor_b32_e32 v4, 8, v203
	v_cmp_lt_i32_e32 vcc, v4, v3
	s_nop 1
	v_cndmask_b32_e32 v4, v203, v4, vcc
	v_lshlrev_b32_e32 v4, 2, v4
	s_nop 1
	v_mov_b32_dpp v4, v2 row_mirror row_mask:0xf bank_mask:0xf
	s_waitcnt lgkmcnt(0)
	v_add_f32_e32 v2, v2, v4
	v_xor_b32_e32 v4, 16, v203
	v_cmp_lt_i32_e32 vcc, v4, v3
	s_nop 1
	v_cndmask_b32_e32 v4, v203, v4, vcc
	v_lshlrev_b32_e32 v4, 2, v4
	v_mov_b32_e32 v4, v2
	s_nop 1
	v_permlane16_swap_b32_e32 v4, v2
	s_waitcnt lgkmcnt(0)
	v_add_f32_e32 v2, v2, v4
	v_xor_b32_e32 v4, 32, v203
	v_cmp_lt_i32_e32 vcc, v4, v3
	s_nop 1
	v_cndmask_b32_e32 v3, v203, v4, vcc
	v_lshlrev_b32_e32 v3, 2, v3
	v_mov_b32_e32 v3, v2
	s_nop 1
	v_permlane32_swap_b32_e32 v3, v2
	s_waitcnt lgkmcnt(0)
	v_add_f32_e32 v2, v2, v3
	v_fmamk_f32 v2, v2, 0x3a800000, v165
	v_rsq_f32_e32 v30, v2
	global_load_dwordx4 v[2:5], v[24:25], off
	v_pk_mul_f32 v[38:39], v[60:61], v[30:31] op_sel_hi:[1,0]
	v_pk_mul_f32 v[40:41], v[58:59], v[30:31] op_sel_hi:[1,0]
	v_pk_mul_f32 v[32:33], v[32:33], v[30:31] op_sel_hi:[1,0]
	s_waitcnt vmcnt(0)
	v_pk_mul_f32 v[4:5], v[4:5], v[40:41]
	v_pk_mul_f32 v[2:3], v[2:3], v[38:39]
	global_store_dwordx4 v[26:27], v[2:5], off
	global_load_dwordx4 v[2:5], v[24:25], off offset:1024
	v_pk_mul_f32 v[38:39], v[50:51], v[30:31] op_sel_hi:[1,0]
	v_pk_mul_f32 v[40:41], v[52:53], v[30:31] op_sel_hi:[1,0]
	s_waitcnt vmcnt(0)
	v_pk_mul_f32 v[4:5], v[4:5], v[38:39]
	v_pk_mul_f32 v[2:3], v[2:3], v[40:41]
	global_store_dwordx4 v[26:27], v[2:5], off offset:1024
	global_load_dwordx4 v[2:5], v[24:25], off offset:2048
	v_pk_mul_f32 v[38:39], v[42:43], v[30:31] op_sel_hi:[1,0]
	v_pk_mul_f32 v[40:41], v[44:45], v[30:31] op_sel_hi:[1,0]
	v_pk_mul_f32 v[30:31], v[36:37], v[30:31] op_sel_hi:[1,0]
	s_waitcnt vmcnt(0)
	v_pk_mul_f32 v[2:3], v[2:3], v[40:41]
	v_pk_mul_f32 v[4:5], v[4:5], v[38:39]
	global_store_dwordx4 v[26:27], v[2:5], off offset:2048
	global_load_dwordx4 v[2:5], v[24:25], off offset:3072
	s_waitcnt vmcnt(0)
	v_pk_mul_f32 v[2:3], v[2:3], v[30:31]
	v_pk_mul_f32 v[4:5], v[4:5], v[32:33]
	global_store_dwordx4 v[26:27], v[2:5], off offset:3072
	s_branch .LBB0_1730
